# v56 + fp8 MFMAs in non-scaled form (unit block scales, same e4m3 operands and f32 accumulate; drops the ld_scale half of every MFMA)
# baseline (speedup 1.0000x reference)
; #define PG8_STAGE(bufoff, gbase, voff) do { _Pragma("unroll") for (int _i = 0; _i < 2; ++_i) \
;         __builtin_amdgcn_global_load_lds((const unsigned*)((const char*)(gbase) + (voff)[_i]), (PG8_LAS unsigned*)(lds + (bufoff) + ldsw + _i * 8192), 16, 0, 0); } while (0)
; #define PG8_WAIT_V(n) asm volatile("s_waitcnt vmcnt(" #n ")" ::: "memory")
; #define PG8_WAIT_L(n) asm volatile("s_waitcnt lgkmcnt(" #n ")" ::: "memory")
; template <class Epi, class Sched, bool ALIGN_EPI = true, bool F8 = false>
; __device__ __forceinline__ void gemm_phase(PG8_LAS unsigned char* lds, const Sched& S, const Epi& E) {
;     ...
;         for (int t = 0; t < nt; t += 2) {
;             const bool last = (t == nt - 2);
;             if constexpr (Sched::GATHER) { if (last && has_next) S.a_off(nxt, Rs, Cs, voffAn); }
;             const char* a1 = cA + (size_t)(t + 1) * kstep;
;             const char* a2 = last ? nA : cA + (size_t)(t + 2) * kstep; const char* b2 = last ? nB : cB + (size_t)(t + 2) * kstepB;
;             const char* a3 = a2 + kstep; const char* b3 = b2 + kstepB;
;             unsigned vA2[2][2];
; #pragma unroll
;             for (int h = 0; h < 2; ++h)
; #pragma unroll
;                 for (int i = 0; i < 2; ++i) { if constexpr (Sched::GATHER) vA2[h][i] = (last && has_next) ? voffAn[h][i] : voffA[h][i]; else vA2[h][i] = voffA[h][i]; }
;             PG8_LDB(B0, 0, 0); PG8_LDB(B1, 0, 1); PG8_SCHED; PG8_LDA(At, 0, 0); PG8_STAGE(PG8_SA(1, 1), a1, voffA[1]);
;             PG8_WAIT_V(8); PG8_WAIT_L(0); PG8_BAR; PG8_MMA(0, 0, At, B0); PG8_MMA(0, 1, At, B1); PG8_BAR; PG8_SCHED;
;             PG8_LDA(At, 0, 1); PG8_STAGE(PG8_SB(0, 0), b2, voffB[0]); PG8_STAGE(PG8_SB(0, 1), b2, voffB[1]); PG8_STAGE(PG8_SA(0, 0), a2, vA2[0]);
;             PG8_WAIT_V(8); PG8_WAIT_L(0); PG8_BAR; PG8_MMA(1, 0, At, B0); PG8_MMA(1, 1, At, B1); PG8_BAR; PG8_SCHED;
;             PG8_LDB(B0, 1, 0); PG8_LDB(B1, 1, 1); PG8_SCHED; PG8_LDA(At, 1, 0); PG8_STAGE(PG8_SA(0, 1), a2, vA2[1]);
;             PG8_WAIT_V(8); PG8_WAIT_L(0); PG8_BAR; PG8_MMA(0, 0, At, B0); PG8_MMA(0, 1, At, B1); PG8_BAR; PG8_SCHED;
;             PG8_LDA(At, 1, 1); PG8_STAGE(PG8_SB(1, 0), b3, voffB[0]); PG8_STAGE(PG8_SB(1, 1), b3, voffB[1]); PG8_STAGE(PG8_SA(1, 0), a3, vA2[0]);
;             PG8_WAIT_V(8); PG8_WAIT_L(0); PG8_BAR; PG8_MMA(1, 0, At, B0); PG8_MMA(1, 1, At, B1); PG8_BAR; PG8_SCHED;
.LBB0_372:
	ds_read_b128 v[18:21], v207
	ds_read_b128 v[22:25], v207 offset:1024
	ds_read_b128 v[26:29], v207 offset:2048
	ds_read_b128 v[30:33], v207 offset:3072
	ds_read_b128 v[2:5], v208
	ds_read_b128 v[6:9], v208 offset:1024
	ds_read_b128 v[10:13], v208 offset:2048
	ds_read_b128 v[14:17], v208 offset:3072
	s_add_u32 s28, s26, 0x8000
	s_addc_u32 s29, s27, 0
	s_cmp_eq_u32 s21, 12
	s_cselect_b32 s40, s22, s28
	s_cselect_b32 s41, s23, s29
	s_cselect_b32 s30, s24, s5
	s_cselect_b32 s31, s25, s19
	s_add_u32 s28, s40, 0x8000
	s_addc_u32 s29, s41, 0
	v_lshl_add_u64 v[244:245], s[26:27], 0, v[190:191]
	s_add_i32 m0, s46, 0xc000
	ds_read_b128 v[212:215], v209
	ds_read_b128 v[216:219], v209 offset:1024
	ds_read_b128 v[220:223], v209 offset:2048
	ds_read_b128 v[224:227], v209 offset:3072
	ds_read_b128 v[228:231], v209 offset:4096
	ds_read_b128 v[232:235], v209 offset:5120
	ds_read_b128 v[236:239], v209 offset:6144
	ds_read_b128 v[240:243], v209 offset:7168
	global_load_lds_dwordx4 v[244:245], off
	v_lshl_add_u64 v[244:245], s[26:27], 0, v[188:189]
	s_add_i32 m0, s46, 0xe000
	s_nop 0
	global_load_lds_dwordx4 v[244:245], off
	s_waitcnt vmcnt(8)
	s_waitcnt lgkmcnt(0)
	s_setprio 1
	v_mfma_f32_16x16x128_f8f6f4 v[158:161], v[18:25], v[212:219], v[158:161]
	v_mfma_f32_16x16x128_f8f6f4 v[154:157], v[26:33], v[212:219], v[154:157]
	v_mfma_f32_16x16x128_f8f6f4 v[142:145], v[18:25], v[220:227], v[142:145]
	v_mfma_f32_16x16x128_f8f6f4 v[138:141], v[26:33], v[220:227], v[138:141]
	v_mfma_f32_16x16x128_f8f6f4 v[126:129], v[18:25], v[228:235], v[126:129]
	v_mfma_f32_16x16x128_f8f6f4 v[122:125], v[26:33], v[228:235], v[122:125]
	v_mfma_f32_16x16x128_f8f6f4 v[110:113], v[18:25], v[236:243], v[110:113]
	v_mfma_f32_16x16x128_f8f6f4 v[106:109], v[26:33], v[236:243], v[106:109]
	s_nop 3
	s_setprio 0
	s_setprio 1
	v_mfma_f32_16x16x128_f8f6f4 v[150:153], v[2:9], v[212:219], v[150:153]
	v_mfma_f32_16x16x128_f8f6f4 v[146:149], v[10:17], v[212:219], v[146:149]
	v_mfma_f32_16x16x128_f8f6f4 v[134:137], v[2:9], v[220:227], v[134:137]
	v_mfma_f32_16x16x128_f8f6f4 v[130:133], v[10:17], v[220:227], v[130:133]
	v_mfma_f32_16x16x128_f8f6f4 v[118:121], v[2:9], v[228:235], v[118:121]
	v_mfma_f32_16x16x128_f8f6f4 v[114:117], v[10:17], v[228:235], v[114:117]
	v_mfma_f32_16x16x128_f8f6f4 v[102:105], v[2:9], v[236:243], v[102:105]
	v_mfma_f32_16x16x128_f8f6f4 v[98:101], v[10:17], v[236:243], v[98:101]
	s_setprio 0
	s_barrier
	s_add_i32 s67, s62, s45
	v_lshl_add_u64 v[244:245], s[30:31], 0, v[164:165]
	s_mov_b32 m0, s67
	ds_read_b128 v[212:215], v209 offset:16384
	ds_read_b128 v[216:219], v209 offset:17408
	ds_read_b128 v[220:223], v209 offset:18432
	ds_read_b128 v[224:227], v209 offset:19456
	ds_read_b128 v[228:231], v209 offset:20480
	ds_read_b128 v[232:235], v209 offset:21504
	ds_read_b128 v[236:239], v209 offset:22528
	ds_read_b128 v[240:243], v209 offset:23552
	global_load_lds_dwordx4 v[244:245], off
	v_lshl_add_u64 v[246:247], s[30:31], 0, v[166:167]
	s_add_i32 m0, s67, 0x2000
	s_add_i32 s67, s63, s45
	global_load_lds_dwordx4 v[246:247], off
	v_lshl_add_u64 v[244:245], v[244:245], 0, s[8:9]
	s_mov_b32 m0, s67
	s_nop 0
	global_load_lds_dwordx4 v[244:245], off
	v_lshl_add_u64 v[244:245], v[246:247], 0, s[8:9]
	s_add_i32 m0, s67, 0x2000
	s_nop 0
	global_load_lds_dwordx4 v[244:245], off
	v_lshl_add_u64 v[244:245], s[40:41], 0, v[174:175]
	s_mov_b32 m0, s46
	s_nop 0
	global_load_lds_dwordx4 v[244:245], off
	v_lshl_add_u64 v[244:245], s[40:41], 0, v[176:177]
	s_mov_b32 m0, s47
	s_nop 0
	global_load_lds_dwordx4 v[244:245], off
	s_waitcnt vmcnt(8)
	s_waitcnt lgkmcnt(0)
	s_setprio 1
	v_mfma_f32_16x16x128_f8f6f4 v[94:97], v[18:25], v[212:219], v[94:97]
	v_mfma_f32_16x16x128_f8f6f4 v[90:93], v[26:33], v[212:219], v[90:93]
	v_mfma_f32_16x16x128_f8f6f4 v[78:81], v[18:25], v[220:227], v[78:81]
	v_mfma_f32_16x16x128_f8f6f4 v[74:77], v[26:33], v[220:227], v[74:77]
	v_mfma_f32_16x16x128_f8f6f4 v[62:65], v[18:25], v[228:235], v[62:65]
	v_mfma_f32_16x16x128_f8f6f4 v[58:61], v[26:33], v[228:235], v[58:61]
	v_mfma_f32_16x16x128_f8f6f4 v[46:49], v[18:25], v[236:243], v[46:49]
	v_mfma_f32_16x16x128_f8f6f4 v[42:45], v[26:33], v[236:243], v[42:45]
	s_nop 3
	s_setprio 0
	s_setprio 1
	v_mfma_f32_16x16x128_f8f6f4 v[86:89], v[2:9], v[212:219], v[86:89]
	v_mfma_f32_16x16x128_f8f6f4 v[82:85], v[10:17], v[212:219], v[82:85]
	v_mfma_f32_16x16x128_f8f6f4 v[70:73], v[2:9], v[220:227], v[70:73]
	v_mfma_f32_16x16x128_f8f6f4 v[66:69], v[10:17], v[220:227], v[66:69]
	v_mfma_f32_16x16x128_f8f6f4 v[54:57], v[2:9], v[228:235], v[54:57]
	v_mfma_f32_16x16x128_f8f6f4 v[50:53], v[10:17], v[228:235], v[50:53]
	v_mfma_f32_16x16x128_f8f6f4 v[38:41], v[2:9], v[236:243], v[38:41]
	v_mfma_f32_16x16x128_f8f6f4 v[34:37], v[10:17], v[236:243], v[34:37]
	s_setprio 0
	s_barrier
; #define PG8_STAGE(bufoff, gbase, voff) do { _Pragma("unroll") for (int _i = 0; _i < 2; ++_i) \
;         __builtin_amdgcn_global_load_lds((const unsigned*)((const char*)(gbase) + (voff)[_i]), (PG8_LAS unsigned*)(lds + (bufoff) + ldsw + _i * 8192), 16, 0, 0); } while (0)
; #define PG8_WAIT_V(n) asm volatile("s_waitcnt vmcnt(" #n ")" ::: "memory")
; #define PG8_WAIT_L(n) asm volatile("s_waitcnt lgkmcnt(" #n ")" ::: "memory")
; #define PG8_BAR __builtin_amdgcn_s_barrier()
; #define PG8_SCHED __builtin_amdgcn_sched_barrier(0)
; template <class Epi, class Sched, bool ALIGN_EPI = true, bool F8 = false>
; __device__ __forceinline__ void gemm_phase(PG8_LAS unsigned char* lds, const Sched& S, const Epi& E) {
;     ...
;             PG8_LDB(B0, 1, 0); PG8_LDB(B1, 1, 1); PG8_SCHED; PG8_LDA(At, 1, 0); PG8_STAGE(PG8_SA(0, 1), a2, vA2[1]);
;             PG8_WAIT_V(8); PG8_WAIT_L(0); PG8_BAR; PG8_MMA(0, 0, At, B0); PG8_MMA(0, 1, At, B1); PG8_BAR; PG8_SCHED;
;             PG8_LDA(At, 1, 1); PG8_STAGE(PG8_SB(1, 0), b3, voffB[0]); PG8_STAGE(PG8_SB(1, 1), b3, voffB[1]); PG8_STAGE(PG8_SA(1, 0), a3, vA2[0]);
;             PG8_WAIT_V(8); PG8_WAIT_L(0); PG8_BAR; PG8_MMA(1, 0, At, B0); PG8_MMA(1, 1, At, B1); PG8_BAR; PG8_SCHED;
	s_add_i32 s67, 0, 0x18000
	s_add_i32 s68, 0, 0x1c000
	v_add_u32_e32 v14, s67, v202
	v_add_u32_e32 v30, s68, v202
	ds_read_b128 v[2:5], v14
	ds_read_b128 v[6:9], v14 offset:1024
	ds_read_b128 v[10:13], v14 offset:2048
	ds_read_b128 v[14:17], v14 offset:3072
	ds_read_b128 v[18:21], v30
	ds_read_b128 v[22:25], v30 offset:1024
	ds_read_b128 v[26:29], v30 offset:2048
	ds_read_b128 v[30:33], v30 offset:3072
	s_mov_b32 m0, s48
	v_lshl_add_u64 v[244:245], s[40:41], 0, v[178:179]
	ds_read_b128 v[212:215], v209 offset:32768
	ds_read_b128 v[216:219], v209 offset:33792
	ds_read_b128 v[220:223], v209 offset:34816
	ds_read_b128 v[224:227], v209 offset:35840
	ds_read_b128 v[228:231], v209 offset:36864
	ds_read_b128 v[232:235], v209 offset:37888
	ds_read_b128 v[236:239], v209 offset:38912
	ds_read_b128 v[240:243], v209 offset:39936
	global_load_lds_dwordx4 v[244:245], off
	v_lshl_add_u64 v[244:245], s[40:41], 0, v[180:181]
	s_mov_b32 m0, s49
	s_nop 0
	global_load_lds_dwordx4 v[244:245], off
	s_waitcnt vmcnt(8)
	s_waitcnt lgkmcnt(0)
	s_setprio 1
	v_mfma_f32_16x16x128_f8f6f4 v[158:161], v[2:9], v[212:219], v[158:161]
	v_mfma_f32_16x16x128_f8f6f4 v[154:157], v[10:17], v[212:219], v[154:157]
	v_mfma_f32_16x16x128_f8f6f4 v[142:145], v[2:9], v[220:227], v[142:145]
	v_mfma_f32_16x16x128_f8f6f4 v[138:141], v[10:17], v[220:227], v[138:141]
	v_mfma_f32_16x16x128_f8f6f4 v[126:129], v[2:9], v[228:235], v[126:129]
	v_mfma_f32_16x16x128_f8f6f4 v[122:125], v[10:17], v[228:235], v[122:125]
	v_mfma_f32_16x16x128_f8f6f4 v[110:113], v[2:9], v[236:243], v[110:113]
	v_mfma_f32_16x16x128_f8f6f4 v[106:109], v[10:17], v[236:243], v[106:109]
	s_nop 3
	s_setprio 0
	s_setprio 1
	v_mfma_f32_16x16x128_f8f6f4 v[150:153], v[18:25], v[212:219], v[150:153]
	v_mfma_f32_16x16x128_f8f6f4 v[146:149], v[26:33], v[212:219], v[146:149]
	v_mfma_f32_16x16x128_f8f6f4 v[134:137], v[18:25], v[220:227], v[134:137]
	v_mfma_f32_16x16x128_f8f6f4 v[130:133], v[26:33], v[220:227], v[130:133]
	v_mfma_f32_16x16x128_f8f6f4 v[118:121], v[18:25], v[228:235], v[118:121]
	v_mfma_f32_16x16x128_f8f6f4 v[114:117], v[26:33], v[228:235], v[114:117]
	v_mfma_f32_16x16x128_f8f6f4 v[102:105], v[18:25], v[236:243], v[102:105]
	v_mfma_f32_16x16x128_f8f6f4 v[98:101], v[26:33], v[236:243], v[98:101]
	s_setprio 0
	s_barrier
	s_add_u32 s30, s30, 0x8000
	s_addc_u32 s31, s31, 0
	s_add_i32 s40, s67, s45
	v_lshl_add_u64 v[244:245], s[30:31], 0, v[164:165]
	s_mov_b32 m0, s40
	ds_read_b128 v[212:215], v209 offset:49152
	ds_read_b128 v[216:219], v209 offset:50176
	ds_read_b128 v[220:223], v209 offset:51200
	ds_read_b128 v[224:227], v209 offset:52224
	ds_read_b128 v[228:231], v209 offset:53248
	ds_read_b128 v[232:235], v209 offset:54272
	ds_read_b128 v[236:239], v209 offset:55296
	ds_read_b128 v[240:243], v209 offset:56320
	global_load_lds_dwordx4 v[244:245], off
	v_lshl_add_u64 v[244:245], s[30:31], 0, v[166:167]
	s_add_i32 m0, s40, 0x2000
	s_add_i32 s40, s68, s45
	global_load_lds_dwordx4 v[244:245], off
	v_lshl_add_u64 v[244:245], s[30:31], 0, v[168:169]
	s_mov_b32 m0, s40
	s_nop 0
	global_load_lds_dwordx4 v[244:245], off
	v_lshl_add_u64 v[244:245], s[30:31], 0, v[172:173]
	s_add_i32 m0, s40, 0x2000
	s_nop 0
	global_load_lds_dwordx4 v[244:245], off
	v_lshl_add_u64 v[244:245], s[28:29], 0, v[174:175]
	s_mov_b32 m0, s52
	s_nop 0
	global_load_lds_dwordx4 v[244:245], off
	v_lshl_add_u64 v[244:245], s[28:29], 0, v[176:177]
	s_mov_b32 m0, s53
	s_nop 0
	global_load_lds_dwordx4 v[244:245], off
	s_waitcnt vmcnt(8)
	s_waitcnt lgkmcnt(0)
	s_setprio 1
	v_mfma_f32_16x16x128_f8f6f4 v[94:97], v[2:9], v[212:219], v[94:97]
	v_mfma_f32_16x16x128_f8f6f4 v[90:93], v[10:17], v[212:219], v[90:93]
	v_mfma_f32_16x16x128_f8f6f4 v[78:81], v[2:9], v[220:227], v[78:81]
	v_mfma_f32_16x16x128_f8f6f4 v[74:77], v[10:17], v[220:227], v[74:77]
	v_mfma_f32_16x16x128_f8f6f4 v[62:65], v[2:9], v[228:235], v[62:65]
	v_mfma_f32_16x16x128_f8f6f4 v[58:61], v[10:17], v[228:235], v[58:61]
	v_mfma_f32_16x16x128_f8f6f4 v[46:49], v[2:9], v[236:243], v[46:49]
	v_mfma_f32_16x16x128_f8f6f4 v[42:45], v[10:17], v[236:243], v[42:45]
	s_nop 3
	s_setprio 0
	s_setprio 1
	v_mfma_f32_16x16x128_f8f6f4 v[86:89], v[18:25], v[212:219], v[86:89]
	v_mfma_f32_16x16x128_f8f6f4 v[82:85], v[26:33], v[212:219], v[82:85]
	v_mfma_f32_16x16x128_f8f6f4 v[70:73], v[18:25], v[220:227], v[70:73]
	v_mfma_f32_16x16x128_f8f6f4 v[66:69], v[26:33], v[220:227], v[66:69]
	v_mfma_f32_16x16x128_f8f6f4 v[54:57], v[18:25], v[228:235], v[54:57]
	v_mfma_f32_16x16x128_f8f6f4 v[50:53], v[26:33], v[228:235], v[50:53]
	v_mfma_f32_16x16x128_f8f6f4 v[38:41], v[18:25], v[236:243], v[38:41]
	v_mfma_f32_16x16x128_f8f6f4 v[34:37], v[26:33], v[236:243], v[34:37]
	s_setprio 0
	s_barrier
	s_add_i32 s21, s21, 2
	s_add_u32 s5, s5, 0x10000
	s_addc_u32 s19, s19, 0
	s_add_u32 s26, s26, 0x10000
	s_addc_u32 s27, s27, 0
	s_cmp_gt_u32 s21, 13
	s_cbranch_scc0 .LBB0_372
	s_branch .Lfx_9967
; #define PG8_STAGE(bufoff, gbase, voff) do { _Pragma("unroll") for (int _i = 0; _i < 2; ++_i) \
;         __builtin_amdgcn_global_load_lds((const unsigned*)((const char*)(gbase) + (voff)[_i]), (PG8_LAS unsigned*)(lds + (bufoff) + ldsw + _i * 8192), 16, 0, 0); } while (0)
; #define PG8_WAIT_V(n) asm volatile("s_waitcnt vmcnt(" #n ")" ::: "memory")
; #define PG8_WAIT_L(n) asm volatile("s_waitcnt lgkmcnt(" #n ")" ::: "memory")
; template <class Epi, class Sched, bool ALIGN_EPI = true, bool F8 = false>
; __device__ __forceinline__ void gemm_phase(PG8_LAS unsigned char* lds, const Sched& S, const Epi& E) {
;     ...
;         for (int t = 0; t < nt; t += 2) {
;             const bool last = (t == nt - 2);
;             if constexpr (Sched::GATHER) { if (last && has_next) S.a_off(nxt, Rs, Cs, voffAn); }
;             const char* a1 = cA + (size_t)(t + 1) * kstep;
;             const char* a2 = last ? nA : cA + (size_t)(t + 2) * kstep; const char* b2 = last ? nB : cB + (size_t)(t + 2) * kstepB;
;             const char* a3 = a2 + kstep; const char* b3 = b2 + kstepB;
;             unsigned vA2[2][2];
; #pragma unroll
;             for (int h = 0; h < 2; ++h)
; #pragma unroll
;                 for (int i = 0; i < 2; ++i) { if constexpr (Sched::GATHER) vA2[h][i] = (last && has_next) ? voffAn[h][i] : voffA[h][i]; else vA2[h][i] = voffA[h][i]; }
;             PG8_LDB(B0, 0, 0); PG8_LDB(B1, 0, 1); PG8_SCHED; PG8_LDA(At, 0, 0); PG8_STAGE(PG8_SA(1, 1), a1, voffA[1]);
;             PG8_WAIT_V(8); PG8_WAIT_L(0); PG8_BAR; PG8_MMA(0, 0, At, B0); PG8_MMA(0, 1, At, B1); PG8_BAR; PG8_SCHED;
;             PG8_LDA(At, 0, 1); PG8_STAGE(PG8_SB(0, 0), b2, voffB[0]); PG8_STAGE(PG8_SB(0, 1), b2, voffB[1]); PG8_STAGE(PG8_SA(0, 0), a2, vA2[0]);
;             PG8_WAIT_V(8); PG8_WAIT_L(0); PG8_BAR; PG8_MMA(1, 0, At, B0); PG8_MMA(1, 1, At, B1); PG8_BAR; PG8_SCHED;
;             PG8_LDB(B0, 1, 0); PG8_LDB(B1, 1, 1); PG8_SCHED; PG8_LDA(At, 1, 0); PG8_STAGE(PG8_SA(0, 1), a2, vA2[1]);
;             PG8_WAIT_V(8); PG8_WAIT_L(0); PG8_BAR; PG8_MMA(0, 0, At, B0); PG8_MMA(0, 1, At, B1); PG8_BAR; PG8_SCHED;
;             PG8_LDA(At, 1, 1); PG8_STAGE(PG8_SB(1, 0), b3, voffB[0]); PG8_STAGE(PG8_SB(1, 1), b3, voffB[1]); PG8_STAGE(PG8_SA(1, 0), a3, vA2[0]);
;             PG8_WAIT_V(8); PG8_WAIT_L(0); PG8_BAR; PG8_MMA(1, 0, At, B0); PG8_MMA(1, 1, At, B1); PG8_BAR; PG8_SCHED;
.Lh1e_9967:
.Lh1_372:
	ds_read_b128 v[18:21], v207
	ds_read_b128 v[22:25], v207 offset:1024
	ds_read_b128 v[26:29], v207 offset:2048
	ds_read_b128 v[30:33], v207 offset:3072
	ds_read_b128 v[2:5], v208
	ds_read_b128 v[6:9], v208 offset:1024
	ds_read_b128 v[10:13], v208 offset:2048
	ds_read_b128 v[14:17], v208 offset:3072
	s_add_u32 s28, s26, 0x8000
	s_addc_u32 s29, s27, 0
	s_cmp_eq_u32 s21, 12
	s_cselect_b32 s40, s22, s28
	s_cselect_b32 s41, s23, s29
	s_cselect_b32 s30, s24, s5
	s_cselect_b32 s31, s25, s19
	s_add_u32 s28, s40, 0x8000
	s_addc_u32 s29, s41, 0
	v_lshl_add_u64 v[244:245], s[26:27], 0, v[190:191]
	s_add_i32 m0, s46, 0xc000
	ds_read_b128 v[212:215], v209
	ds_read_b128 v[216:219], v209 offset:1024
	ds_read_b128 v[220:223], v209 offset:2048
	ds_read_b128 v[224:227], v209 offset:3072
	ds_read_b128 v[228:231], v209 offset:4096
	ds_read_b128 v[232:235], v209 offset:5120
	ds_read_b128 v[236:239], v209 offset:6144
	ds_read_b128 v[240:243], v209 offset:7168
	global_load_lds_dwordx4 v[244:245], off
	v_lshl_add_u64 v[244:245], s[26:27], 0, v[188:189]
	s_add_i32 m0, s46, 0xe000
	s_nop 0
	global_load_lds_dwordx4 v[244:245], off
	s_waitcnt vmcnt(8)
	s_waitcnt lgkmcnt(0)
	s_barrier
	s_setprio 2
	v_mfma_f32_16x16x128_f8f6f4 v[158:161], v[18:25], v[212:219], v[158:161]
	v_mfma_f32_16x16x128_f8f6f4 v[154:157], v[26:33], v[212:219], v[154:157]
	v_mfma_f32_16x16x128_f8f6f4 v[142:145], v[18:25], v[220:227], v[142:145]
	v_mfma_f32_16x16x128_f8f6f4 v[138:141], v[26:33], v[220:227], v[138:141]
	v_mfma_f32_16x16x128_f8f6f4 v[126:129], v[18:25], v[228:235], v[126:129]
	v_mfma_f32_16x16x128_f8f6f4 v[122:125], v[26:33], v[228:235], v[122:125]
	v_mfma_f32_16x16x128_f8f6f4 v[110:113], v[18:25], v[236:243], v[110:113]
	v_mfma_f32_16x16x128_f8f6f4 v[106:109], v[26:33], v[236:243], v[106:109]
	s_nop 3
	s_setprio 0
	s_setprio 2
	v_mfma_f32_16x16x128_f8f6f4 v[150:153], v[2:9], v[212:219], v[150:153]
	v_mfma_f32_16x16x128_f8f6f4 v[146:149], v[10:17], v[212:219], v[146:149]
	v_mfma_f32_16x16x128_f8f6f4 v[134:137], v[2:9], v[220:227], v[134:137]
	v_mfma_f32_16x16x128_f8f6f4 v[130:133], v[10:17], v[220:227], v[130:133]
	v_mfma_f32_16x16x128_f8f6f4 v[118:121], v[2:9], v[228:235], v[118:121]
	v_mfma_f32_16x16x128_f8f6f4 v[114:117], v[10:17], v[228:235], v[114:117]
	v_mfma_f32_16x16x128_f8f6f4 v[102:105], v[2:9], v[236:243], v[102:105]
	v_mfma_f32_16x16x128_f8f6f4 v[98:101], v[10:17], v[236:243], v[98:101]
	s_setprio 0
	s_add_i32 s67, s62, s45
	v_lshl_add_u64 v[244:245], s[30:31], 0, v[164:165]
	s_mov_b32 m0, s67
	ds_read_b128 v[212:215], v209 offset:16384
	ds_read_b128 v[216:219], v209 offset:17408
	ds_read_b128 v[220:223], v209 offset:18432
	ds_read_b128 v[224:227], v209 offset:19456
	ds_read_b128 v[228:231], v209 offset:20480
	ds_read_b128 v[232:235], v209 offset:21504
	ds_read_b128 v[236:239], v209 offset:22528
	ds_read_b128 v[240:243], v209 offset:23552
	global_load_lds_dwordx4 v[244:245], off
	v_lshl_add_u64 v[246:247], s[30:31], 0, v[166:167]
	s_add_i32 m0, s67, 0x2000
	s_add_i32 s67, s63, s45
	global_load_lds_dwordx4 v[246:247], off
	v_lshl_add_u64 v[244:245], v[244:245], 0, s[8:9]
	s_mov_b32 m0, s67
	s_nop 0
	global_load_lds_dwordx4 v[244:245], off
	v_lshl_add_u64 v[244:245], v[246:247], 0, s[8:9]
	s_add_i32 m0, s67, 0x2000
	s_nop 0
	global_load_lds_dwordx4 v[244:245], off
	v_lshl_add_u64 v[244:245], s[40:41], 0, v[174:175]
	s_mov_b32 m0, s46
	s_nop 0
	global_load_lds_dwordx4 v[244:245], off
	v_lshl_add_u64 v[244:245], s[40:41], 0, v[176:177]
	s_mov_b32 m0, s47
	s_nop 0
	global_load_lds_dwordx4 v[244:245], off
	s_waitcnt vmcnt(8)
	s_waitcnt lgkmcnt(0)
	s_barrier
	s_setprio 2
	v_mfma_f32_16x16x128_f8f6f4 v[94:97], v[18:25], v[212:219], v[94:97]
	v_mfma_f32_16x16x128_f8f6f4 v[90:93], v[26:33], v[212:219], v[90:93]
	v_mfma_f32_16x16x128_f8f6f4 v[78:81], v[18:25], v[220:227], v[78:81]
	v_mfma_f32_16x16x128_f8f6f4 v[74:77], v[26:33], v[220:227], v[74:77]
	v_mfma_f32_16x16x128_f8f6f4 v[62:65], v[18:25], v[228:235], v[62:65]
	v_mfma_f32_16x16x128_f8f6f4 v[58:61], v[26:33], v[228:235], v[58:61]
	v_mfma_f32_16x16x128_f8f6f4 v[46:49], v[18:25], v[236:243], v[46:49]
	v_mfma_f32_16x16x128_f8f6f4 v[42:45], v[26:33], v[236:243], v[42:45]
	s_nop 3
	s_setprio 0
	s_setprio 2
	v_mfma_f32_16x16x128_f8f6f4 v[86:89], v[2:9], v[212:219], v[86:89]
	v_mfma_f32_16x16x128_f8f6f4 v[82:85], v[10:17], v[212:219], v[82:85]
	v_mfma_f32_16x16x128_f8f6f4 v[70:73], v[2:9], v[220:227], v[70:73]
	v_mfma_f32_16x16x128_f8f6f4 v[66:69], v[10:17], v[220:227], v[66:69]
	v_mfma_f32_16x16x128_f8f6f4 v[54:57], v[2:9], v[228:235], v[54:57]
	v_mfma_f32_16x16x128_f8f6f4 v[50:53], v[10:17], v[228:235], v[50:53]
	v_mfma_f32_16x16x128_f8f6f4 v[38:41], v[2:9], v[236:243], v[38:41]
	v_mfma_f32_16x16x128_f8f6f4 v[34:37], v[10:17], v[236:243], v[34:37]
	s_setprio 0
	s_add_i32 s67, 0, 0x18000
	s_add_i32 s68, 0, 0x1c000
	v_add_u32_e32 v14, s67, v202
	v_add_u32_e32 v30, s68, v202
	ds_read_b128 v[2:5], v14
	ds_read_b128 v[6:9], v14 offset:1024
	ds_read_b128 v[10:13], v14 offset:2048
	ds_read_b128 v[14:17], v14 offset:3072
	ds_read_b128 v[18:21], v30
	ds_read_b128 v[22:25], v30 offset:1024
	ds_read_b128 v[26:29], v30 offset:2048
	ds_read_b128 v[30:33], v30 offset:3072
	s_mov_b32 m0, s48
	v_lshl_add_u64 v[244:245], s[40:41], 0, v[178:179]
	ds_read_b128 v[212:215], v209 offset:32768
	ds_read_b128 v[216:219], v209 offset:33792
	ds_read_b128 v[220:223], v209 offset:34816
	ds_read_b128 v[224:227], v209 offset:35840
	ds_read_b128 v[228:231], v209 offset:36864
	ds_read_b128 v[232:235], v209 offset:37888
	ds_read_b128 v[236:239], v209 offset:38912
	ds_read_b128 v[240:243], v209 offset:39936
	global_load_lds_dwordx4 v[244:245], off
	v_lshl_add_u64 v[244:245], s[40:41], 0, v[180:181]
	s_mov_b32 m0, s49
	s_nop 0
	global_load_lds_dwordx4 v[244:245], off
	s_waitcnt vmcnt(8)
	s_waitcnt lgkmcnt(0)
	s_barrier
; #define PG8_STAGE(bufoff, gbase, voff) do { _Pragma("unroll") for (int _i = 0; _i < 2; ++_i) \
;         __builtin_amdgcn_global_load_lds((const unsigned*)((const char*)(gbase) + (voff)[_i]), (PG8_LAS unsigned*)(lds + (bufoff) + ldsw + _i * 8192), 16, 0, 0); } while (0)
; #define PG8_WAIT_V(n) asm volatile("s_waitcnt vmcnt(" #n ")" ::: "memory")
; #define PG8_WAIT_L(n) asm volatile("s_waitcnt lgkmcnt(" #n ")" ::: "memory")
; #define PG8_BAR __builtin_amdgcn_s_barrier()
; #define PG8_SCHED __builtin_amdgcn_sched_barrier(0)
; template <class Epi, class Sched, bool ALIGN_EPI = true, bool F8 = false>
; __device__ __forceinline__ void gemm_phase(PG8_LAS unsigned char* lds, const Sched& S, const Epi& E) {
;     ...
;             PG8_LDB(B0, 1, 0); PG8_LDB(B1, 1, 1); PG8_SCHED; PG8_LDA(At, 1, 0); PG8_STAGE(PG8_SA(0, 1), a2, vA2[1]);
;             PG8_WAIT_V(8); PG8_WAIT_L(0); PG8_BAR; PG8_MMA(0, 0, At, B0); PG8_MMA(0, 1, At, B1); PG8_BAR; PG8_SCHED;
;             PG8_LDA(At, 1, 1); PG8_STAGE(PG8_SB(1, 0), b3, voffB[0]); PG8_STAGE(PG8_SB(1, 1), b3, voffB[1]); PG8_STAGE(PG8_SA(1, 0), a3, vA2[0]);
;             PG8_WAIT_V(8); PG8_WAIT_L(0); PG8_BAR; PG8_MMA(1, 0, At, B0); PG8_MMA(1, 1, At, B1); PG8_BAR; PG8_SCHED;
	s_setprio 2
	v_mfma_f32_16x16x128_f8f6f4 v[158:161], v[2:9], v[212:219], v[158:161]
	v_mfma_f32_16x16x128_f8f6f4 v[154:157], v[10:17], v[212:219], v[154:157]
	v_mfma_f32_16x16x128_f8f6f4 v[142:145], v[2:9], v[220:227], v[142:145]
	v_mfma_f32_16x16x128_f8f6f4 v[138:141], v[10:17], v[220:227], v[138:141]
	v_mfma_f32_16x16x128_f8f6f4 v[126:129], v[2:9], v[228:235], v[126:129]
	v_mfma_f32_16x16x128_f8f6f4 v[122:125], v[10:17], v[228:235], v[122:125]
	v_mfma_f32_16x16x128_f8f6f4 v[110:113], v[2:9], v[236:243], v[110:113]
	v_mfma_f32_16x16x128_f8f6f4 v[106:109], v[10:17], v[236:243], v[106:109]
	s_nop 3
	s_setprio 0
	s_setprio 2
	v_mfma_f32_16x16x128_f8f6f4 v[150:153], v[18:25], v[212:219], v[150:153]
	v_mfma_f32_16x16x128_f8f6f4 v[146:149], v[26:33], v[212:219], v[146:149]
	v_mfma_f32_16x16x128_f8f6f4 v[134:137], v[18:25], v[220:227], v[134:137]
	v_mfma_f32_16x16x128_f8f6f4 v[130:133], v[26:33], v[220:227], v[130:133]
	v_mfma_f32_16x16x128_f8f6f4 v[118:121], v[18:25], v[228:235], v[118:121]
	v_mfma_f32_16x16x128_f8f6f4 v[114:117], v[26:33], v[228:235], v[114:117]
	v_mfma_f32_16x16x128_f8f6f4 v[102:105], v[18:25], v[236:243], v[102:105]
	v_mfma_f32_16x16x128_f8f6f4 v[98:101], v[26:33], v[236:243], v[98:101]
	s_setprio 0
	s_add_u32 s30, s30, 0x8000
	s_addc_u32 s31, s31, 0
	s_add_i32 s40, s67, s45
	v_lshl_add_u64 v[244:245], s[30:31], 0, v[164:165]
	s_mov_b32 m0, s40
	ds_read_b128 v[212:215], v209 offset:49152
	ds_read_b128 v[216:219], v209 offset:50176
	ds_read_b128 v[220:223], v209 offset:51200
	ds_read_b128 v[224:227], v209 offset:52224
	ds_read_b128 v[228:231], v209 offset:53248
	ds_read_b128 v[232:235], v209 offset:54272
	ds_read_b128 v[236:239], v209 offset:55296
	ds_read_b128 v[240:243], v209 offset:56320
	global_load_lds_dwordx4 v[244:245], off
	v_lshl_add_u64 v[244:245], s[30:31], 0, v[166:167]
	s_add_i32 m0, s40, 0x2000
	s_add_i32 s40, s68, s45
	global_load_lds_dwordx4 v[244:245], off
	v_lshl_add_u64 v[244:245], s[30:31], 0, v[168:169]
	s_mov_b32 m0, s40
	s_nop 0
	global_load_lds_dwordx4 v[244:245], off
	v_lshl_add_u64 v[244:245], s[30:31], 0, v[172:173]
	s_add_i32 m0, s40, 0x2000
	s_nop 0
	global_load_lds_dwordx4 v[244:245], off
	v_lshl_add_u64 v[244:245], s[28:29], 0, v[174:175]
	s_mov_b32 m0, s52
	s_nop 0
	global_load_lds_dwordx4 v[244:245], off
	v_lshl_add_u64 v[244:245], s[28:29], 0, v[176:177]
	s_mov_b32 m0, s53
	s_nop 0
	global_load_lds_dwordx4 v[244:245], off
	s_waitcnt vmcnt(8)
	s_waitcnt lgkmcnt(0)
	s_barrier
	s_setprio 2
	v_mfma_f32_16x16x128_f8f6f4 v[94:97], v[2:9], v[212:219], v[94:97]
	v_mfma_f32_16x16x128_f8f6f4 v[90:93], v[10:17], v[212:219], v[90:93]
	v_mfma_f32_16x16x128_f8f6f4 v[78:81], v[2:9], v[220:227], v[78:81]
	v_mfma_f32_16x16x128_f8f6f4 v[74:77], v[10:17], v[220:227], v[74:77]
	v_mfma_f32_16x16x128_f8f6f4 v[62:65], v[2:9], v[228:235], v[62:65]
	v_mfma_f32_16x16x128_f8f6f4 v[58:61], v[10:17], v[228:235], v[58:61]
	v_mfma_f32_16x16x128_f8f6f4 v[46:49], v[2:9], v[236:243], v[46:49]
	v_mfma_f32_16x16x128_f8f6f4 v[42:45], v[10:17], v[236:243], v[42:45]
	s_nop 3
	s_setprio 0
	s_setprio 2
	v_mfma_f32_16x16x128_f8f6f4 v[86:89], v[18:25], v[212:219], v[86:89]
	v_mfma_f32_16x16x128_f8f6f4 v[82:85], v[26:33], v[212:219], v[82:85]
	v_mfma_f32_16x16x128_f8f6f4 v[70:73], v[18:25], v[220:227], v[70:73]
	v_mfma_f32_16x16x128_f8f6f4 v[66:69], v[26:33], v[220:227], v[66:69]
	v_mfma_f32_16x16x128_f8f6f4 v[54:57], v[18:25], v[228:235], v[54:57]
	v_mfma_f32_16x16x128_f8f6f4 v[50:53], v[26:33], v[228:235], v[50:53]
	v_mfma_f32_16x16x128_f8f6f4 v[38:41], v[18:25], v[236:243], v[38:41]
	v_mfma_f32_16x16x128_f8f6f4 v[34:37], v[26:33], v[236:243], v[34:37]
	s_setprio 0
	s_add_i32 s21, s21, 2
	s_add_u32 s5, s5, 0x10000
	s_addc_u32 s19, s19, 0
	s_add_u32 s26, s26, 0x10000
	s_addc_u32 s27, s27, 0
	s_cmp_gt_u32 s21, 13
	s_cbranch_scc0 .Lh1_372

; #define PG8_STAGE(bufoff, gbase, voff) do { _Pragma("unroll") for (int _i = 0; _i < 2; ++_i) \
;         __builtin_amdgcn_global_load_lds((const unsigned*)((const char*)(gbase) + (voff)[_i]), (PG8_LAS unsigned*)(lds + (bufoff) + ldsw + _i * 8192), 16, 0, 0); } while (0)
; #define PG8_WAIT_V(n) asm volatile("s_waitcnt vmcnt(" #n ")" ::: "memory")
; #define PG8_WAIT_L(n) asm volatile("s_waitcnt lgkmcnt(" #n ")" ::: "memory")
; #define PG8_BAR __builtin_amdgcn_s_barrier()
; #define PG8_SCHED __builtin_amdgcn_sched_barrier(0)
; template <class Epi, class Sched, bool ALIGN_EPI = true, bool F8 = false>
; __device__ __forceinline__ void gemm_phase(PG8_LAS unsigned char* lds, const Sched& S, const Epi& E) {
;     ...
;         for (int t = 0; t < nt; t += 2) {
;             const bool last = (t == nt - 2);
;             if constexpr (Sched::GATHER) { if (last && has_next) S.a_off(nxt, Rs, Cs, voffAn); }
;             const char* a1 = cA + (size_t)(t + 1) * kstep;
;             const char* a2 = last ? nA : cA + (size_t)(t + 2) * kstep; const char* b2 = last ? nB : cB + (size_t)(t + 2) * kstepB;
;             const char* a3 = a2 + kstep; const char* b3 = b2 + kstepB;
;             unsigned vA2[2][2];
; #pragma unroll
;             for (int h = 0; h < 2; ++h)
; #pragma unroll
;                 for (int i = 0; i < 2; ++i) { if constexpr (Sched::GATHER) vA2[h][i] = (last && has_next) ? voffAn[h][i] : voffA[h][i]; else vA2[h][i] = voffA[h][i]; }
;             PG8_LDB(B0, 0, 0); PG8_LDB(B1, 0, 1); PG8_SCHED; PG8_LDA(At, 0, 0); PG8_STAGE(PG8_SA(1, 1), a1, voffA[1]);
;             PG8_WAIT_V(8); PG8_WAIT_L(0); PG8_BAR; PG8_MMA(0, 0, At, B0); PG8_MMA(0, 1, At, B1); PG8_BAR; PG8_SCHED;
;             PG8_LDA(At, 0, 1); PG8_STAGE(PG8_SB(0, 0), b2, voffB[0]); PG8_STAGE(PG8_SB(0, 1), b2, voffB[1]); PG8_STAGE(PG8_SA(0, 0), a2, vA2[0]);
;             PG8_WAIT_V(8); PG8_WAIT_L(0); PG8_BAR; PG8_MMA(1, 0, At, B0); PG8_MMA(1, 1, At, B1); PG8_BAR; PG8_SCHED;
.LBB0_428:
	ds_read_b128 v[18:21], v192
	ds_read_b128 v[22:25], v192 offset:1024
	ds_read_b128 v[26:29], v192 offset:2048
	ds_read_b128 v[30:33], v192 offset:3072
	ds_read_b128 v[2:5], v193
	ds_read_b128 v[6:9], v193 offset:1024
	ds_read_b128 v[10:13], v193 offset:2048
	ds_read_b128 v[14:17], v193 offset:3072
	s_add_u32 s26, s24, 0x8000
	s_addc_u32 s27, s25, 0
	s_cmp_eq_u32 s74, 12
	s_cselect_b32 s30, s20, s26
	s_cselect_b32 s31, s21, s27
	s_cselect_b32 s28, s22, s17
	s_cselect_b32 s29, s23, s19
	s_add_u32 s26, s30, 0x8000
	s_addc_u32 s27, s31, 0
	v_lshl_add_u64 v[230:231], s[24:25], 0, v[184:185]
	s_add_i32 m0, s48, 0xc000
	ds_read_b128 v[198:201], v194
	ds_read_b128 v[202:205], v194 offset:1024
	ds_read_b128 v[206:209], v194 offset:2048
	ds_read_b128 v[210:213], v194 offset:3072
	ds_read_b128 v[214:217], v194 offset:4096
	ds_read_b128 v[218:221], v194 offset:5120
	ds_read_b128 v[222:225], v194 offset:6144
	ds_read_b128 v[226:229], v194 offset:7168
	global_load_lds_dwordx4 v[230:231], off
	v_lshl_add_u64 v[230:231], s[24:25], 0, v[182:183]
	s_add_i32 m0, s48, 0xe000
	s_nop 0
	global_load_lds_dwordx4 v[230:231], off
	s_waitcnt vmcnt(8)
	s_waitcnt lgkmcnt(0)
	s_setprio 1
	v_mfma_f32_16x16x128_f8f6f4 v[158:161], v[18:25], v[198:205], v[158:161]
	v_mfma_f32_16x16x128_f8f6f4 v[154:157], v[26:33], v[198:205], v[154:157]
	v_mfma_f32_16x16x128_f8f6f4 v[142:145], v[18:25], v[206:213], v[142:145]
	v_mfma_f32_16x16x128_f8f6f4 v[138:141], v[26:33], v[206:213], v[138:141]
	v_mfma_f32_16x16x128_f8f6f4 v[126:129], v[18:25], v[214:221], v[126:129]
	v_mfma_f32_16x16x128_f8f6f4 v[122:125], v[26:33], v[214:221], v[122:125]
	v_mfma_f32_16x16x128_f8f6f4 v[110:113], v[18:25], v[222:229], v[110:113]
	v_mfma_f32_16x16x128_f8f6f4 v[106:109], v[26:33], v[222:229], v[106:109]
	s_nop 3
	s_setprio 0
	s_setprio 1
	v_mfma_f32_16x16x128_f8f6f4 v[150:153], v[2:9], v[198:205], v[150:153]
	v_mfma_f32_16x16x128_f8f6f4 v[146:149], v[10:17], v[198:205], v[146:149]
	v_mfma_f32_16x16x128_f8f6f4 v[134:137], v[2:9], v[206:213], v[134:137]
	v_mfma_f32_16x16x128_f8f6f4 v[130:133], v[10:17], v[206:213], v[130:133]
	v_mfma_f32_16x16x128_f8f6f4 v[118:121], v[2:9], v[214:221], v[118:121]
	v_mfma_f32_16x16x128_f8f6f4 v[114:117], v[10:17], v[214:221], v[114:117]
	v_mfma_f32_16x16x128_f8f6f4 v[102:105], v[2:9], v[222:229], v[102:105]
	v_mfma_f32_16x16x128_f8f6f4 v[98:101], v[10:17], v[222:229], v[98:101]
	s_setprio 0
	s_barrier
	s_add_i32 s75, s65, s47
	v_lshl_add_u64 v[230:231], s[28:29], 0, v[164:165]
	s_mov_b32 m0, s75
	ds_read_b128 v[198:201], v194 offset:16384
	ds_read_b128 v[202:205], v194 offset:17408
	ds_read_b128 v[206:209], v194 offset:18432
	ds_read_b128 v[210:213], v194 offset:19456
	ds_read_b128 v[214:217], v194 offset:20480
	ds_read_b128 v[218:221], v194 offset:21504
	ds_read_b128 v[222:225], v194 offset:22528
	ds_read_b128 v[226:229], v194 offset:23552
	global_load_lds_dwordx4 v[230:231], off
	v_lshl_add_u64 v[232:233], s[28:29], 0, v[166:167]
	s_add_i32 m0, s75, 0x2000
	s_add_i32 s75, s66, s47
	global_load_lds_dwordx4 v[232:233], off
	v_lshl_add_u64 v[230:231], v[230:231], 0, s[4:5]
	s_mov_b32 m0, s75
	s_nop 0
	global_load_lds_dwordx4 v[230:231], off
	v_lshl_add_u64 v[230:231], v[232:233], 0, s[4:5]
	s_add_i32 m0, s75, 0x2000
	s_nop 0
	global_load_lds_dwordx4 v[230:231], off
	v_lshl_add_u64 v[230:231], s[30:31], 0, v[174:175]
	s_mov_b32 m0, s48
	s_nop 0
	global_load_lds_dwordx4 v[230:231], off
	v_lshl_add_u64 v[230:231], s[30:31], 0, v[176:177]
	s_mov_b32 m0, s49
	s_nop 0
	global_load_lds_dwordx4 v[230:231], off
	s_waitcnt vmcnt(8)
	s_waitcnt lgkmcnt(0)
	s_setprio 1
	v_mfma_f32_16x16x128_f8f6f4 v[94:97], v[18:25], v[198:205], v[94:97]
	v_mfma_f32_16x16x128_f8f6f4 v[90:93], v[26:33], v[198:205], v[90:93]
	v_mfma_f32_16x16x128_f8f6f4 v[78:81], v[18:25], v[206:213], v[78:81]
	v_mfma_f32_16x16x128_f8f6f4 v[74:77], v[26:33], v[206:213], v[74:77]
	v_mfma_f32_16x16x128_f8f6f4 v[62:65], v[18:25], v[214:221], v[62:65]
	v_mfma_f32_16x16x128_f8f6f4 v[58:61], v[26:33], v[214:221], v[58:61]
	v_mfma_f32_16x16x128_f8f6f4 v[46:49], v[18:25], v[222:229], v[46:49]
	v_mfma_f32_16x16x128_f8f6f4 v[42:45], v[26:33], v[222:229], v[42:45]
	s_nop 3
	s_setprio 0
	s_setprio 1
	v_mfma_f32_16x16x128_f8f6f4 v[86:89], v[2:9], v[198:205], v[86:89]
	v_mfma_f32_16x16x128_f8f6f4 v[82:85], v[10:17], v[198:205], v[82:85]
	v_mfma_f32_16x16x128_f8f6f4 v[70:73], v[2:9], v[206:213], v[70:73]
	v_mfma_f32_16x16x128_f8f6f4 v[66:69], v[10:17], v[206:213], v[66:69]
	v_mfma_f32_16x16x128_f8f6f4 v[54:57], v[2:9], v[214:221], v[54:57]
	v_mfma_f32_16x16x128_f8f6f4 v[50:53], v[10:17], v[214:221], v[50:53]
	v_mfma_f32_16x16x128_f8f6f4 v[38:41], v[2:9], v[222:229], v[38:41]
	v_mfma_f32_16x16x128_f8f6f4 v[34:37], v[10:17], v[222:229], v[34:37]
	s_setprio 0
	s_barrier
; #define PG8_STAGE(bufoff, gbase, voff) do { _Pragma("unroll") for (int _i = 0; _i < 2; ++_i) \
;         __builtin_amdgcn_global_load_lds((const unsigned*)((const char*)(gbase) + (voff)[_i]), (PG8_LAS unsigned*)(lds + (bufoff) + ldsw + _i * 8192), 16, 0, 0); } while (0)
; #define PG8_WAIT_V(n) asm volatile("s_waitcnt vmcnt(" #n ")" ::: "memory")
; #define PG8_WAIT_L(n) asm volatile("s_waitcnt lgkmcnt(" #n ")" ::: "memory")
; #define PG8_BAR __builtin_amdgcn_s_barrier()
; #define PG8_SCHED __builtin_amdgcn_sched_barrier(0)
; template <class Epi, class Sched, bool ALIGN_EPI = true, bool F8 = false>
; __device__ __forceinline__ void gemm_phase(PG8_LAS unsigned char* lds, const Sched& S, const Epi& E) {
;     ...
;             PG8_LDB(B0, 1, 0); PG8_LDB(B1, 1, 1); PG8_SCHED; PG8_LDA(At, 1, 0); PG8_STAGE(PG8_SA(0, 1), a2, vA2[1]);
;             PG8_WAIT_V(8); PG8_WAIT_L(0); PG8_BAR; PG8_MMA(0, 0, At, B0); PG8_MMA(0, 1, At, B1); PG8_BAR; PG8_SCHED;
;             PG8_LDA(At, 1, 1); PG8_STAGE(PG8_SB(1, 0), b3, voffB[0]); PG8_STAGE(PG8_SB(1, 1), b3, voffB[1]); PG8_STAGE(PG8_SA(1, 0), a3, vA2[0]);
;             PG8_WAIT_V(8); PG8_WAIT_L(0); PG8_BAR; PG8_MMA(1, 0, At, B0); PG8_MMA(1, 1, At, B1); PG8_BAR; PG8_SCHED;
	s_add_i32 s75, 0, 0x18000
	s_add_i32 s76, 0, 0x1c000
	v_add_u32_e32 v14, s75, v191
	v_add_u32_e32 v30, s76, v191
	ds_read_b128 v[2:5], v14
	ds_read_b128 v[6:9], v14 offset:1024
	ds_read_b128 v[10:13], v14 offset:2048
	ds_read_b128 v[14:17], v14 offset:3072
	ds_read_b128 v[18:21], v30
	ds_read_b128 v[22:25], v30 offset:1024
	ds_read_b128 v[26:29], v30 offset:2048
	ds_read_b128 v[30:33], v30 offset:3072
	s_mov_b32 m0, s50
	v_lshl_add_u64 v[230:231], s[30:31], 0, v[178:179]
	ds_read_b128 v[198:201], v194 offset:32768
	ds_read_b128 v[202:205], v194 offset:33792
	ds_read_b128 v[206:209], v194 offset:34816
	ds_read_b128 v[210:213], v194 offset:35840
	ds_read_b128 v[214:217], v194 offset:36864
	ds_read_b128 v[218:221], v194 offset:37888
	ds_read_b128 v[222:225], v194 offset:38912
	ds_read_b128 v[226:229], v194 offset:39936
	global_load_lds_dwordx4 v[230:231], off
	v_lshl_add_u64 v[230:231], s[30:31], 0, v[180:181]
	s_mov_b32 m0, s51
	s_nop 0
	global_load_lds_dwordx4 v[230:231], off
	s_waitcnt vmcnt(8)
	s_waitcnt lgkmcnt(0)
	s_setprio 1
	v_mfma_f32_16x16x128_f8f6f4 v[158:161], v[2:9], v[198:205], v[158:161]
	v_mfma_f32_16x16x128_f8f6f4 v[154:157], v[10:17], v[198:205], v[154:157]
	v_mfma_f32_16x16x128_f8f6f4 v[142:145], v[2:9], v[206:213], v[142:145]
	v_mfma_f32_16x16x128_f8f6f4 v[138:141], v[10:17], v[206:213], v[138:141]
	v_mfma_f32_16x16x128_f8f6f4 v[126:129], v[2:9], v[214:221], v[126:129]
	v_mfma_f32_16x16x128_f8f6f4 v[122:125], v[10:17], v[214:221], v[122:125]
	v_mfma_f32_16x16x128_f8f6f4 v[110:113], v[2:9], v[222:229], v[110:113]
	v_mfma_f32_16x16x128_f8f6f4 v[106:109], v[10:17], v[222:229], v[106:109]
	s_nop 3
	s_setprio 0
	s_setprio 1
	v_mfma_f32_16x16x128_f8f6f4 v[150:153], v[18:25], v[198:205], v[150:153]
	v_mfma_f32_16x16x128_f8f6f4 v[146:149], v[26:33], v[198:205], v[146:149]
	v_mfma_f32_16x16x128_f8f6f4 v[134:137], v[18:25], v[206:213], v[134:137]
	v_mfma_f32_16x16x128_f8f6f4 v[130:133], v[26:33], v[206:213], v[130:133]
	v_mfma_f32_16x16x128_f8f6f4 v[118:121], v[18:25], v[214:221], v[118:121]
	v_mfma_f32_16x16x128_f8f6f4 v[114:117], v[26:33], v[214:221], v[114:117]
	v_mfma_f32_16x16x128_f8f6f4 v[102:105], v[18:25], v[222:229], v[102:105]
	v_mfma_f32_16x16x128_f8f6f4 v[98:101], v[26:33], v[222:229], v[98:101]
	s_setprio 0
	s_barrier
	s_add_u32 s28, s28, 0x8000
	s_addc_u32 s29, s29, 0
	s_add_i32 s30, s75, s47
	v_lshl_add_u64 v[230:231], s[28:29], 0, v[164:165]
	s_mov_b32 m0, s30
	ds_read_b128 v[198:201], v194 offset:49152
	ds_read_b128 v[202:205], v194 offset:50176
	ds_read_b128 v[206:209], v194 offset:51200
	ds_read_b128 v[210:213], v194 offset:52224
	ds_read_b128 v[214:217], v194 offset:53248
	ds_read_b128 v[218:221], v194 offset:54272
	ds_read_b128 v[222:225], v194 offset:55296
	ds_read_b128 v[226:229], v194 offset:56320
	global_load_lds_dwordx4 v[230:231], off
	v_lshl_add_u64 v[230:231], s[28:29], 0, v[166:167]
	s_add_i32 m0, s30, 0x2000
	s_add_i32 s30, s76, s47
	global_load_lds_dwordx4 v[230:231], off
	v_lshl_add_u64 v[230:231], s[28:29], 0, v[168:169]
	s_mov_b32 m0, s30
	s_nop 0
	global_load_lds_dwordx4 v[230:231], off
	v_lshl_add_u64 v[230:231], s[28:29], 0, v[172:173]
	s_add_i32 m0, s30, 0x2000
	s_nop 0
	global_load_lds_dwordx4 v[230:231], off
	v_lshl_add_u64 v[230:231], s[26:27], 0, v[174:175]
	s_mov_b32 m0, s60
	s_nop 0
	global_load_lds_dwordx4 v[230:231], off
	v_lshl_add_u64 v[230:231], s[26:27], 0, v[176:177]
	s_mov_b32 m0, s61
	s_nop 0
	global_load_lds_dwordx4 v[230:231], off
	s_waitcnt vmcnt(8)
	s_waitcnt lgkmcnt(0)
	s_setprio 1
	v_mfma_f32_16x16x128_f8f6f4 v[94:97], v[2:9], v[198:205], v[94:97]
	v_mfma_f32_16x16x128_f8f6f4 v[90:93], v[10:17], v[198:205], v[90:93]
	v_mfma_f32_16x16x128_f8f6f4 v[78:81], v[2:9], v[206:213], v[78:81]
	v_mfma_f32_16x16x128_f8f6f4 v[74:77], v[10:17], v[206:213], v[74:77]
	v_mfma_f32_16x16x128_f8f6f4 v[62:65], v[2:9], v[214:221], v[62:65]
	v_mfma_f32_16x16x128_f8f6f4 v[58:61], v[10:17], v[214:221], v[58:61]
	v_mfma_f32_16x16x128_f8f6f4 v[46:49], v[2:9], v[222:229], v[46:49]
	v_mfma_f32_16x16x128_f8f6f4 v[42:45], v[10:17], v[222:229], v[42:45]
	s_nop 3
	s_setprio 0
	s_setprio 1
	v_mfma_f32_16x16x128_f8f6f4 v[86:89], v[18:25], v[198:205], v[86:89]
	v_mfma_f32_16x16x128_f8f6f4 v[82:85], v[26:33], v[198:205], v[82:85]
	v_mfma_f32_16x16x128_f8f6f4 v[70:73], v[18:25], v[206:213], v[70:73]
	v_mfma_f32_16x16x128_f8f6f4 v[66:69], v[26:33], v[206:213], v[66:69]
	v_mfma_f32_16x16x128_f8f6f4 v[54:57], v[18:25], v[214:221], v[54:57]
	v_mfma_f32_16x16x128_f8f6f4 v[50:53], v[26:33], v[214:221], v[50:53]
	v_mfma_f32_16x16x128_f8f6f4 v[38:41], v[18:25], v[222:229], v[38:41]
	v_mfma_f32_16x16x128_f8f6f4 v[34:37], v[26:33], v[222:229], v[34:37]
	s_setprio 0
	s_barrier
	s_add_i32 s74, s74, 2
	s_add_u32 s17, s17, 0x10000
	s_addc_u32 s19, s19, 0
	s_add_u32 s24, s24, 0x10000
	s_addc_u32 s25, s25, 0
	s_cmp_gt_u32 s74, 13
	s_cbranch_scc0 .LBB0_428
	s_branch .Lfx_11141
; #define PG8_STAGE(bufoff, gbase, voff) do { _Pragma("unroll") for (int _i = 0; _i < 2; ++_i) \
;         __builtin_amdgcn_global_load_lds((const unsigned*)((const char*)(gbase) + (voff)[_i]), (PG8_LAS unsigned*)(lds + (bufoff) + ldsw + _i * 8192), 16, 0, 0); } while (0)
; #define PG8_WAIT_V(n) asm volatile("s_waitcnt vmcnt(" #n ")" ::: "memory")
; #define PG8_WAIT_L(n) asm volatile("s_waitcnt lgkmcnt(" #n ")" ::: "memory")
; #define PG8_BAR __builtin_amdgcn_s_barrier()
; #define PG8_SCHED __builtin_amdgcn_sched_barrier(0)
; template <class Epi, class Sched, bool ALIGN_EPI = true, bool F8 = false>
; __device__ __forceinline__ void gemm_phase(PG8_LAS unsigned char* lds, const Sched& S, const Epi& E) {
;     ...
;         for (int t = 0; t < nt; t += 2) {
;             const bool last = (t == nt - 2);
;             if constexpr (Sched::GATHER) { if (last && has_next) S.a_off(nxt, Rs, Cs, voffAn); }
;             const char* a1 = cA + (size_t)(t + 1) * kstep;
;             const char* a2 = last ? nA : cA + (size_t)(t + 2) * kstep; const char* b2 = last ? nB : cB + (size_t)(t + 2) * kstepB;
;             const char* a3 = a2 + kstep; const char* b3 = b2 + kstepB;
;             unsigned vA2[2][2];
; #pragma unroll
;             for (int h = 0; h < 2; ++h)
; #pragma unroll
;                 for (int i = 0; i < 2; ++i) { if constexpr (Sched::GATHER) vA2[h][i] = (last && has_next) ? voffAn[h][i] : voffA[h][i]; else vA2[h][i] = voffA[h][i]; }
;             PG8_LDB(B0, 0, 0); PG8_LDB(B1, 0, 1); PG8_SCHED; PG8_LDA(At, 0, 0); PG8_STAGE(PG8_SA(1, 1), a1, voffA[1]);
;             PG8_WAIT_V(8); PG8_WAIT_L(0); PG8_BAR; PG8_MMA(0, 0, At, B0); PG8_MMA(0, 1, At, B1); PG8_BAR; PG8_SCHED;
;             PG8_LDA(At, 0, 1); PG8_STAGE(PG8_SB(0, 0), b2, voffB[0]); PG8_STAGE(PG8_SB(0, 1), b2, voffB[1]); PG8_STAGE(PG8_SA(0, 0), a2, vA2[0]);
;             PG8_WAIT_V(8); PG8_WAIT_L(0); PG8_BAR; PG8_MMA(1, 0, At, B0); PG8_MMA(1, 1, At, B1); PG8_BAR; PG8_SCHED;
;             PG8_LDB(B0, 1, 0); PG8_LDB(B1, 1, 1); PG8_SCHED; PG8_LDA(At, 1, 0); PG8_STAGE(PG8_SA(0, 1), a2, vA2[1]);
;             PG8_WAIT_V(8); PG8_WAIT_L(0); PG8_BAR; PG8_MMA(0, 0, At, B0); PG8_MMA(0, 1, At, B1); PG8_BAR; PG8_SCHED;
.Lh1e_11141:
.Lh1_428:
	ds_read_b128 v[18:21], v192
	ds_read_b128 v[22:25], v192 offset:1024
	ds_read_b128 v[26:29], v192 offset:2048
	ds_read_b128 v[30:33], v192 offset:3072
	ds_read_b128 v[2:5], v193
	ds_read_b128 v[6:9], v193 offset:1024
	ds_read_b128 v[10:13], v193 offset:2048
	ds_read_b128 v[14:17], v193 offset:3072
	s_add_u32 s26, s24, 0x8000
	s_addc_u32 s27, s25, 0
	s_cmp_eq_u32 s74, 12
	s_cselect_b32 s30, s20, s26
	s_cselect_b32 s31, s21, s27
	s_cselect_b32 s28, s22, s17
	s_cselect_b32 s29, s23, s19
	s_add_u32 s26, s30, 0x8000
	s_addc_u32 s27, s31, 0
	v_lshl_add_u64 v[230:231], s[24:25], 0, v[184:185]
	s_add_i32 m0, s48, 0xc000
	ds_read_b128 v[198:201], v194
	ds_read_b128 v[202:205], v194 offset:1024
	ds_read_b128 v[206:209], v194 offset:2048
	ds_read_b128 v[210:213], v194 offset:3072
	ds_read_b128 v[214:217], v194 offset:4096
	ds_read_b128 v[218:221], v194 offset:5120
	ds_read_b128 v[222:225], v194 offset:6144
	ds_read_b128 v[226:229], v194 offset:7168
	global_load_lds_dwordx4 v[230:231], off
	v_lshl_add_u64 v[230:231], s[24:25], 0, v[182:183]
	s_add_i32 m0, s48, 0xe000
	s_nop 0
	global_load_lds_dwordx4 v[230:231], off
	s_waitcnt vmcnt(8)
	s_waitcnt lgkmcnt(0)
	s_barrier
	s_setprio 2
	v_mfma_f32_16x16x128_f8f6f4 v[158:161], v[18:25], v[198:205], v[158:161]
	v_mfma_f32_16x16x128_f8f6f4 v[154:157], v[26:33], v[198:205], v[154:157]
	v_mfma_f32_16x16x128_f8f6f4 v[142:145], v[18:25], v[206:213], v[142:145]
	v_mfma_f32_16x16x128_f8f6f4 v[138:141], v[26:33], v[206:213], v[138:141]
	v_mfma_f32_16x16x128_f8f6f4 v[126:129], v[18:25], v[214:221], v[126:129]
	v_mfma_f32_16x16x128_f8f6f4 v[122:125], v[26:33], v[214:221], v[122:125]
	v_mfma_f32_16x16x128_f8f6f4 v[110:113], v[18:25], v[222:229], v[110:113]
	v_mfma_f32_16x16x128_f8f6f4 v[106:109], v[26:33], v[222:229], v[106:109]
	s_nop 3
	s_setprio 0
	s_setprio 2
	v_mfma_f32_16x16x128_f8f6f4 v[150:153], v[2:9], v[198:205], v[150:153]
	v_mfma_f32_16x16x128_f8f6f4 v[146:149], v[10:17], v[198:205], v[146:149]
	v_mfma_f32_16x16x128_f8f6f4 v[134:137], v[2:9], v[206:213], v[134:137]
	v_mfma_f32_16x16x128_f8f6f4 v[130:133], v[10:17], v[206:213], v[130:133]
	v_mfma_f32_16x16x128_f8f6f4 v[118:121], v[2:9], v[214:221], v[118:121]
	v_mfma_f32_16x16x128_f8f6f4 v[114:117], v[10:17], v[214:221], v[114:117]
	v_mfma_f32_16x16x128_f8f6f4 v[102:105], v[2:9], v[222:229], v[102:105]
	v_mfma_f32_16x16x128_f8f6f4 v[98:101], v[10:17], v[222:229], v[98:101]
	s_setprio 0
	s_add_i32 s75, s65, s47
	v_lshl_add_u64 v[230:231], s[28:29], 0, v[164:165]
	s_mov_b32 m0, s75
	ds_read_b128 v[198:201], v194 offset:16384
	ds_read_b128 v[202:205], v194 offset:17408
	ds_read_b128 v[206:209], v194 offset:18432
	ds_read_b128 v[210:213], v194 offset:19456
	ds_read_b128 v[214:217], v194 offset:20480
	ds_read_b128 v[218:221], v194 offset:21504
	ds_read_b128 v[222:225], v194 offset:22528
	ds_read_b128 v[226:229], v194 offset:23552
	global_load_lds_dwordx4 v[230:231], off
	v_lshl_add_u64 v[232:233], s[28:29], 0, v[166:167]
	s_add_i32 m0, s75, 0x2000
	s_add_i32 s75, s66, s47
	global_load_lds_dwordx4 v[232:233], off
	v_lshl_add_u64 v[230:231], v[230:231], 0, s[4:5]
	s_mov_b32 m0, s75
	s_nop 0
	global_load_lds_dwordx4 v[230:231], off
	v_lshl_add_u64 v[230:231], v[232:233], 0, s[4:5]
	s_add_i32 m0, s75, 0x2000
	s_nop 0
	global_load_lds_dwordx4 v[230:231], off
	v_lshl_add_u64 v[230:231], s[30:31], 0, v[174:175]
	s_mov_b32 m0, s48
	s_nop 0
	global_load_lds_dwordx4 v[230:231], off
	v_lshl_add_u64 v[230:231], s[30:31], 0, v[176:177]
	s_mov_b32 m0, s49
	s_nop 0
	global_load_lds_dwordx4 v[230:231], off
	s_waitcnt vmcnt(8)
	s_waitcnt lgkmcnt(0)
	s_barrier
	s_setprio 2
	v_mfma_f32_16x16x128_f8f6f4 v[94:97], v[18:25], v[198:205], v[94:97]
	v_mfma_f32_16x16x128_f8f6f4 v[90:93], v[26:33], v[198:205], v[90:93]
	v_mfma_f32_16x16x128_f8f6f4 v[78:81], v[18:25], v[206:213], v[78:81]
	v_mfma_f32_16x16x128_f8f6f4 v[74:77], v[26:33], v[206:213], v[74:77]
	v_mfma_f32_16x16x128_f8f6f4 v[62:65], v[18:25], v[214:221], v[62:65]
	v_mfma_f32_16x16x128_f8f6f4 v[58:61], v[26:33], v[214:221], v[58:61]
	v_mfma_f32_16x16x128_f8f6f4 v[46:49], v[18:25], v[222:229], v[46:49]
	v_mfma_f32_16x16x128_f8f6f4 v[42:45], v[26:33], v[222:229], v[42:45]
	s_nop 3
	s_setprio 0
	s_setprio 2
	v_mfma_f32_16x16x128_f8f6f4 v[86:89], v[2:9], v[198:205], v[86:89]
	v_mfma_f32_16x16x128_f8f6f4 v[82:85], v[10:17], v[198:205], v[82:85]
	v_mfma_f32_16x16x128_f8f6f4 v[70:73], v[2:9], v[206:213], v[70:73]
	v_mfma_f32_16x16x128_f8f6f4 v[66:69], v[10:17], v[206:213], v[66:69]
	v_mfma_f32_16x16x128_f8f6f4 v[54:57], v[2:9], v[214:221], v[54:57]
	v_mfma_f32_16x16x128_f8f6f4 v[50:53], v[10:17], v[214:221], v[50:53]
	v_mfma_f32_16x16x128_f8f6f4 v[38:41], v[2:9], v[222:229], v[38:41]
	v_mfma_f32_16x16x128_f8f6f4 v[34:37], v[10:17], v[222:229], v[34:37]
	s_setprio 0
	s_add_i32 s75, 0, 0x18000
	s_add_i32 s76, 0, 0x1c000
	v_add_u32_e32 v14, s75, v191
	v_add_u32_e32 v30, s76, v191
	ds_read_b128 v[2:5], v14
	ds_read_b128 v[6:9], v14 offset:1024
	ds_read_b128 v[10:13], v14 offset:2048
	ds_read_b128 v[14:17], v14 offset:3072
	ds_read_b128 v[18:21], v30
	ds_read_b128 v[22:25], v30 offset:1024
	ds_read_b128 v[26:29], v30 offset:2048
	ds_read_b128 v[30:33], v30 offset:3072
	s_mov_b32 m0, s50
	v_lshl_add_u64 v[230:231], s[30:31], 0, v[178:179]
	ds_read_b128 v[198:201], v194 offset:32768
	ds_read_b128 v[202:205], v194 offset:33792
	ds_read_b128 v[206:209], v194 offset:34816
	ds_read_b128 v[210:213], v194 offset:35840
	ds_read_b128 v[214:217], v194 offset:36864
	ds_read_b128 v[218:221], v194 offset:37888
	ds_read_b128 v[222:225], v194 offset:38912
	ds_read_b128 v[226:229], v194 offset:39936
	global_load_lds_dwordx4 v[230:231], off
	v_lshl_add_u64 v[230:231], s[30:31], 0, v[180:181]
	s_mov_b32 m0, s51
	s_nop 0
	global_load_lds_dwordx4 v[230:231], off
	s_waitcnt vmcnt(8)
	s_waitcnt lgkmcnt(0)
	s_barrier
; #define PG8_STAGE(bufoff, gbase, voff) do { _Pragma("unroll") for (int _i = 0; _i < 2; ++_i) \
;         __builtin_amdgcn_global_load_lds((const unsigned*)((const char*)(gbase) + (voff)[_i]), (PG8_LAS unsigned*)(lds + (bufoff) + ldsw + _i * 8192), 16, 0, 0); } while (0)
; #define PG8_WAIT_V(n) asm volatile("s_waitcnt vmcnt(" #n ")" ::: "memory")
; #define PG8_WAIT_L(n) asm volatile("s_waitcnt lgkmcnt(" #n ")" ::: "memory")
; #define PG8_BAR __builtin_amdgcn_s_barrier()
; #define PG8_SCHED __builtin_amdgcn_sched_barrier(0)
; template <class Epi, class Sched, bool ALIGN_EPI = true, bool F8 = false>
; __device__ __forceinline__ void gemm_phase(PG8_LAS unsigned char* lds, const Sched& S, const Epi& E) {
;     ...
;             PG8_WAIT_V(8); PG8_WAIT_L(0); PG8_BAR; PG8_MMA(0, 0, At, B0); PG8_MMA(0, 1, At, B1); PG8_BAR; PG8_SCHED;
;             PG8_LDA(At, 1, 1); PG8_STAGE(PG8_SB(1, 0), b3, voffB[0]); PG8_STAGE(PG8_SB(1, 1), b3, voffB[1]); PG8_STAGE(PG8_SA(1, 0), a3, vA2[0]);
;             PG8_WAIT_V(8); PG8_WAIT_L(0); PG8_BAR; PG8_MMA(1, 0, At, B0); PG8_MMA(1, 1, At, B1); PG8_BAR; PG8_SCHED;
	s_setprio 2
	v_mfma_f32_16x16x128_f8f6f4 v[158:161], v[2:9], v[198:205], v[158:161]
	v_mfma_f32_16x16x128_f8f6f4 v[154:157], v[10:17], v[198:205], v[154:157]
	v_mfma_f32_16x16x128_f8f6f4 v[142:145], v[2:9], v[206:213], v[142:145]
	v_mfma_f32_16x16x128_f8f6f4 v[138:141], v[10:17], v[206:213], v[138:141]
	v_mfma_f32_16x16x128_f8f6f4 v[126:129], v[2:9], v[214:221], v[126:129]
	v_mfma_f32_16x16x128_f8f6f4 v[122:125], v[10:17], v[214:221], v[122:125]
	v_mfma_f32_16x16x128_f8f6f4 v[110:113], v[2:9], v[222:229], v[110:113]
	v_mfma_f32_16x16x128_f8f6f4 v[106:109], v[10:17], v[222:229], v[106:109]
	s_nop 3
	s_setprio 0
	s_setprio 2
	v_mfma_f32_16x16x128_f8f6f4 v[150:153], v[18:25], v[198:205], v[150:153]
	v_mfma_f32_16x16x128_f8f6f4 v[146:149], v[26:33], v[198:205], v[146:149]
	v_mfma_f32_16x16x128_f8f6f4 v[134:137], v[18:25], v[206:213], v[134:137]
	v_mfma_f32_16x16x128_f8f6f4 v[130:133], v[26:33], v[206:213], v[130:133]
	v_mfma_f32_16x16x128_f8f6f4 v[118:121], v[18:25], v[214:221], v[118:121]
	v_mfma_f32_16x16x128_f8f6f4 v[114:117], v[26:33], v[214:221], v[114:117]
	v_mfma_f32_16x16x128_f8f6f4 v[102:105], v[18:25], v[222:229], v[102:105]
	v_mfma_f32_16x16x128_f8f6f4 v[98:101], v[26:33], v[222:229], v[98:101]
	s_setprio 0
	s_add_u32 s28, s28, 0x8000
	s_addc_u32 s29, s29, 0
	s_add_i32 s30, s75, s47
	v_lshl_add_u64 v[230:231], s[28:29], 0, v[164:165]
	s_mov_b32 m0, s30
	ds_read_b128 v[198:201], v194 offset:49152
	ds_read_b128 v[202:205], v194 offset:50176
	ds_read_b128 v[206:209], v194 offset:51200
	ds_read_b128 v[210:213], v194 offset:52224
	ds_read_b128 v[214:217], v194 offset:53248
	ds_read_b128 v[218:221], v194 offset:54272
	ds_read_b128 v[222:225], v194 offset:55296
	ds_read_b128 v[226:229], v194 offset:56320
	global_load_lds_dwordx4 v[230:231], off
	v_lshl_add_u64 v[230:231], s[28:29], 0, v[166:167]
	s_add_i32 m0, s30, 0x2000
	s_add_i32 s30, s76, s47
	global_load_lds_dwordx4 v[230:231], off
	v_lshl_add_u64 v[230:231], s[28:29], 0, v[168:169]
	s_mov_b32 m0, s30
	s_nop 0
	global_load_lds_dwordx4 v[230:231], off
	v_lshl_add_u64 v[230:231], s[28:29], 0, v[172:173]
	s_add_i32 m0, s30, 0x2000
	s_nop 0
	global_load_lds_dwordx4 v[230:231], off
	v_lshl_add_u64 v[230:231], s[26:27], 0, v[174:175]
	s_mov_b32 m0, s60
	s_nop 0
	global_load_lds_dwordx4 v[230:231], off
	v_lshl_add_u64 v[230:231], s[26:27], 0, v[176:177]
	s_mov_b32 m0, s61
	s_nop 0
	global_load_lds_dwordx4 v[230:231], off
	s_waitcnt vmcnt(8)
	s_waitcnt lgkmcnt(0)
	s_barrier
	s_setprio 2
	v_mfma_f32_16x16x128_f8f6f4 v[94:97], v[2:9], v[198:205], v[94:97]
	v_mfma_f32_16x16x128_f8f6f4 v[90:93], v[10:17], v[198:205], v[90:93]
	v_mfma_f32_16x16x128_f8f6f4 v[78:81], v[2:9], v[206:213], v[78:81]
	v_mfma_f32_16x16x128_f8f6f4 v[74:77], v[10:17], v[206:213], v[74:77]
	v_mfma_f32_16x16x128_f8f6f4 v[62:65], v[2:9], v[214:221], v[62:65]
	v_mfma_f32_16x16x128_f8f6f4 v[58:61], v[10:17], v[214:221], v[58:61]
	v_mfma_f32_16x16x128_f8f6f4 v[46:49], v[2:9], v[222:229], v[46:49]
	v_mfma_f32_16x16x128_f8f6f4 v[42:45], v[10:17], v[222:229], v[42:45]
	s_nop 3
	s_setprio 0
	s_setprio 2
	v_mfma_f32_16x16x128_f8f6f4 v[86:89], v[18:25], v[198:205], v[86:89]
	v_mfma_f32_16x16x128_f8f6f4 v[82:85], v[26:33], v[198:205], v[82:85]
	v_mfma_f32_16x16x128_f8f6f4 v[70:73], v[18:25], v[206:213], v[70:73]
	v_mfma_f32_16x16x128_f8f6f4 v[66:69], v[26:33], v[206:213], v[66:69]
	v_mfma_f32_16x16x128_f8f6f4 v[54:57], v[18:25], v[214:221], v[54:57]
	v_mfma_f32_16x16x128_f8f6f4 v[50:53], v[26:33], v[214:221], v[50:53]
	v_mfma_f32_16x16x128_f8f6f4 v[38:41], v[18:25], v[222:229], v[38:41]
	v_mfma_f32_16x16x128_f8f6f4 v[34:37], v[26:33], v[222:229], v[34:37]
	s_setprio 0
	s_add_i32 s74, s74, 2
	s_add_u32 s17, s17, 0x10000
	s_addc_u32 s19, s19, 0
	s_add_u32 s24, s24, 0x10000
	s_addc_u32 s25, s25, 0
	s_cmp_gt_u32 s74, 13
	s_cbranch_scc0 .Lh1_428

; #define PG8_STAGE(bufoff, gbase, voff) do { _Pragma("unroll") for (int _i = 0; _i < 2; ++_i) \
;         __builtin_amdgcn_global_load_lds((const unsigned*)((const char*)(gbase) + (voff)[_i]), (PG8_LAS unsigned*)(lds + (bufoff) + ldsw + _i * 8192), 16, 0, 0); } while (0)
; #define PG8_WAIT_V(n) asm volatile("s_waitcnt vmcnt(" #n ")" ::: "memory")
; #define PG8_WAIT_L(n) asm volatile("s_waitcnt lgkmcnt(" #n ")" ::: "memory")
; #define PG8_BAR __builtin_amdgcn_s_barrier()
; #define PG8_SCHED __builtin_amdgcn_sched_barrier(0)
; template <class Epi, class Sched, bool ALIGN_EPI = true, bool F8 = false>
; __device__ __forceinline__ void gemm_phase(PG8_LAS unsigned char* lds, const Sched& S, const Epi& E) {
;     ...
;             PG8_LDB(B0, 0, 0); PG8_LDB(B1, 0, 1); PG8_SCHED; PG8_LDA(At, 0, 0); PG8_STAGE(PG8_SA(1, 1), a1, voffA[1]);
;             PG8_WAIT_V(8); PG8_WAIT_L(0); PG8_BAR; PG8_MMA(0, 0, At, B0); PG8_MMA(0, 1, At, B1); PG8_BAR; PG8_SCHED;
;             PG8_LDA(At, 0, 1); PG8_STAGE(PG8_SB(0, 0), b2, voffB[0]); PG8_STAGE(PG8_SB(0, 1), b2, voffB[1]); PG8_STAGE(PG8_SA(0, 0), a2, vA2[0]);
;             PG8_WAIT_V(8); PG8_WAIT_L(0); PG8_BAR; PG8_MMA(1, 0, At, B0); PG8_MMA(1, 1, At, B1); PG8_BAR; PG8_SCHED;
.LBB0_834:
	v_add_u32_e32 v10, s58, v190
	ds_read_b128 v[2:5], v10
	ds_read_b128 v[6:9], v10 offset:1024
	ds_read_b128 v[142:145], v10 offset:2048
	ds_read_b128 v[146:149], v10 offset:3072
	v_add_u32_e32 v10, s59, v190
	ds_read_b128 v[150:153], v10
	ds_read_b128 v[154:157], v10 offset:1024
	ds_read_b128 v[202:205], v10 offset:2048
	ds_read_b128 v[206:209], v10 offset:3072
	s_add_i32 s77, s26, 2
	s_add_u32 s27, s24, 0x8000
	s_addc_u32 s28, s25, 0
	s_cmp_eq_u32 s74, s26
	s_cselect_b32 s30, s20, s27
	s_cselect_b32 s31, s21, s28
	s_cselect_b32 s28, s22, s75
	s_cselect_b32 s29, s23, s76
	s_add_u32 s26, s30, 0x8000
	s_addc_u32 s27, s31, 0
	v_lshl_add_u64 v[12:13], s[24:25], 0, v[182:183]
	s_add_i32 m0, s45, 0xc000
	ds_read_b128 v[210:213], v198
	ds_read_b128 v[214:217], v198 offset:1024
	ds_read_b128 v[218:221], v198 offset:2048
	ds_read_b128 v[222:225], v198 offset:3072
	ds_read_b128 v[226:229], v198 offset:4096
	ds_read_b128 v[230:233], v198 offset:5120
	ds_read_b128 v[234:237], v198 offset:6144
	ds_read_b128 v[238:241], v198 offset:7168
	global_load_lds_dwordx4 v[12:13], off
	v_lshl_add_u64 v[12:13], s[24:25], 0, v[180:181]
	s_add_i32 m0, s45, 0xe000
	s_nop 0
	global_load_lds_dwordx4 v[12:13], off
	s_waitcnt vmcnt(8)
	s_waitcnt lgkmcnt(0)
	s_setprio 1
	v_mfma_f32_16x16x128_f8f6f4 v[138:141], v[2:9], v[210:217], v[138:141]
	v_mfma_f32_16x16x128_f8f6f4 v[134:137], v[142:149], v[210:217], v[134:137]
	v_mfma_f32_16x16x128_f8f6f4 v[130:133], v[2:9], v[218:225], v[130:133]
	v_mfma_f32_16x16x128_f8f6f4 v[126:129], v[142:149], v[218:225], v[126:129]
	v_mfma_f32_16x16x128_f8f6f4 v[122:125], v[2:9], v[226:233], v[122:125]
	v_mfma_f32_16x16x128_f8f6f4 v[118:121], v[142:149], v[226:233], v[118:121]
	v_mfma_f32_16x16x128_f8f6f4 v[114:117], v[2:9], v[234:241], v[114:117]
	v_mfma_f32_16x16x128_f8f6f4 v[110:113], v[142:149], v[234:241], v[110:113]
	s_nop 3
	s_setprio 0
	s_setprio 1
	v_mfma_f32_16x16x128_f8f6f4 v[106:109], v[150:157], v[210:217], v[106:109]
	v_mfma_f32_16x16x128_f8f6f4 v[102:105], v[202:209], v[210:217], v[102:105]
	v_mfma_f32_16x16x128_f8f6f4 v[98:101], v[150:157], v[218:225], v[98:101]
	v_mfma_f32_16x16x128_f8f6f4 v[94:97], v[202:209], v[218:225], v[94:97]
	v_mfma_f32_16x16x128_f8f6f4 v[90:93], v[150:157], v[226:233], v[90:93]
	v_mfma_f32_16x16x128_f8f6f4 v[86:89], v[202:209], v[226:233], v[86:89]
	v_mfma_f32_16x16x128_f8f6f4 v[82:85], v[150:157], v[234:241], v[82:85]
	v_mfma_f32_16x16x128_f8f6f4 v[78:81], v[202:209], v[234:241], v[78:81]
	s_setprio 0
	s_barrier
	s_add_i32 s78, s58, s44
	v_lshl_add_u64 v[12:13], s[28:29], 0, v[158:159]
	s_mov_b32 m0, s78
	ds_read_b128 v[210:213], v198 offset:16384
	ds_read_b128 v[214:217], v198 offset:17408
	ds_read_b128 v[218:221], v198 offset:18432
	ds_read_b128 v[222:225], v198 offset:19456
	ds_read_b128 v[226:229], v198 offset:20480
	ds_read_b128 v[230:233], v198 offset:21504
	ds_read_b128 v[234:237], v198 offset:22528
	ds_read_b128 v[238:241], v198 offset:23552
	global_load_lds_dwordx4 v[12:13], off
	v_lshl_add_u64 v[188:189], s[28:29], 0, v[160:161]
	s_add_i32 m0, s78, 0x2000
	s_add_i32 s78, s59, s44
	global_load_lds_dwordx4 v[188:189], off
	v_lshl_add_u64 v[12:13], v[12:13], 0, s[8:9]
	s_mov_b32 m0, s78
	s_nop 0
	global_load_lds_dwordx4 v[12:13], off
	v_lshl_add_u64 v[12:13], v[188:189], 0, s[8:9]
	s_add_i32 m0, s78, 0x2000
	s_nop 0
	global_load_lds_dwordx4 v[12:13], off
	v_lshl_add_u64 v[12:13], s[30:31], 0, v[162:163]
	s_mov_b32 m0, s45
	s_nop 0
	global_load_lds_dwordx4 v[12:13], off
	v_lshl_add_u64 v[12:13], s[30:31], 0, v[164:165]
	s_mov_b32 m0, s46
	s_nop 0
	global_load_lds_dwordx4 v[12:13], off
	s_waitcnt vmcnt(8)
	s_waitcnt lgkmcnt(0)
	s_setprio 1
	v_mfma_f32_16x16x128_f8f6f4 v[74:77], v[2:9], v[210:217], v[74:77]
	v_mfma_f32_16x16x128_f8f6f4 v[70:73], v[142:149], v[210:217], v[70:73]
	v_mfma_f32_16x16x128_f8f6f4 v[66:69], v[2:9], v[218:225], v[66:69]
	v_mfma_f32_16x16x128_f8f6f4 v[62:65], v[142:149], v[218:225], v[62:65]
	v_mfma_f32_16x16x128_f8f6f4 v[58:61], v[2:9], v[226:233], v[58:61]
	v_mfma_f32_16x16x128_f8f6f4 v[54:57], v[142:149], v[226:233], v[54:57]
	v_mfma_f32_16x16x128_f8f6f4 v[50:53], v[2:9], v[234:241], v[50:53]
	v_mfma_f32_16x16x128_f8f6f4 v[46:49], v[142:149], v[234:241], v[46:49]
	s_nop 3
	s_setprio 0
	s_setprio 1
	v_mfma_f32_16x16x128_f8f6f4 v[42:45], v[150:157], v[210:217], v[42:45]
	v_mfma_f32_16x16x128_f8f6f4 v[38:41], v[202:209], v[210:217], v[38:41]
	v_mfma_f32_16x16x128_f8f6f4 v[34:37], v[150:157], v[218:225], v[34:37]
	v_mfma_f32_16x16x128_f8f6f4 v[30:33], v[202:209], v[218:225], v[30:33]
	v_mfma_f32_16x16x128_f8f6f4 v[26:29], v[150:157], v[226:233], v[26:29]
	v_mfma_f32_16x16x128_f8f6f4 v[22:25], v[202:209], v[226:233], v[22:25]
	v_mfma_f32_16x16x128_f8f6f4 v[18:21], v[150:157], v[234:241], v[18:21]
	v_mfma_f32_16x16x128_f8f6f4 v[14:17], v[202:209], v[234:241], v[14:17]
	s_setprio 0
	s_barrier
; #define PG8_STAGE(bufoff, gbase, voff) do { _Pragma("unroll") for (int _i = 0; _i < 2; ++_i) \
;         __builtin_amdgcn_global_load_lds((const unsigned*)((const char*)(gbase) + (voff)[_i]), (PG8_LAS unsigned*)(lds + (bufoff) + ldsw + _i * 8192), 16, 0, 0); } while (0)
; #define PG8_WAIT_V(n) asm volatile("s_waitcnt vmcnt(" #n ")" ::: "memory")
; #define PG8_WAIT_L(n) asm volatile("s_waitcnt lgkmcnt(" #n ")" ::: "memory")
; #define PG8_BAR __builtin_amdgcn_s_barrier()
; #define PG8_SCHED __builtin_amdgcn_sched_barrier(0)
; template <class Epi, class Sched, bool ALIGN_EPI = true, bool F8 = false>
; __device__ __forceinline__ void gemm_phase(PG8_LAS unsigned char* lds, const Sched& S, const Epi& E) {
;     ...
;             PG8_LDB(B0, 1, 0); PG8_LDB(B1, 1, 1); PG8_SCHED; PG8_LDA(At, 1, 0); PG8_STAGE(PG8_SA(0, 1), a2, vA2[1]);
;             PG8_WAIT_V(8); PG8_WAIT_L(0); PG8_BAR; PG8_MMA(0, 0, At, B0); PG8_MMA(0, 1, At, B1); PG8_BAR; PG8_SCHED;
;             PG8_LDA(At, 1, 1); PG8_STAGE(PG8_SB(1, 0), b3, voffB[0]); PG8_STAGE(PG8_SB(1, 1), b3, voffB[1]); PG8_STAGE(PG8_SA(1, 0), a3, vA2[0]);
;             PG8_WAIT_V(8); PG8_WAIT_L(0); PG8_BAR; PG8_MMA(1, 0, At, B0); PG8_MMA(1, 1, At, B1); PG8_BAR; PG8_SCHED;
	s_add_i32 s78, 0, 0x18000
	s_add_i32 s79, 0, 0x1c000
	v_add_u32_e32 v2, s78, v190
	v_add_u32_e32 v10, s79, v190
	ds_read_b128 v[142:145], v2
	ds_read_b128 v[146:149], v2 offset:1024
	ds_read_b128 v[150:153], v2 offset:2048
	ds_read_b128 v[154:157], v2 offset:3072
	ds_read_b128 v[2:5], v10
	ds_read_b128 v[6:9], v10 offset:1024
	ds_read_b128 v[202:205], v10 offset:2048
	ds_read_b128 v[206:209], v10 offset:3072
	s_mov_b32 m0, s47
	v_lshl_add_u64 v[12:13], s[30:31], 0, v[166:167]
	ds_read_b128 v[210:213], v198 offset:32768
	ds_read_b128 v[214:217], v198 offset:33792
	ds_read_b128 v[218:221], v198 offset:34816
	ds_read_b128 v[222:225], v198 offset:35840
	ds_read_b128 v[226:229], v198 offset:36864
	ds_read_b128 v[230:233], v198 offset:37888
	ds_read_b128 v[234:237], v198 offset:38912
	ds_read_b128 v[238:241], v198 offset:39936
	global_load_lds_dwordx4 v[12:13], off
	v_lshl_add_u64 v[12:13], s[30:31], 0, v[168:169]
	s_mov_b32 m0, s48
	s_nop 0
	global_load_lds_dwordx4 v[12:13], off
	s_waitcnt vmcnt(8)
	s_waitcnt lgkmcnt(0)
	s_setprio 1
	v_mfma_f32_16x16x128_f8f6f4 v[138:141], v[142:149], v[210:217], v[138:141]
	v_mfma_f32_16x16x128_f8f6f4 v[134:137], v[150:157], v[210:217], v[134:137]
	v_mfma_f32_16x16x128_f8f6f4 v[130:133], v[142:149], v[218:225], v[130:133]
	v_mfma_f32_16x16x128_f8f6f4 v[126:129], v[150:157], v[218:225], v[126:129]
	v_mfma_f32_16x16x128_f8f6f4 v[122:125], v[142:149], v[226:233], v[122:125]
	v_mfma_f32_16x16x128_f8f6f4 v[118:121], v[150:157], v[226:233], v[118:121]
	v_mfma_f32_16x16x128_f8f6f4 v[114:117], v[142:149], v[234:241], v[114:117]
	v_mfma_f32_16x16x128_f8f6f4 v[110:113], v[150:157], v[234:241], v[110:113]
	s_nop 3
	s_setprio 0
	s_setprio 1
	v_mfma_f32_16x16x128_f8f6f4 v[106:109], v[2:9], v[210:217], v[106:109]
	v_mfma_f32_16x16x128_f8f6f4 v[102:105], v[202:209], v[210:217], v[102:105]
	v_mfma_f32_16x16x128_f8f6f4 v[98:101], v[2:9], v[218:225], v[98:101]
	v_mfma_f32_16x16x128_f8f6f4 v[94:97], v[202:209], v[218:225], v[94:97]
	v_mfma_f32_16x16x128_f8f6f4 v[90:93], v[2:9], v[226:233], v[90:93]
	v_mfma_f32_16x16x128_f8f6f4 v[86:89], v[202:209], v[226:233], v[86:89]
	v_mfma_f32_16x16x128_f8f6f4 v[82:85], v[2:9], v[234:241], v[82:85]
	v_mfma_f32_16x16x128_f8f6f4 v[78:81], v[202:209], v[234:241], v[78:81]
	s_setprio 0
	s_barrier
	s_add_u32 s28, s28, 0x8000
	s_addc_u32 s29, s29, 0
	s_add_i32 s30, s78, s44
	v_lshl_add_u64 v[12:13], s[28:29], 0, v[158:159]
	s_mov_b32 m0, s30
	ds_read_b128 v[210:213], v198 offset:49152
	ds_read_b128 v[214:217], v198 offset:50176
	ds_read_b128 v[218:221], v198 offset:51200
	ds_read_b128 v[222:225], v198 offset:52224
	ds_read_b128 v[226:229], v198 offset:53248
	ds_read_b128 v[230:233], v198 offset:54272
	ds_read_b128 v[234:237], v198 offset:55296
	ds_read_b128 v[238:241], v198 offset:56320
	global_load_lds_dwordx4 v[12:13], off
	v_lshl_add_u64 v[12:13], s[28:29], 0, v[160:161]
	s_add_i32 m0, s30, 0x2000
	s_add_i32 s30, s79, s44
	global_load_lds_dwordx4 v[12:13], off
	v_lshl_add_u64 v[12:13], s[28:29], 0, v[172:173]
	s_mov_b32 m0, s30
	s_nop 0
	global_load_lds_dwordx4 v[12:13], off
	v_lshl_add_u64 v[12:13], s[28:29], 0, v[174:175]
	s_add_i32 m0, s30, 0x2000
	s_nop 0
	global_load_lds_dwordx4 v[12:13], off
	v_lshl_add_u64 v[12:13], s[26:27], 0, v[162:163]
	s_mov_b32 m0, s50
	s_nop 0
	global_load_lds_dwordx4 v[12:13], off
	v_lshl_add_u64 v[12:13], s[26:27], 0, v[164:165]
	s_mov_b32 m0, s51
	s_nop 0
	global_load_lds_dwordx4 v[12:13], off
	s_waitcnt vmcnt(8)
	s_waitcnt lgkmcnt(0)
	s_setprio 1
	v_mfma_f32_16x16x128_f8f6f4 v[74:77], v[142:149], v[210:217], v[74:77]
	v_mfma_f32_16x16x128_f8f6f4 v[70:73], v[150:157], v[210:217], v[70:73]
	v_mfma_f32_16x16x128_f8f6f4 v[66:69], v[142:149], v[218:225], v[66:69]
	v_mfma_f32_16x16x128_f8f6f4 v[62:65], v[150:157], v[218:225], v[62:65]
	v_mfma_f32_16x16x128_f8f6f4 v[58:61], v[142:149], v[226:233], v[58:61]
	v_mfma_f32_16x16x128_f8f6f4 v[54:57], v[150:157], v[226:233], v[54:57]
	v_mfma_f32_16x16x128_f8f6f4 v[50:53], v[142:149], v[234:241], v[50:53]
	v_mfma_f32_16x16x128_f8f6f4 v[46:49], v[150:157], v[234:241], v[46:49]
	s_nop 3
	s_setprio 0
	s_setprio 1
	v_mfma_f32_16x16x128_f8f6f4 v[42:45], v[2:9], v[210:217], v[42:45]
	v_mfma_f32_16x16x128_f8f6f4 v[38:41], v[202:209], v[210:217], v[38:41]
	v_mfma_f32_16x16x128_f8f6f4 v[34:37], v[2:9], v[218:225], v[34:37]
	v_mfma_f32_16x16x128_f8f6f4 v[30:33], v[202:209], v[218:225], v[30:33]
	v_mfma_f32_16x16x128_f8f6f4 v[26:29], v[2:9], v[226:233], v[26:29]
	v_mfma_f32_16x16x128_f8f6f4 v[22:25], v[202:209], v[226:233], v[22:25]
	v_mfma_f32_16x16x128_f8f6f4 v[18:21], v[2:9], v[234:241], v[18:21]
	v_mfma_f32_16x16x128_f8f6f4 v[14:17], v[202:209], v[234:241], v[14:17]
	s_setprio 0
	s_barrier
	s_add_u32 s75, s75, 0x10000
	s_addc_u32 s76, s76, 0
	s_add_u32 s24, s24, 0x10000
	s_addc_u32 s25, s25, 0
	s_cmp_ge_i32 s77, s72
	s_mov_b32 s26, s77
	s_cbranch_scc0 .LBB0_834
	s_branch .Lfx_23459
; #define PG8_STAGE(bufoff, gbase, voff) do { _Pragma("unroll") for (int _i = 0; _i < 2; ++_i) \
;         __builtin_amdgcn_global_load_lds((const unsigned*)((const char*)(gbase) + (voff)[_i]), (PG8_LAS unsigned*)(lds + (bufoff) + ldsw + _i * 8192), 16, 0, 0); } while (0)
; #define PG8_WAIT_V(n) asm volatile("s_waitcnt vmcnt(" #n ")" ::: "memory")
; #define PG8_WAIT_L(n) asm volatile("s_waitcnt lgkmcnt(" #n ")" ::: "memory")
; #define PG8_BAR __builtin_amdgcn_s_barrier()
; #define PG8_SCHED __builtin_amdgcn_sched_barrier(0)
; template <class Epi, class Sched, bool ALIGN_EPI = true, bool F8 = false>
; __device__ __forceinline__ void gemm_phase(PG8_LAS unsigned char* lds, const Sched& S, const Epi& E) {
;     ...
;             PG8_LDB(B0, 0, 0); PG8_LDB(B1, 0, 1); PG8_SCHED; PG8_LDA(At, 0, 0); PG8_STAGE(PG8_SA(1, 1), a1, voffA[1]);
;             PG8_WAIT_V(8); PG8_WAIT_L(0); PG8_BAR; PG8_MMA(0, 0, At, B0); PG8_MMA(0, 1, At, B1); PG8_BAR; PG8_SCHED;
;             PG8_LDA(At, 0, 1); PG8_STAGE(PG8_SB(0, 0), b2, voffB[0]); PG8_STAGE(PG8_SB(0, 1), b2, voffB[1]); PG8_STAGE(PG8_SA(0, 0), a2, vA2[0]);
;             PG8_WAIT_V(8); PG8_WAIT_L(0); PG8_BAR; PG8_MMA(1, 0, At, B0); PG8_MMA(1, 1, At, B1); PG8_BAR; PG8_SCHED;
;             PG8_LDB(B0, 1, 0); PG8_LDB(B1, 1, 1); PG8_SCHED; PG8_LDA(At, 1, 0); PG8_STAGE(PG8_SA(0, 1), a2, vA2[1]);
;             PG8_WAIT_V(8); PG8_WAIT_L(0); PG8_BAR; PG8_MMA(0, 0, At, B0); PG8_MMA(0, 1, At, B1); PG8_BAR; PG8_SCHED;
.Lh1e_23459:
.Lh1_834:
	v_add_u32_e32 v10, s58, v190
	ds_read_b128 v[2:5], v10
	ds_read_b128 v[6:9], v10 offset:1024
	ds_read_b128 v[142:145], v10 offset:2048
	ds_read_b128 v[146:149], v10 offset:3072
	v_add_u32_e32 v10, s59, v190
	ds_read_b128 v[150:153], v10
	ds_read_b128 v[154:157], v10 offset:1024
	ds_read_b128 v[202:205], v10 offset:2048
	ds_read_b128 v[206:209], v10 offset:3072
	s_add_i32 s77, s26, 2
	s_add_u32 s27, s24, 0x8000
	s_addc_u32 s28, s25, 0
	s_cmp_eq_u32 s74, s26
	s_cselect_b32 s30, s20, s27
	s_cselect_b32 s31, s21, s28
	s_cselect_b32 s28, s22, s75
	s_cselect_b32 s29, s23, s76
	s_add_u32 s26, s30, 0x8000
	s_addc_u32 s27, s31, 0
	v_lshl_add_u64 v[12:13], s[24:25], 0, v[182:183]
	s_add_i32 m0, s45, 0xc000
	ds_read_b128 v[210:213], v198
	ds_read_b128 v[214:217], v198 offset:1024
	ds_read_b128 v[218:221], v198 offset:2048
	ds_read_b128 v[222:225], v198 offset:3072
	ds_read_b128 v[226:229], v198 offset:4096
	ds_read_b128 v[230:233], v198 offset:5120
	ds_read_b128 v[234:237], v198 offset:6144
	ds_read_b128 v[238:241], v198 offset:7168
	global_load_lds_dwordx4 v[12:13], off
	v_lshl_add_u64 v[12:13], s[24:25], 0, v[180:181]
	s_add_i32 m0, s45, 0xe000
	s_nop 0
	global_load_lds_dwordx4 v[12:13], off
	s_waitcnt vmcnt(8)
	s_waitcnt lgkmcnt(0)
	s_barrier
	s_setprio 2
	v_mfma_f32_16x16x128_f8f6f4 v[138:141], v[2:9], v[210:217], v[138:141]
	v_mfma_f32_16x16x128_f8f6f4 v[134:137], v[142:149], v[210:217], v[134:137]
	v_mfma_f32_16x16x128_f8f6f4 v[130:133], v[2:9], v[218:225], v[130:133]
	v_mfma_f32_16x16x128_f8f6f4 v[126:129], v[142:149], v[218:225], v[126:129]
	v_mfma_f32_16x16x128_f8f6f4 v[122:125], v[2:9], v[226:233], v[122:125]
	v_mfma_f32_16x16x128_f8f6f4 v[118:121], v[142:149], v[226:233], v[118:121]
	v_mfma_f32_16x16x128_f8f6f4 v[114:117], v[2:9], v[234:241], v[114:117]
	v_mfma_f32_16x16x128_f8f6f4 v[110:113], v[142:149], v[234:241], v[110:113]
	s_nop 3
	s_setprio 0
	s_setprio 2
	v_mfma_f32_16x16x128_f8f6f4 v[106:109], v[150:157], v[210:217], v[106:109]
	v_mfma_f32_16x16x128_f8f6f4 v[102:105], v[202:209], v[210:217], v[102:105]
	v_mfma_f32_16x16x128_f8f6f4 v[98:101], v[150:157], v[218:225], v[98:101]
	v_mfma_f32_16x16x128_f8f6f4 v[94:97], v[202:209], v[218:225], v[94:97]
	v_mfma_f32_16x16x128_f8f6f4 v[90:93], v[150:157], v[226:233], v[90:93]
	v_mfma_f32_16x16x128_f8f6f4 v[86:89], v[202:209], v[226:233], v[86:89]
	v_mfma_f32_16x16x128_f8f6f4 v[82:85], v[150:157], v[234:241], v[82:85]
	v_mfma_f32_16x16x128_f8f6f4 v[78:81], v[202:209], v[234:241], v[78:81]
	s_setprio 0
	s_add_i32 s78, s58, s44
	v_lshl_add_u64 v[12:13], s[28:29], 0, v[158:159]
	s_mov_b32 m0, s78
	ds_read_b128 v[210:213], v198 offset:16384
	ds_read_b128 v[214:217], v198 offset:17408
	ds_read_b128 v[218:221], v198 offset:18432
	ds_read_b128 v[222:225], v198 offset:19456
	ds_read_b128 v[226:229], v198 offset:20480
	ds_read_b128 v[230:233], v198 offset:21504
	ds_read_b128 v[234:237], v198 offset:22528
	ds_read_b128 v[238:241], v198 offset:23552
	global_load_lds_dwordx4 v[12:13], off
	v_lshl_add_u64 v[188:189], s[28:29], 0, v[160:161]
	s_add_i32 m0, s78, 0x2000
	s_add_i32 s78, s59, s44
	global_load_lds_dwordx4 v[188:189], off
	v_lshl_add_u64 v[12:13], v[12:13], 0, s[8:9]
	s_mov_b32 m0, s78
	s_nop 0
	global_load_lds_dwordx4 v[12:13], off
	v_lshl_add_u64 v[12:13], v[188:189], 0, s[8:9]
	s_add_i32 m0, s78, 0x2000
	s_nop 0
	global_load_lds_dwordx4 v[12:13], off
	v_lshl_add_u64 v[12:13], s[30:31], 0, v[162:163]
	s_mov_b32 m0, s45
	s_nop 0
	global_load_lds_dwordx4 v[12:13], off
	v_lshl_add_u64 v[12:13], s[30:31], 0, v[164:165]
	s_mov_b32 m0, s46
	s_nop 0
	global_load_lds_dwordx4 v[12:13], off
	s_waitcnt vmcnt(8)
	s_waitcnt lgkmcnt(0)
	s_barrier
	s_setprio 2
	v_mfma_f32_16x16x128_f8f6f4 v[74:77], v[2:9], v[210:217], v[74:77]
	v_mfma_f32_16x16x128_f8f6f4 v[70:73], v[142:149], v[210:217], v[70:73]
	v_mfma_f32_16x16x128_f8f6f4 v[66:69], v[2:9], v[218:225], v[66:69]
	v_mfma_f32_16x16x128_f8f6f4 v[62:65], v[142:149], v[218:225], v[62:65]
	v_mfma_f32_16x16x128_f8f6f4 v[58:61], v[2:9], v[226:233], v[58:61]
	v_mfma_f32_16x16x128_f8f6f4 v[54:57], v[142:149], v[226:233], v[54:57]
	v_mfma_f32_16x16x128_f8f6f4 v[50:53], v[2:9], v[234:241], v[50:53]
	v_mfma_f32_16x16x128_f8f6f4 v[46:49], v[142:149], v[234:241], v[46:49]
	s_nop 3
	s_setprio 0
	s_setprio 2
	v_mfma_f32_16x16x128_f8f6f4 v[42:45], v[150:157], v[210:217], v[42:45]
	v_mfma_f32_16x16x128_f8f6f4 v[38:41], v[202:209], v[210:217], v[38:41]
	v_mfma_f32_16x16x128_f8f6f4 v[34:37], v[150:157], v[218:225], v[34:37]
	v_mfma_f32_16x16x128_f8f6f4 v[30:33], v[202:209], v[218:225], v[30:33]
	v_mfma_f32_16x16x128_f8f6f4 v[26:29], v[150:157], v[226:233], v[26:29]
	v_mfma_f32_16x16x128_f8f6f4 v[22:25], v[202:209], v[226:233], v[22:25]
	v_mfma_f32_16x16x128_f8f6f4 v[18:21], v[150:157], v[234:241], v[18:21]
	v_mfma_f32_16x16x128_f8f6f4 v[14:17], v[202:209], v[234:241], v[14:17]
	s_setprio 0
	s_add_i32 s78, 0, 0x18000
	s_add_i32 s79, 0, 0x1c000
	v_add_u32_e32 v2, s78, v190
	v_add_u32_e32 v10, s79, v190
	ds_read_b128 v[142:145], v2
	ds_read_b128 v[146:149], v2 offset:1024
	ds_read_b128 v[150:153], v2 offset:2048
	ds_read_b128 v[154:157], v2 offset:3072
	ds_read_b128 v[2:5], v10
	ds_read_b128 v[6:9], v10 offset:1024
	ds_read_b128 v[202:205], v10 offset:2048
	ds_read_b128 v[206:209], v10 offset:3072
	s_mov_b32 m0, s47
	v_lshl_add_u64 v[12:13], s[30:31], 0, v[166:167]
	ds_read_b128 v[210:213], v198 offset:32768
	ds_read_b128 v[214:217], v198 offset:33792
	ds_read_b128 v[218:221], v198 offset:34816
	ds_read_b128 v[222:225], v198 offset:35840
	ds_read_b128 v[226:229], v198 offset:36864
	ds_read_b128 v[230:233], v198 offset:37888
	ds_read_b128 v[234:237], v198 offset:38912
	ds_read_b128 v[238:241], v198 offset:39936
	global_load_lds_dwordx4 v[12:13], off
	v_lshl_add_u64 v[12:13], s[30:31], 0, v[168:169]
	s_mov_b32 m0, s48
	s_nop 0
	global_load_lds_dwordx4 v[12:13], off
	s_waitcnt vmcnt(8)
	s_waitcnt lgkmcnt(0)
	s_barrier
; #define PG8_STAGE(bufoff, gbase, voff) do { _Pragma("unroll") for (int _i = 0; _i < 2; ++_i) \
;         __builtin_amdgcn_global_load_lds((const unsigned*)((const char*)(gbase) + (voff)[_i]), (PG8_LAS unsigned*)(lds + (bufoff) + ldsw + _i * 8192), 16, 0, 0); } while (0)
; #define PG8_WAIT_V(n) asm volatile("s_waitcnt vmcnt(" #n ")" ::: "memory")
; #define PG8_WAIT_L(n) asm volatile("s_waitcnt lgkmcnt(" #n ")" ::: "memory")
; #define PG8_BAR __builtin_amdgcn_s_barrier()
; #define PG8_SCHED __builtin_amdgcn_sched_barrier(0)
; template <class Epi, class Sched, bool ALIGN_EPI = true, bool F8 = false>
; __device__ __forceinline__ void gemm_phase(PG8_LAS unsigned char* lds, const Sched& S, const Epi& E) {
;     ...
;             PG8_WAIT_V(8); PG8_WAIT_L(0); PG8_BAR; PG8_MMA(0, 0, At, B0); PG8_MMA(0, 1, At, B1); PG8_BAR; PG8_SCHED;
;             PG8_LDA(At, 1, 1); PG8_STAGE(PG8_SB(1, 0), b3, voffB[0]); PG8_STAGE(PG8_SB(1, 1), b3, voffB[1]); PG8_STAGE(PG8_SA(1, 0), a3, vA2[0]);
;             PG8_WAIT_V(8); PG8_WAIT_L(0); PG8_BAR; PG8_MMA(1, 0, At, B0); PG8_MMA(1, 1, At, B1); PG8_BAR; PG8_SCHED;
	s_setprio 2
	v_mfma_f32_16x16x128_f8f6f4 v[138:141], v[142:149], v[210:217], v[138:141]
	v_mfma_f32_16x16x128_f8f6f4 v[134:137], v[150:157], v[210:217], v[134:137]
	v_mfma_f32_16x16x128_f8f6f4 v[130:133], v[142:149], v[218:225], v[130:133]
	v_mfma_f32_16x16x128_f8f6f4 v[126:129], v[150:157], v[218:225], v[126:129]
	v_mfma_f32_16x16x128_f8f6f4 v[122:125], v[142:149], v[226:233], v[122:125]
	v_mfma_f32_16x16x128_f8f6f4 v[118:121], v[150:157], v[226:233], v[118:121]
	v_mfma_f32_16x16x128_f8f6f4 v[114:117], v[142:149], v[234:241], v[114:117]
	v_mfma_f32_16x16x128_f8f6f4 v[110:113], v[150:157], v[234:241], v[110:113]
	s_nop 3
	s_setprio 0
	s_setprio 2
	v_mfma_f32_16x16x128_f8f6f4 v[106:109], v[2:9], v[210:217], v[106:109]
	v_mfma_f32_16x16x128_f8f6f4 v[102:105], v[202:209], v[210:217], v[102:105]
	v_mfma_f32_16x16x128_f8f6f4 v[98:101], v[2:9], v[218:225], v[98:101]
	v_mfma_f32_16x16x128_f8f6f4 v[94:97], v[202:209], v[218:225], v[94:97]
	v_mfma_f32_16x16x128_f8f6f4 v[90:93], v[2:9], v[226:233], v[90:93]
	v_mfma_f32_16x16x128_f8f6f4 v[86:89], v[202:209], v[226:233], v[86:89]
	v_mfma_f32_16x16x128_f8f6f4 v[82:85], v[2:9], v[234:241], v[82:85]
	v_mfma_f32_16x16x128_f8f6f4 v[78:81], v[202:209], v[234:241], v[78:81]
	s_setprio 0
	s_add_u32 s28, s28, 0x8000
	s_addc_u32 s29, s29, 0
	s_add_i32 s30, s78, s44
	v_lshl_add_u64 v[12:13], s[28:29], 0, v[158:159]
	s_mov_b32 m0, s30
	ds_read_b128 v[210:213], v198 offset:49152
	ds_read_b128 v[214:217], v198 offset:50176
	ds_read_b128 v[218:221], v198 offset:51200
	ds_read_b128 v[222:225], v198 offset:52224
	ds_read_b128 v[226:229], v198 offset:53248
	ds_read_b128 v[230:233], v198 offset:54272
	ds_read_b128 v[234:237], v198 offset:55296
	ds_read_b128 v[238:241], v198 offset:56320
	global_load_lds_dwordx4 v[12:13], off
	v_lshl_add_u64 v[12:13], s[28:29], 0, v[160:161]
	s_add_i32 m0, s30, 0x2000
	s_add_i32 s30, s79, s44
	global_load_lds_dwordx4 v[12:13], off
	v_lshl_add_u64 v[12:13], s[28:29], 0, v[172:173]
	s_mov_b32 m0, s30
	s_nop 0
	global_load_lds_dwordx4 v[12:13], off
	v_lshl_add_u64 v[12:13], s[28:29], 0, v[174:175]
	s_add_i32 m0, s30, 0x2000
	s_nop 0
	global_load_lds_dwordx4 v[12:13], off
	v_lshl_add_u64 v[12:13], s[26:27], 0, v[162:163]
	s_mov_b32 m0, s50
	s_nop 0
	global_load_lds_dwordx4 v[12:13], off
	v_lshl_add_u64 v[12:13], s[26:27], 0, v[164:165]
	s_mov_b32 m0, s51
	s_nop 0
	global_load_lds_dwordx4 v[12:13], off
	s_waitcnt vmcnt(8)
	s_waitcnt lgkmcnt(0)
	s_barrier
	s_setprio 2
	v_mfma_f32_16x16x128_f8f6f4 v[74:77], v[142:149], v[210:217], v[74:77]
	v_mfma_f32_16x16x128_f8f6f4 v[70:73], v[150:157], v[210:217], v[70:73]
	v_mfma_f32_16x16x128_f8f6f4 v[66:69], v[142:149], v[218:225], v[66:69]
	v_mfma_f32_16x16x128_f8f6f4 v[62:65], v[150:157], v[218:225], v[62:65]
	v_mfma_f32_16x16x128_f8f6f4 v[58:61], v[142:149], v[226:233], v[58:61]
	v_mfma_f32_16x16x128_f8f6f4 v[54:57], v[150:157], v[226:233], v[54:57]
	v_mfma_f32_16x16x128_f8f6f4 v[50:53], v[142:149], v[234:241], v[50:53]
	v_mfma_f32_16x16x128_f8f6f4 v[46:49], v[150:157], v[234:241], v[46:49]
	s_nop 3
	s_setprio 0
	s_setprio 2
	v_mfma_f32_16x16x128_f8f6f4 v[42:45], v[2:9], v[210:217], v[42:45]
	v_mfma_f32_16x16x128_f8f6f4 v[38:41], v[202:209], v[210:217], v[38:41]
	v_mfma_f32_16x16x128_f8f6f4 v[34:37], v[2:9], v[218:225], v[34:37]
	v_mfma_f32_16x16x128_f8f6f4 v[30:33], v[202:209], v[218:225], v[30:33]
	v_mfma_f32_16x16x128_f8f6f4 v[26:29], v[2:9], v[226:233], v[26:29]
	v_mfma_f32_16x16x128_f8f6f4 v[22:25], v[202:209], v[226:233], v[22:25]
	v_mfma_f32_16x16x128_f8f6f4 v[18:21], v[2:9], v[234:241], v[18:21]
	v_mfma_f32_16x16x128_f8f6f4 v[14:17], v[202:209], v[234:241], v[14:17]
	s_setprio 0
	s_add_u32 s75, s75, 0x10000
	s_addc_u32 s76, s76, 0
	s_add_u32 s24, s24, 0x10000
	s_addc_u32 s25, s25, 0
	s_cmp_ge_i32 s77, s72
	s_mov_b32 s26, s77
	s_cbranch_scc0 .Lh1_834

; #define PG8_STAGE(bufoff, gbase, voff) do { _Pragma("unroll") for (int _i = 0; _i < 2; ++_i) \
;         __builtin_amdgcn_global_load_lds((const unsigned*)((const char*)(gbase) + (voff)[_i]), (PG8_LAS unsigned*)(lds + (bufoff) + ldsw + _i * 8192), 16, 0, 0); } while (0)
; #define PG8_WAIT_V(n) asm volatile("s_waitcnt vmcnt(" #n ")" ::: "memory")
; #define PG8_WAIT_L(n) asm volatile("s_waitcnt lgkmcnt(" #n ")" ::: "memory")
; #define PG8_BAR __builtin_amdgcn_s_barrier()
; #define PG8_SCHED __builtin_amdgcn_sched_barrier(0)
; template <class Epi, class Sched, bool ALIGN_EPI = true, bool F8 = false>
; __device__ __forceinline__ void gemm_phase(PG8_LAS unsigned char* lds, const Sched& S, const Epi& E) {
;     ...
;             PG8_LDB(B0, 0, 0); PG8_LDB(B1, 0, 1); PG8_SCHED; PG8_LDA(At, 0, 0); PG8_STAGE(PG8_SA(1, 1), a1, voffA[1]);
;             PG8_WAIT_V(8); PG8_WAIT_L(0); PG8_BAR; PG8_MMA(0, 0, At, B0); PG8_MMA(0, 1, At, B1); PG8_BAR; PG8_SCHED;
;             PG8_LDA(At, 0, 1); PG8_STAGE(PG8_SB(0, 0), b2, voffB[0]); PG8_STAGE(PG8_SB(0, 1), b2, voffB[1]); PG8_STAGE(PG8_SA(0, 0), a2, vA2[0]);
;             PG8_WAIT_V(8); PG8_WAIT_L(0); PG8_BAR; PG8_MMA(1, 0, At, B0); PG8_MMA(1, 1, At, B1); PG8_BAR; PG8_SCHED;
.LBB0_911:
	ds_read_b128 v[18:21], v191
	ds_read_b128 v[22:25], v191 offset:1024
	ds_read_b128 v[26:29], v191 offset:2048
	ds_read_b128 v[30:33], v191 offset:3072
	ds_read_b128 v[2:5], v192
	ds_read_b128 v[6:9], v192 offset:1024
	ds_read_b128 v[10:13], v192 offset:2048
	ds_read_b128 v[14:17], v192 offset:3072
	s_add_u32 s30, s28, 0x8000
	s_addc_u32 s31, s29, 0
	s_cmp_eq_u32 s65, 12
	s_cselect_b32 s42, s22, s30
	s_cselect_b32 s43, s23, s31
	s_cselect_b32 s40, s24, s19
	s_cselect_b32 s41, s25, s21
	s_add_u32 s30, s42, 0x8000
	s_addc_u32 s31, s43, 0
	v_lshl_add_u64 v[228:229], s[28:29], 0, v[182:183]
	s_add_i32 m0, s27, 0xc000
	ds_read_b128 v[196:199], v193
	ds_read_b128 v[200:203], v193 offset:1024
	ds_read_b128 v[204:207], v193 offset:2048
	ds_read_b128 v[208:211], v193 offset:3072
	ds_read_b128 v[212:215], v193 offset:4096
	ds_read_b128 v[216:219], v193 offset:5120
	ds_read_b128 v[220:223], v193 offset:6144
	ds_read_b128 v[224:227], v193 offset:7168
	global_load_lds_dwordx4 v[228:229], off
	v_lshl_add_u64 v[228:229], s[28:29], 0, v[180:181]
	s_add_i32 m0, s27, 0xe000
	s_nop 0
	global_load_lds_dwordx4 v[228:229], off
	s_waitcnt vmcnt(8)
	s_waitcnt lgkmcnt(0)
	s_setprio 1
	v_mfma_f32_16x16x128_f8f6f4 v[158:161], v[18:25], v[196:203], v[158:161]
	v_mfma_f32_16x16x128_f8f6f4 v[154:157], v[26:33], v[196:203], v[154:157]
	v_mfma_f32_16x16x128_f8f6f4 v[150:153], v[18:25], v[204:211], v[150:153]
	v_mfma_f32_16x16x128_f8f6f4 v[146:149], v[26:33], v[204:211], v[146:149]
	v_mfma_f32_16x16x128_f8f6f4 v[130:133], v[18:25], v[212:219], v[130:133]
	v_mfma_f32_16x16x128_f8f6f4 v[122:125], v[26:33], v[212:219], v[122:125]
	v_mfma_f32_16x16x128_f8f6f4 v[114:117], v[18:25], v[220:227], v[114:117]
	v_mfma_f32_16x16x128_f8f6f4 v[106:109], v[26:33], v[220:227], v[106:109]
	s_nop 3
	s_setprio 0
	s_setprio 1
	v_mfma_f32_16x16x128_f8f6f4 v[142:145], v[2:9], v[196:203], v[142:145]
	v_mfma_f32_16x16x128_f8f6f4 v[138:141], v[10:17], v[196:203], v[138:141]
	v_mfma_f32_16x16x128_f8f6f4 v[134:137], v[2:9], v[204:211], v[134:137]
	v_mfma_f32_16x16x128_f8f6f4 v[126:129], v[10:17], v[204:211], v[126:129]
	v_mfma_f32_16x16x128_f8f6f4 v[118:121], v[2:9], v[212:219], v[118:121]
	v_mfma_f32_16x16x128_f8f6f4 v[110:113], v[10:17], v[212:219], v[110:113]
	v_mfma_f32_16x16x128_f8f6f4 v[102:105], v[2:9], v[220:227], v[102:105]
	v_mfma_f32_16x16x128_f8f6f4 v[98:101], v[10:17], v[220:227], v[98:101]
	s_setprio 0
	s_barrier
	s_add_i32 s66, s60, s48
	v_lshl_add_u64 v[228:229], s[40:41], 0, v[162:163]
	s_mov_b32 m0, s66
	ds_read_b128 v[196:199], v193 offset:16384
	ds_read_b128 v[200:203], v193 offset:17408
	ds_read_b128 v[204:207], v193 offset:18432
	ds_read_b128 v[208:211], v193 offset:19456
	ds_read_b128 v[212:215], v193 offset:20480
	ds_read_b128 v[216:219], v193 offset:21504
	ds_read_b128 v[220:223], v193 offset:22528
	ds_read_b128 v[224:227], v193 offset:23552
	global_load_lds_dwordx4 v[228:229], off
	v_lshl_add_u64 v[230:231], s[40:41], 0, v[164:165]
	s_add_i32 m0, s66, 0x2000
	s_add_i32 s66, s61, s48
	global_load_lds_dwordx4 v[230:231], off
	v_lshl_add_u64 v[228:229], v[228:229], 0, s[6:7]
	s_mov_b32 m0, s66
	s_nop 0
	global_load_lds_dwordx4 v[228:229], off
	v_lshl_add_u64 v[228:229], v[230:231], 0, s[6:7]
	s_add_i32 m0, s66, 0x2000
	s_nop 0
	global_load_lds_dwordx4 v[228:229], off
	v_lshl_add_u64 v[228:229], s[42:43], 0, v[166:167]
	s_mov_b32 m0, s27
	s_nop 0
	global_load_lds_dwordx4 v[228:229], off
	v_lshl_add_u64 v[228:229], s[42:43], 0, v[168:169]
	s_mov_b32 m0, s49
	s_nop 0
	global_load_lds_dwordx4 v[228:229], off
	s_waitcnt vmcnt(8)
	s_waitcnt lgkmcnt(0)
	s_setprio 1
	v_mfma_f32_16x16x128_f8f6f4 v[94:97], v[18:25], v[196:203], v[94:97]
	v_mfma_f32_16x16x128_f8f6f4 v[90:93], v[26:33], v[196:203], v[90:93]
	v_mfma_f32_16x16x128_f8f6f4 v[82:85], v[18:25], v[204:211], v[82:85]
	v_mfma_f32_16x16x128_f8f6f4 v[74:77], v[26:33], v[204:211], v[74:77]
	v_mfma_f32_16x16x128_f8f6f4 v[66:69], v[18:25], v[212:219], v[66:69]
	v_mfma_f32_16x16x128_f8f6f4 v[58:61], v[26:33], v[212:219], v[58:61]
	v_mfma_f32_16x16x128_f8f6f4 v[50:53], v[18:25], v[220:227], v[50:53]
	v_mfma_f32_16x16x128_f8f6f4 v[42:45], v[26:33], v[220:227], v[42:45]
	s_nop 3
	s_setprio 0
	s_setprio 1
	v_mfma_f32_16x16x128_f8f6f4 v[86:89], v[2:9], v[196:203], v[86:89]
	v_mfma_f32_16x16x128_f8f6f4 v[78:81], v[10:17], v[196:203], v[78:81]
	v_mfma_f32_16x16x128_f8f6f4 v[70:73], v[2:9], v[204:211], v[70:73]
	v_mfma_f32_16x16x128_f8f6f4 v[62:65], v[10:17], v[204:211], v[62:65]
	v_mfma_f32_16x16x128_f8f6f4 v[54:57], v[2:9], v[212:219], v[54:57]
	v_mfma_f32_16x16x128_f8f6f4 v[46:49], v[10:17], v[212:219], v[46:49]
	v_mfma_f32_16x16x128_f8f6f4 v[38:41], v[2:9], v[220:227], v[38:41]
	v_mfma_f32_16x16x128_f8f6f4 v[34:37], v[10:17], v[220:227], v[34:37]
	s_setprio 0
	s_barrier
; #define PG8_STAGE(bufoff, gbase, voff) do { _Pragma("unroll") for (int _i = 0; _i < 2; ++_i) \
;         __builtin_amdgcn_global_load_lds((const unsigned*)((const char*)(gbase) + (voff)[_i]), (PG8_LAS unsigned*)(lds + (bufoff) + ldsw + _i * 8192), 16, 0, 0); } while (0)
; #define PG8_WAIT_V(n) asm volatile("s_waitcnt vmcnt(" #n ")" ::: "memory")
; #define PG8_WAIT_L(n) asm volatile("s_waitcnt lgkmcnt(" #n ")" ::: "memory")
; #define PG8_BAR __builtin_amdgcn_s_barrier()
; #define PG8_SCHED __builtin_amdgcn_sched_barrier(0)
; template <class Epi, class Sched, bool ALIGN_EPI = true, bool F8 = false>
; __device__ __forceinline__ void gemm_phase(PG8_LAS unsigned char* lds, const Sched& S, const Epi& E) {
;     ...
;             PG8_LDB(B0, 1, 0); PG8_LDB(B1, 1, 1); PG8_SCHED; PG8_LDA(At, 1, 0); PG8_STAGE(PG8_SA(0, 1), a2, vA2[1]);
;             PG8_WAIT_V(8); PG8_WAIT_L(0); PG8_BAR; PG8_MMA(0, 0, At, B0); PG8_MMA(0, 1, At, B1); PG8_BAR; PG8_SCHED;
;             PG8_LDA(At, 1, 1); PG8_STAGE(PG8_SB(1, 0), b3, voffB[0]); PG8_STAGE(PG8_SB(1, 1), b3, voffB[1]); PG8_STAGE(PG8_SA(1, 0), a3, vA2[0]);
;             PG8_WAIT_V(8); PG8_WAIT_L(0); PG8_BAR; PG8_MMA(1, 0, At, B0); PG8_MMA(1, 1, At, B1); PG8_BAR; PG8_SCHED;
	s_add_i32 s66, 0, 0x18000
	s_add_i32 s67, 0, 0x1c000
	v_add_u32_e32 v14, s66, v189
	v_add_u32_e32 v30, s67, v189
	ds_read_b128 v[2:5], v14
	ds_read_b128 v[6:9], v14 offset:1024
	ds_read_b128 v[10:13], v14 offset:2048
	ds_read_b128 v[14:17], v14 offset:3072
	ds_read_b128 v[18:21], v30
	ds_read_b128 v[22:25], v30 offset:1024
	ds_read_b128 v[26:29], v30 offset:2048
	ds_read_b128 v[30:33], v30 offset:3072
	s_mov_b32 m0, s50
	v_lshl_add_u64 v[228:229], s[42:43], 0, v[172:173]
	ds_read_b128 v[196:199], v193 offset:32768
	ds_read_b128 v[200:203], v193 offset:33792
	ds_read_b128 v[204:207], v193 offset:34816
	ds_read_b128 v[208:211], v193 offset:35840
	ds_read_b128 v[212:215], v193 offset:36864
	ds_read_b128 v[216:219], v193 offset:37888
	ds_read_b128 v[220:223], v193 offset:38912
	ds_read_b128 v[224:227], v193 offset:39936
	global_load_lds_dwordx4 v[228:229], off
	v_lshl_add_u64 v[228:229], s[42:43], 0, v[174:175]
	s_mov_b32 m0, s51
	s_nop 0
	global_load_lds_dwordx4 v[228:229], off
	s_waitcnt vmcnt(8)
	s_waitcnt lgkmcnt(0)
	s_setprio 1
	v_mfma_f32_16x16x128_f8f6f4 v[158:161], v[2:9], v[196:203], v[158:161]
	v_mfma_f32_16x16x128_f8f6f4 v[154:157], v[10:17], v[196:203], v[154:157]
	v_mfma_f32_16x16x128_f8f6f4 v[150:153], v[2:9], v[204:211], v[150:153]
	v_mfma_f32_16x16x128_f8f6f4 v[146:149], v[10:17], v[204:211], v[146:149]
	v_mfma_f32_16x16x128_f8f6f4 v[130:133], v[2:9], v[212:219], v[130:133]
	v_mfma_f32_16x16x128_f8f6f4 v[122:125], v[10:17], v[212:219], v[122:125]
	v_mfma_f32_16x16x128_f8f6f4 v[114:117], v[2:9], v[220:227], v[114:117]
	v_mfma_f32_16x16x128_f8f6f4 v[106:109], v[10:17], v[220:227], v[106:109]
	s_nop 3
	s_setprio 0
	s_setprio 1
	v_mfma_f32_16x16x128_f8f6f4 v[142:145], v[18:25], v[196:203], v[142:145]
	v_mfma_f32_16x16x128_f8f6f4 v[138:141], v[26:33], v[196:203], v[138:141]
	v_mfma_f32_16x16x128_f8f6f4 v[134:137], v[18:25], v[204:211], v[134:137]
	v_mfma_f32_16x16x128_f8f6f4 v[126:129], v[26:33], v[204:211], v[126:129]
	v_mfma_f32_16x16x128_f8f6f4 v[118:121], v[18:25], v[212:219], v[118:121]
	v_mfma_f32_16x16x128_f8f6f4 v[110:113], v[26:33], v[212:219], v[110:113]
	v_mfma_f32_16x16x128_f8f6f4 v[102:105], v[18:25], v[220:227], v[102:105]
	v_mfma_f32_16x16x128_f8f6f4 v[98:101], v[26:33], v[220:227], v[98:101]
	s_setprio 0
	s_barrier
	s_add_u32 s40, s40, 0x8000
	s_addc_u32 s41, s41, 0
	s_add_i32 s42, s66, s48
	v_lshl_add_u64 v[228:229], s[40:41], 0, v[162:163]
	s_mov_b32 m0, s42
	ds_read_b128 v[196:199], v193 offset:49152
	ds_read_b128 v[200:203], v193 offset:50176
	ds_read_b128 v[204:207], v193 offset:51200
	ds_read_b128 v[208:211], v193 offset:52224
	ds_read_b128 v[212:215], v193 offset:53248
	ds_read_b128 v[216:219], v193 offset:54272
	ds_read_b128 v[220:223], v193 offset:55296
	ds_read_b128 v[224:227], v193 offset:56320
	global_load_lds_dwordx4 v[228:229], off
	v_lshl_add_u64 v[228:229], s[40:41], 0, v[164:165]
	s_add_i32 m0, s42, 0x2000
	s_add_i32 s42, s67, s48
	global_load_lds_dwordx4 v[228:229], off
	v_lshl_add_u64 v[228:229], s[40:41], 0, v[176:177]
	s_mov_b32 m0, s42
	s_nop 0
	global_load_lds_dwordx4 v[228:229], off
	v_lshl_add_u64 v[228:229], s[40:41], 0, v[178:179]
	s_add_i32 m0, s42, 0x2000
	s_nop 0
	global_load_lds_dwordx4 v[228:229], off
	v_lshl_add_u64 v[228:229], s[30:31], 0, v[166:167]
	s_mov_b32 m0, s53
	s_nop 0
	global_load_lds_dwordx4 v[228:229], off
	v_lshl_add_u64 v[228:229], s[30:31], 0, v[168:169]
	s_mov_b32 m0, s58
	s_nop 0
	global_load_lds_dwordx4 v[228:229], off
	s_waitcnt vmcnt(8)
	s_waitcnt lgkmcnt(0)
	s_setprio 1
	v_mfma_f32_16x16x128_f8f6f4 v[94:97], v[2:9], v[196:203], v[94:97]
	v_mfma_f32_16x16x128_f8f6f4 v[90:93], v[10:17], v[196:203], v[90:93]
	v_mfma_f32_16x16x128_f8f6f4 v[82:85], v[2:9], v[204:211], v[82:85]
	v_mfma_f32_16x16x128_f8f6f4 v[74:77], v[10:17], v[204:211], v[74:77]
	v_mfma_f32_16x16x128_f8f6f4 v[66:69], v[2:9], v[212:219], v[66:69]
	v_mfma_f32_16x16x128_f8f6f4 v[58:61], v[10:17], v[212:219], v[58:61]
	v_mfma_f32_16x16x128_f8f6f4 v[50:53], v[2:9], v[220:227], v[50:53]
	v_mfma_f32_16x16x128_f8f6f4 v[42:45], v[10:17], v[220:227], v[42:45]
	s_nop 3
	s_setprio 0
	s_setprio 1
	v_mfma_f32_16x16x128_f8f6f4 v[86:89], v[18:25], v[196:203], v[86:89]
	v_mfma_f32_16x16x128_f8f6f4 v[78:81], v[26:33], v[196:203], v[78:81]
	v_mfma_f32_16x16x128_f8f6f4 v[70:73], v[18:25], v[204:211], v[70:73]
	v_mfma_f32_16x16x128_f8f6f4 v[62:65], v[26:33], v[204:211], v[62:65]
	v_mfma_f32_16x16x128_f8f6f4 v[54:57], v[18:25], v[212:219], v[54:57]
	v_mfma_f32_16x16x128_f8f6f4 v[46:49], v[26:33], v[212:219], v[46:49]
	v_mfma_f32_16x16x128_f8f6f4 v[38:41], v[18:25], v[220:227], v[38:41]
	v_mfma_f32_16x16x128_f8f6f4 v[34:37], v[26:33], v[220:227], v[34:37]
	s_setprio 0
	s_barrier
	s_add_i32 s65, s65, 2
	s_add_u32 s19, s19, 0x10000
	s_addc_u32 s21, s21, 0
	s_add_u32 s28, s28, 0x10000
	s_addc_u32 s29, s29, 0
	s_cmp_gt_u32 s65, 13
	s_cbranch_scc0 .LBB0_911
	s_branch .Lfx_26630
; #define PG8_STAGE(bufoff, gbase, voff) do { _Pragma("unroll") for (int _i = 0; _i < 2; ++_i) \
;         __builtin_amdgcn_global_load_lds((const unsigned*)((const char*)(gbase) + (voff)[_i]), (PG8_LAS unsigned*)(lds + (bufoff) + ldsw + _i * 8192), 16, 0, 0); } while (0)
; #define PG8_WAIT_V(n) asm volatile("s_waitcnt vmcnt(" #n ")" ::: "memory")
; #define PG8_WAIT_L(n) asm volatile("s_waitcnt lgkmcnt(" #n ")" ::: "memory")
; #define PG8_BAR __builtin_amdgcn_s_barrier()
; #define PG8_SCHED __builtin_amdgcn_sched_barrier(0)
; template <class Epi, class Sched, bool ALIGN_EPI = true, bool F8 = false>
; __device__ __forceinline__ void gemm_phase(PG8_LAS unsigned char* lds, const Sched& S, const Epi& E) {
;     ...
;             PG8_LDB(B0, 0, 0); PG8_LDB(B1, 0, 1); PG8_SCHED; PG8_LDA(At, 0, 0); PG8_STAGE(PG8_SA(1, 1), a1, voffA[1]);
;             PG8_WAIT_V(8); PG8_WAIT_L(0); PG8_BAR; PG8_MMA(0, 0, At, B0); PG8_MMA(0, 1, At, B1); PG8_BAR; PG8_SCHED;
;             PG8_LDA(At, 0, 1); PG8_STAGE(PG8_SB(0, 0), b2, voffB[0]); PG8_STAGE(PG8_SB(0, 1), b2, voffB[1]); PG8_STAGE(PG8_SA(0, 0), a2, vA2[0]);
;             PG8_WAIT_V(8); PG8_WAIT_L(0); PG8_BAR; PG8_MMA(1, 0, At, B0); PG8_MMA(1, 1, At, B1); PG8_BAR; PG8_SCHED;
;             PG8_LDB(B0, 1, 0); PG8_LDB(B1, 1, 1); PG8_SCHED; PG8_LDA(At, 1, 0); PG8_STAGE(PG8_SA(0, 1), a2, vA2[1]);
;             PG8_WAIT_V(8); PG8_WAIT_L(0); PG8_BAR; PG8_MMA(0, 0, At, B0); PG8_MMA(0, 1, At, B1); PG8_BAR; PG8_SCHED;
.Lh1e_26630:
.Lh1_911:
	ds_read_b128 v[18:21], v191
	ds_read_b128 v[22:25], v191 offset:1024
	ds_read_b128 v[26:29], v191 offset:2048
	ds_read_b128 v[30:33], v191 offset:3072
	ds_read_b128 v[2:5], v192
	ds_read_b128 v[6:9], v192 offset:1024
	ds_read_b128 v[10:13], v192 offset:2048
	ds_read_b128 v[14:17], v192 offset:3072
	s_add_u32 s30, s28, 0x8000
	s_addc_u32 s31, s29, 0
	s_cmp_eq_u32 s65, 12
	s_cselect_b32 s42, s22, s30
	s_cselect_b32 s43, s23, s31
	s_cselect_b32 s40, s24, s19
	s_cselect_b32 s41, s25, s21
	s_add_u32 s30, s42, 0x8000
	s_addc_u32 s31, s43, 0
	v_lshl_add_u64 v[228:229], s[28:29], 0, v[182:183]
	s_add_i32 m0, s27, 0xc000
	ds_read_b128 v[196:199], v193
	ds_read_b128 v[200:203], v193 offset:1024
	ds_read_b128 v[204:207], v193 offset:2048
	ds_read_b128 v[208:211], v193 offset:3072
	ds_read_b128 v[212:215], v193 offset:4096
	ds_read_b128 v[216:219], v193 offset:5120
	ds_read_b128 v[220:223], v193 offset:6144
	ds_read_b128 v[224:227], v193 offset:7168
	global_load_lds_dwordx4 v[228:229], off
	v_lshl_add_u64 v[228:229], s[28:29], 0, v[180:181]
	s_add_i32 m0, s27, 0xe000
	s_nop 0
	global_load_lds_dwordx4 v[228:229], off
	s_waitcnt vmcnt(8)
	s_waitcnt lgkmcnt(0)
	s_barrier
	s_setprio 2
	v_mfma_f32_16x16x128_f8f6f4 v[158:161], v[18:25], v[196:203], v[158:161]
	v_mfma_f32_16x16x128_f8f6f4 v[154:157], v[26:33], v[196:203], v[154:157]
	v_mfma_f32_16x16x128_f8f6f4 v[150:153], v[18:25], v[204:211], v[150:153]
	v_mfma_f32_16x16x128_f8f6f4 v[146:149], v[26:33], v[204:211], v[146:149]
	v_mfma_f32_16x16x128_f8f6f4 v[130:133], v[18:25], v[212:219], v[130:133]
	v_mfma_f32_16x16x128_f8f6f4 v[122:125], v[26:33], v[212:219], v[122:125]
	v_mfma_f32_16x16x128_f8f6f4 v[114:117], v[18:25], v[220:227], v[114:117]
	v_mfma_f32_16x16x128_f8f6f4 v[106:109], v[26:33], v[220:227], v[106:109]
	s_nop 3
	s_setprio 0
	s_setprio 2
	v_mfma_f32_16x16x128_f8f6f4 v[142:145], v[2:9], v[196:203], v[142:145]
	v_mfma_f32_16x16x128_f8f6f4 v[138:141], v[10:17], v[196:203], v[138:141]
	v_mfma_f32_16x16x128_f8f6f4 v[134:137], v[2:9], v[204:211], v[134:137]
	v_mfma_f32_16x16x128_f8f6f4 v[126:129], v[10:17], v[204:211], v[126:129]
	v_mfma_f32_16x16x128_f8f6f4 v[118:121], v[2:9], v[212:219], v[118:121]
	v_mfma_f32_16x16x128_f8f6f4 v[110:113], v[10:17], v[212:219], v[110:113]
	v_mfma_f32_16x16x128_f8f6f4 v[102:105], v[2:9], v[220:227], v[102:105]
	v_mfma_f32_16x16x128_f8f6f4 v[98:101], v[10:17], v[220:227], v[98:101]
	s_setprio 0
	s_add_i32 s66, s60, s48
	v_lshl_add_u64 v[228:229], s[40:41], 0, v[162:163]
	s_mov_b32 m0, s66
	ds_read_b128 v[196:199], v193 offset:16384
	ds_read_b128 v[200:203], v193 offset:17408
	ds_read_b128 v[204:207], v193 offset:18432
	ds_read_b128 v[208:211], v193 offset:19456
	ds_read_b128 v[212:215], v193 offset:20480
	ds_read_b128 v[216:219], v193 offset:21504
	ds_read_b128 v[220:223], v193 offset:22528
	ds_read_b128 v[224:227], v193 offset:23552
	global_load_lds_dwordx4 v[228:229], off
	v_lshl_add_u64 v[230:231], s[40:41], 0, v[164:165]
	s_add_i32 m0, s66, 0x2000
	s_add_i32 s66, s61, s48
	global_load_lds_dwordx4 v[230:231], off
	v_lshl_add_u64 v[228:229], v[228:229], 0, s[6:7]
	s_mov_b32 m0, s66
	s_nop 0
	global_load_lds_dwordx4 v[228:229], off
	v_lshl_add_u64 v[228:229], v[230:231], 0, s[6:7]
	s_add_i32 m0, s66, 0x2000
	s_nop 0
	global_load_lds_dwordx4 v[228:229], off
	v_lshl_add_u64 v[228:229], s[42:43], 0, v[166:167]
	s_mov_b32 m0, s27
	s_nop 0
	global_load_lds_dwordx4 v[228:229], off
	v_lshl_add_u64 v[228:229], s[42:43], 0, v[168:169]
	s_mov_b32 m0, s49
	s_nop 0
	global_load_lds_dwordx4 v[228:229], off
	s_waitcnt vmcnt(8)
	s_waitcnt lgkmcnt(0)
	s_barrier
	s_setprio 2
	v_mfma_f32_16x16x128_f8f6f4 v[94:97], v[18:25], v[196:203], v[94:97]
	v_mfma_f32_16x16x128_f8f6f4 v[90:93], v[26:33], v[196:203], v[90:93]
	v_mfma_f32_16x16x128_f8f6f4 v[82:85], v[18:25], v[204:211], v[82:85]
	v_mfma_f32_16x16x128_f8f6f4 v[74:77], v[26:33], v[204:211], v[74:77]
	v_mfma_f32_16x16x128_f8f6f4 v[66:69], v[18:25], v[212:219], v[66:69]
	v_mfma_f32_16x16x128_f8f6f4 v[58:61], v[26:33], v[212:219], v[58:61]
	v_mfma_f32_16x16x128_f8f6f4 v[50:53], v[18:25], v[220:227], v[50:53]
	v_mfma_f32_16x16x128_f8f6f4 v[42:45], v[26:33], v[220:227], v[42:45]
	s_nop 3
	s_setprio 0
	s_setprio 2
	v_mfma_f32_16x16x128_f8f6f4 v[86:89], v[2:9], v[196:203], v[86:89]
	v_mfma_f32_16x16x128_f8f6f4 v[78:81], v[10:17], v[196:203], v[78:81]
	v_mfma_f32_16x16x128_f8f6f4 v[70:73], v[2:9], v[204:211], v[70:73]
	v_mfma_f32_16x16x128_f8f6f4 v[62:65], v[10:17], v[204:211], v[62:65]
	v_mfma_f32_16x16x128_f8f6f4 v[54:57], v[2:9], v[212:219], v[54:57]
	v_mfma_f32_16x16x128_f8f6f4 v[46:49], v[10:17], v[212:219], v[46:49]
	v_mfma_f32_16x16x128_f8f6f4 v[38:41], v[2:9], v[220:227], v[38:41]
	v_mfma_f32_16x16x128_f8f6f4 v[34:37], v[10:17], v[220:227], v[34:37]
	s_setprio 0
	s_add_i32 s66, 0, 0x18000
	s_add_i32 s67, 0, 0x1c000
	v_add_u32_e32 v14, s66, v189
	v_add_u32_e32 v30, s67, v189
	ds_read_b128 v[2:5], v14
	ds_read_b128 v[6:9], v14 offset:1024
	ds_read_b128 v[10:13], v14 offset:2048
	ds_read_b128 v[14:17], v14 offset:3072
	ds_read_b128 v[18:21], v30
	ds_read_b128 v[22:25], v30 offset:1024
	ds_read_b128 v[26:29], v30 offset:2048
	ds_read_b128 v[30:33], v30 offset:3072
	s_mov_b32 m0, s50
	v_lshl_add_u64 v[228:229], s[42:43], 0, v[172:173]
	ds_read_b128 v[196:199], v193 offset:32768
	ds_read_b128 v[200:203], v193 offset:33792
	ds_read_b128 v[204:207], v193 offset:34816
	ds_read_b128 v[208:211], v193 offset:35840
	ds_read_b128 v[212:215], v193 offset:36864
	ds_read_b128 v[216:219], v193 offset:37888
	ds_read_b128 v[220:223], v193 offset:38912
	ds_read_b128 v[224:227], v193 offset:39936
	global_load_lds_dwordx4 v[228:229], off
	v_lshl_add_u64 v[228:229], s[42:43], 0, v[174:175]
	s_mov_b32 m0, s51
	s_nop 0
	global_load_lds_dwordx4 v[228:229], off
	s_waitcnt vmcnt(8)
	s_waitcnt lgkmcnt(0)
	s_barrier
; #define PG8_STAGE(bufoff, gbase, voff) do { _Pragma("unroll") for (int _i = 0; _i < 2; ++_i) \
;         __builtin_amdgcn_global_load_lds((const unsigned*)((const char*)(gbase) + (voff)[_i]), (PG8_LAS unsigned*)(lds + (bufoff) + ldsw + _i * 8192), 16, 0, 0); } while (0)
; #define PG8_WAIT_V(n) asm volatile("s_waitcnt vmcnt(" #n ")" ::: "memory")
; #define PG8_WAIT_L(n) asm volatile("s_waitcnt lgkmcnt(" #n ")" ::: "memory")
; #define PG8_BAR __builtin_amdgcn_s_barrier()
; #define PG8_SCHED __builtin_amdgcn_sched_barrier(0)
; template <class Epi, class Sched, bool ALIGN_EPI = true, bool F8 = false>
; __device__ __forceinline__ void gemm_phase(PG8_LAS unsigned char* lds, const Sched& S, const Epi& E) {
;     ...
;             PG8_WAIT_V(8); PG8_WAIT_L(0); PG8_BAR; PG8_MMA(0, 0, At, B0); PG8_MMA(0, 1, At, B1); PG8_BAR; PG8_SCHED;
;             PG8_LDA(At, 1, 1); PG8_STAGE(PG8_SB(1, 0), b3, voffB[0]); PG8_STAGE(PG8_SB(1, 1), b3, voffB[1]); PG8_STAGE(PG8_SA(1, 0), a3, vA2[0]);
;             PG8_WAIT_V(8); PG8_WAIT_L(0); PG8_BAR; PG8_MMA(1, 0, At, B0); PG8_MMA(1, 1, At, B1); PG8_BAR; PG8_SCHED;
	s_setprio 2
	v_mfma_f32_16x16x128_f8f6f4 v[158:161], v[2:9], v[196:203], v[158:161]
	v_mfma_f32_16x16x128_f8f6f4 v[154:157], v[10:17], v[196:203], v[154:157]
	v_mfma_f32_16x16x128_f8f6f4 v[150:153], v[2:9], v[204:211], v[150:153]
	v_mfma_f32_16x16x128_f8f6f4 v[146:149], v[10:17], v[204:211], v[146:149]
	v_mfma_f32_16x16x128_f8f6f4 v[130:133], v[2:9], v[212:219], v[130:133]
	v_mfma_f32_16x16x128_f8f6f4 v[122:125], v[10:17], v[212:219], v[122:125]
	v_mfma_f32_16x16x128_f8f6f4 v[114:117], v[2:9], v[220:227], v[114:117]
	v_mfma_f32_16x16x128_f8f6f4 v[106:109], v[10:17], v[220:227], v[106:109]
	s_nop 3
	s_setprio 0
	s_setprio 2
	v_mfma_f32_16x16x128_f8f6f4 v[142:145], v[18:25], v[196:203], v[142:145]
	v_mfma_f32_16x16x128_f8f6f4 v[138:141], v[26:33], v[196:203], v[138:141]
	v_mfma_f32_16x16x128_f8f6f4 v[134:137], v[18:25], v[204:211], v[134:137]
	v_mfma_f32_16x16x128_f8f6f4 v[126:129], v[26:33], v[204:211], v[126:129]
	v_mfma_f32_16x16x128_f8f6f4 v[118:121], v[18:25], v[212:219], v[118:121]
	v_mfma_f32_16x16x128_f8f6f4 v[110:113], v[26:33], v[212:219], v[110:113]
	v_mfma_f32_16x16x128_f8f6f4 v[102:105], v[18:25], v[220:227], v[102:105]
	v_mfma_f32_16x16x128_f8f6f4 v[98:101], v[26:33], v[220:227], v[98:101]
	s_setprio 0
	s_add_u32 s40, s40, 0x8000
	s_addc_u32 s41, s41, 0
	s_add_i32 s42, s66, s48
	v_lshl_add_u64 v[228:229], s[40:41], 0, v[162:163]
	s_mov_b32 m0, s42
	ds_read_b128 v[196:199], v193 offset:49152
	ds_read_b128 v[200:203], v193 offset:50176
	ds_read_b128 v[204:207], v193 offset:51200
	ds_read_b128 v[208:211], v193 offset:52224
	ds_read_b128 v[212:215], v193 offset:53248
	ds_read_b128 v[216:219], v193 offset:54272
	ds_read_b128 v[220:223], v193 offset:55296
	ds_read_b128 v[224:227], v193 offset:56320
	global_load_lds_dwordx4 v[228:229], off
	v_lshl_add_u64 v[228:229], s[40:41], 0, v[164:165]
	s_add_i32 m0, s42, 0x2000
	s_add_i32 s42, s67, s48
	global_load_lds_dwordx4 v[228:229], off
	v_lshl_add_u64 v[228:229], s[40:41], 0, v[176:177]
	s_mov_b32 m0, s42
	s_nop 0
	global_load_lds_dwordx4 v[228:229], off
	v_lshl_add_u64 v[228:229], s[40:41], 0, v[178:179]
	s_add_i32 m0, s42, 0x2000
	s_nop 0
	global_load_lds_dwordx4 v[228:229], off
	v_lshl_add_u64 v[228:229], s[30:31], 0, v[166:167]
	s_mov_b32 m0, s53
	s_nop 0
	global_load_lds_dwordx4 v[228:229], off
	v_lshl_add_u64 v[228:229], s[30:31], 0, v[168:169]
	s_mov_b32 m0, s58
	s_nop 0
	global_load_lds_dwordx4 v[228:229], off
	s_waitcnt vmcnt(8)
	s_waitcnt lgkmcnt(0)
	s_barrier
	s_setprio 2
	v_mfma_f32_16x16x128_f8f6f4 v[94:97], v[2:9], v[196:203], v[94:97]
	v_mfma_f32_16x16x128_f8f6f4 v[90:93], v[10:17], v[196:203], v[90:93]
	v_mfma_f32_16x16x128_f8f6f4 v[82:85], v[2:9], v[204:211], v[82:85]
	v_mfma_f32_16x16x128_f8f6f4 v[74:77], v[10:17], v[204:211], v[74:77]
	v_mfma_f32_16x16x128_f8f6f4 v[66:69], v[2:9], v[212:219], v[66:69]
	v_mfma_f32_16x16x128_f8f6f4 v[58:61], v[10:17], v[212:219], v[58:61]
	v_mfma_f32_16x16x128_f8f6f4 v[50:53], v[2:9], v[220:227], v[50:53]
	v_mfma_f32_16x16x128_f8f6f4 v[42:45], v[10:17], v[220:227], v[42:45]
	s_nop 3
	s_setprio 0
	s_setprio 2
	v_mfma_f32_16x16x128_f8f6f4 v[86:89], v[18:25], v[196:203], v[86:89]
	v_mfma_f32_16x16x128_f8f6f4 v[78:81], v[26:33], v[196:203], v[78:81]
	v_mfma_f32_16x16x128_f8f6f4 v[70:73], v[18:25], v[204:211], v[70:73]
	v_mfma_f32_16x16x128_f8f6f4 v[62:65], v[26:33], v[204:211], v[62:65]
	v_mfma_f32_16x16x128_f8f6f4 v[54:57], v[18:25], v[212:219], v[54:57]
	v_mfma_f32_16x16x128_f8f6f4 v[46:49], v[26:33], v[212:219], v[46:49]
	v_mfma_f32_16x16x128_f8f6f4 v[38:41], v[18:25], v[220:227], v[38:41]
	v_mfma_f32_16x16x128_f8f6f4 v[34:37], v[26:33], v[220:227], v[34:37]
	s_setprio 0
	s_add_i32 s65, s65, 2
	s_add_u32 s19, s19, 0x10000
	s_addc_u32 s21, s21, 0
	s_add_u32 s28, s28, 0x10000
	s_addc_u32 s29, s29, 0
	s_cmp_gt_u32 s65, 13
	s_cbranch_scc0 .Lh1_911

; #define PG8_STAGE(bufoff, gbase, voff) do { _Pragma("unroll") for (int _i = 0; _i < 2; ++_i) \
;         __builtin_amdgcn_global_load_lds((const unsigned*)((const char*)(gbase) + (voff)[_i]), (PG8_LAS unsigned*)(lds + (bufoff) + ldsw + _i * 8192), 16, 0, 0); } while (0)
; #define PG8_WAIT_V(n) asm volatile("s_waitcnt vmcnt(" #n ")" ::: "memory")
; #define PG8_WAIT_L(n) asm volatile("s_waitcnt lgkmcnt(" #n ")" ::: "memory")
; #define PG8_BAR __builtin_amdgcn_s_barrier()
; #define PG8_SCHED __builtin_amdgcn_sched_barrier(0)
; template <class Epi, class Sched, bool ALIGN_EPI = true, bool F8 = false>
; __device__ __forceinline__ void gemm_phase(PG8_LAS unsigned char* lds, const Sched& S, const Epi& E) {
;     ...
;             if constexpr (Sched::GATHER) { if (last && has_next) S.a_off(nxt, Rs, Cs, voffAn); }
;             const char* a1 = cA + (size_t)(t + 1) * kstep;
;             const char* a2 = last ? nA : cA + (size_t)(t + 2) * kstep; const char* b2 = last ? nB : cB + (size_t)(t + 2) * kstepB;
;             const char* a3 = a2 + kstep; const char* b3 = b2 + kstepB;
;             unsigned vA2[2][2];
; #pragma unroll
;             for (int h = 0; h < 2; ++h)
; #pragma unroll
;                 for (int i = 0; i < 2; ++i) { if constexpr (Sched::GATHER) vA2[h][i] = (last && has_next) ? voffAn[h][i] : voffA[h][i]; else vA2[h][i] = voffA[h][i]; }
;             PG8_LDB(B0, 0, 0); PG8_LDB(B1, 0, 1); PG8_SCHED; PG8_LDA(At, 0, 0); PG8_STAGE(PG8_SA(1, 1), a1, voffA[1]);
;             PG8_WAIT_V(8); PG8_WAIT_L(0); PG8_BAR; PG8_MMA(0, 0, At, B0); PG8_MMA(0, 1, At, B1); PG8_BAR; PG8_SCHED;
;             PG8_LDA(At, 0, 1); PG8_STAGE(PG8_SB(0, 0), b2, voffB[0]); PG8_STAGE(PG8_SB(0, 1), b2, voffB[1]); PG8_STAGE(PG8_SA(0, 0), a2, vA2[0]);
;             PG8_WAIT_V(8); PG8_WAIT_L(0); PG8_BAR; PG8_MMA(1, 0, At, B0); PG8_MMA(1, 1, At, B1); PG8_BAR; PG8_SCHED;
;     __device__ __forceinline__ void a_off(const GUnit& u, const int (&R)[2], const int (&C)[2], unsigned (&v)[2][2]) const {
;         const int* rl = rowlist + (size_t)u.x0 * ECAP; const int base = u.x1 * 256, cm = u.x3 - 1;
; #pragma unroll
;         for (int h = 0; h < 2; ++h)
; #pragma unroll
;             for (int i = 0; i < 2; ++i) { int p = base + h * 128 + R[i]; p = p < cm ? p : cm; const unsigned ent = (unsigned)rl[p]; v[h][i] = (ent >> SHIFT) * (unsigned)PA + (unsigned)C[i] * 2u; } }
.LBB0_1060:
	v_add_u32_e32 v2, s12, v210
	v_add_u32_e32 v14, s62, v210
	s_add_u32 s28, s30, 0x100
	ds_read_b128 v[18:21], v2
	ds_read_b128 v[22:25], v2 offset:1024
	ds_read_b128 v[26:29], v2 offset:2048
	ds_read_b128 v[30:33], v2 offset:3072
	ds_read_b128 v[2:5], v14
	ds_read_b128 v[6:9], v14 offset:1024
	ds_read_b128 v[10:13], v14 offset:2048
	ds_read_b128 v[14:17], v14 offset:3072
	s_addc_u32 s29, s31, 0
	s_and_b64 s[42:43], s[40:41], exec
	s_cselect_b32 s42, 0, s28
	s_cselect_b32 s43, 0, s29
	s_add_u32 s42, s6, s42
	s_addc_u32 s43, s7, s43
	s_and_b64 s[40:41], s[40:41], exec
	s_cselect_b32 s41, s25, s68
	s_cselect_b32 s40, s24, s21
	v_lshl_add_u64 v[204:205], v[196:197], 0, s[30:31]
	s_add_i32 m0, s52, 0xc000
	ds_read_b128 v[222:225], v213
	ds_read_b128 v[226:229], v213 offset:1024
	ds_read_b128 v[230:233], v213 offset:2048
	ds_read_b128 v[234:237], v213 offset:3072
	ds_read_b128 v[238:241], v213 offset:4096
	ds_read_b128 v[242:245], v213 offset:5120
	ds_read_b128 v[246:249], v213 offset:6144
	ds_read_b128 v[250:253], v213 offset:7168
	global_load_lds_dwordx4 v[204:205], off
	v_lshl_add_u64 v[204:205], v[194:195], 0, s[30:31]
	s_add_i32 m0, s52, 0xe000
	s_nop 0
	global_load_lds_dwordx4 v[204:205], off
	s_waitcnt vmcnt(8)
	s_waitcnt lgkmcnt(0)
	s_setprio 1
	v_mfma_f32_16x16x128_f8f6f4 v[142:145], v[18:25], v[222:229], v[142:145]
	v_mfma_f32_16x16x128_f8f6f4 v[138:141], v[26:33], v[222:229], v[138:141]
	v_mfma_f32_16x16x128_f8f6f4 v[134:137], v[18:25], v[230:237], v[134:137]
	v_mfma_f32_16x16x128_f8f6f4 v[130:133], v[26:33], v[230:237], v[130:133]
	v_mfma_f32_16x16x128_f8f6f4 v[126:129], v[18:25], v[238:245], v[126:129]
	v_mfma_f32_16x16x128_f8f6f4 v[122:125], v[26:33], v[238:245], v[122:125]
	v_mfma_f32_16x16x128_f8f6f4 v[118:121], v[18:25], v[246:253], v[118:121]
	v_mfma_f32_16x16x128_f8f6f4 v[114:117], v[26:33], v[246:253], v[114:117]
	s_nop 3
	s_setprio 0
	s_setprio 1
	v_mfma_f32_16x16x128_f8f6f4 v[110:113], v[2:9], v[222:229], v[110:113]
	v_mfma_f32_16x16x128_f8f6f4 v[106:109], v[10:17], v[222:229], v[106:109]
	v_mfma_f32_16x16x128_f8f6f4 v[102:105], v[2:9], v[230:237], v[102:105]
	v_mfma_f32_16x16x128_f8f6f4 v[98:101], v[10:17], v[230:237], v[98:101]
	v_mfma_f32_16x16x128_f8f6f4 v[94:97], v[2:9], v[238:245], v[94:97]
	v_mfma_f32_16x16x128_f8f6f4 v[90:93], v[10:17], v[238:245], v[90:93]
	v_mfma_f32_16x16x128_f8f6f4 v[86:89], v[2:9], v[246:253], v[86:89]
	v_mfma_f32_16x16x128_f8f6f4 v[82:85], v[10:17], v[246:253], v[82:85]
	s_setprio 0
	s_barrier
	s_add_i32 s30, s12, s48
	v_lshl_add_u64 v[204:205], s[40:41], 0, v[162:163]
	s_mov_b32 m0, s30
	ds_read_b128 v[222:225], v213 offset:16384
	ds_read_b128 v[226:229], v213 offset:17408
	ds_read_b128 v[230:233], v213 offset:18432
	ds_read_b128 v[234:237], v213 offset:19456
	ds_read_b128 v[238:241], v213 offset:20480
	ds_read_b128 v[242:245], v213 offset:21504
	ds_read_b128 v[246:249], v213 offset:22528
	ds_read_b128 v[250:253], v213 offset:23552
	global_load_lds_dwordx4 v[204:205], off
	v_lshl_add_u64 v[204:205], s[40:41], 0, v[164:165]
	s_add_i32 m0, s30, 0x2000
	s_add_i32 s30, s62, s48
	global_load_lds_dwordx4 v[204:205], off
	v_lshl_add_u64 v[204:205], s[40:41], 0, v[166:167]
	s_mov_b32 m0, s30
	v_mov_b32_e32 v203, v171
	global_load_lds_dwordx4 v[204:205], off
	v_lshl_add_u64 v[204:205], s[40:41], 0, v[168:169]
	s_add_i32 m0, s30, 0x2000
	s_nop 0
	global_load_lds_dwordx4 v[204:205], off
	s_mov_b32 m0, s52
	v_lshl_add_u64 v[204:205], s[42:43], 0, v[170:171]
	global_load_lds_dwordx4 v170, s[42:43]
	s_mov_b32 m0, s53
	s_nop 0
	global_load_lds_dwordx4 v202, s[42:43]
	s_waitcnt vmcnt(8)
	s_waitcnt lgkmcnt(0)
	v_lshl_add_u64 v[202:203], s[42:43], 0, v[202:203]
	s_setprio 1
	v_mfma_f32_16x16x128_f8f6f4 v[78:81], v[18:25], v[222:229], v[78:81]
	v_mfma_f32_16x16x128_f8f6f4 v[74:77], v[26:33], v[222:229], v[74:77]
	v_mfma_f32_16x16x128_f8f6f4 v[70:73], v[18:25], v[230:237], v[70:73]
	v_mfma_f32_16x16x128_f8f6f4 v[66:69], v[26:33], v[230:237], v[66:69]
	v_mfma_f32_16x16x128_f8f6f4 v[62:65], v[18:25], v[238:245], v[62:65]
	v_mfma_f32_16x16x128_f8f6f4 v[58:61], v[26:33], v[238:245], v[58:61]
	v_mfma_f32_16x16x128_f8f6f4 v[54:57], v[18:25], v[246:253], v[54:57]
	v_mfma_f32_16x16x128_f8f6f4 v[50:53], v[26:33], v[246:253], v[50:53]
	s_nop 3
	s_setprio 0
	s_setprio 1
	v_mfma_f32_16x16x128_f8f6f4 v[46:49], v[2:9], v[222:229], v[46:49]
	v_mfma_f32_16x16x128_f8f6f4 v[42:45], v[10:17], v[222:229], v[42:45]
	v_mfma_f32_16x16x128_f8f6f4 v[38:41], v[2:9], v[230:237], v[38:41]
	v_mfma_f32_16x16x128_f8f6f4 v[34:37], v[10:17], v[230:237], v[34:37]
	v_mfma_f32_16x16x128_f8f6f4 v[146:149], v[2:9], v[238:245], v[146:149]
	v_mfma_f32_16x16x128_f8f6f4 v[150:153], v[10:17], v[238:245], v[150:153]
	v_mfma_f32_16x16x128_f8f6f4 v[154:157], v[2:9], v[246:253], v[154:157]
	v_mfma_f32_16x16x128_f8f6f4 v[158:161], v[10:17], v[246:253], v[158:161]
	s_setprio 0
	s_barrier
; #define PG8_STAGE(bufoff, gbase, voff) do { _Pragma("unroll") for (int _i = 0; _i < 2; ++_i) \
;         __builtin_amdgcn_global_load_lds((const unsigned*)((const char*)(gbase) + (voff)[_i]), (PG8_LAS unsigned*)(lds + (bufoff) + ldsw + _i * 8192), 16, 0, 0); } while (0)
; #define PG8_WAIT_V(n) asm volatile("s_waitcnt vmcnt(" #n ")" ::: "memory")
; #define PG8_WAIT_L(n) asm volatile("s_waitcnt lgkmcnt(" #n ")" ::: "memory")
; #define PG8_BAR __builtin_amdgcn_s_barrier()
; #define PG8_SCHED __builtin_amdgcn_sched_barrier(0)
; template <class Epi, class Sched, bool ALIGN_EPI = true, bool F8 = false>
; __device__ __forceinline__ void gemm_phase(PG8_LAS unsigned char* lds, const Sched& S, const Epi& E) {
;     ...
;             PG8_LDB(B0, 1, 0); PG8_LDB(B1, 1, 1); PG8_SCHED; PG8_LDA(At, 1, 0); PG8_STAGE(PG8_SA(0, 1), a2, vA2[1]);
;             PG8_WAIT_V(8); PG8_WAIT_L(0); PG8_BAR; PG8_MMA(0, 0, At, B0); PG8_MMA(0, 1, At, B1); PG8_BAR; PG8_SCHED;
;             PG8_LDA(At, 1, 1); PG8_STAGE(PG8_SB(1, 0), b3, voffB[0]); PG8_STAGE(PG8_SB(1, 1), b3, voffB[1]); PG8_STAGE(PG8_SA(1, 0), a3, vA2[0]);
;             PG8_WAIT_V(8); PG8_WAIT_L(0); PG8_BAR; PG8_MMA(1, 0, At, B0); PG8_MMA(1, 1, At, B1); PG8_BAR; PG8_SCHED;
	s_add_i32 s70, 0, 0x18000
	s_add_i32 s71, 0, 0x1c000
	v_add_u32_e32 v14, s70, v210
	v_add_u32_e32 v30, s71, v210
	ds_read_b128 v[2:5], v14
	ds_read_b128 v[6:9], v14 offset:1024
	ds_read_b128 v[10:13], v14 offset:2048
	ds_read_b128 v[14:17], v14 offset:3072
	ds_read_b128 v[18:21], v30
	ds_read_b128 v[22:25], v30 offset:1024
	ds_read_b128 v[26:29], v30 offset:2048
	ds_read_b128 v[30:33], v30 offset:3072
	s_mov_b32 m0, s58
	v_lshl_add_u64 v[200:201], s[42:43], 0, v[200:201]
	ds_read_b128 v[222:225], v213 offset:32768
	ds_read_b128 v[226:229], v213 offset:33792
	ds_read_b128 v[230:233], v213 offset:34816
	ds_read_b128 v[234:237], v213 offset:35840
	ds_read_b128 v[238:241], v213 offset:36864
	ds_read_b128 v[242:245], v213 offset:37888
	ds_read_b128 v[246:249], v213 offset:38912
	ds_read_b128 v[250:253], v213 offset:39936
	global_load_lds_dwordx4 v[200:201], off
	v_lshl_add_u64 v[198:199], s[42:43], 0, v[198:199]
	s_mov_b32 m0, s59
	s_nop 0
	global_load_lds_dwordx4 v[198:199], off
	s_waitcnt vmcnt(8)
	s_waitcnt lgkmcnt(0)
	s_setprio 1
	v_mfma_f32_16x16x128_f8f6f4 v[142:145], v[2:9], v[222:229], v[142:145]
	v_mfma_f32_16x16x128_f8f6f4 v[138:141], v[10:17], v[222:229], v[138:141]
	v_mfma_f32_16x16x128_f8f6f4 v[134:137], v[2:9], v[230:237], v[134:137]
	v_mfma_f32_16x16x128_f8f6f4 v[130:133], v[10:17], v[230:237], v[130:133]
	v_mfma_f32_16x16x128_f8f6f4 v[126:129], v[2:9], v[238:245], v[126:129]
	v_mfma_f32_16x16x128_f8f6f4 v[122:125], v[10:17], v[238:245], v[122:125]
	v_mfma_f32_16x16x128_f8f6f4 v[118:121], v[2:9], v[246:253], v[118:121]
	v_mfma_f32_16x16x128_f8f6f4 v[114:117], v[10:17], v[246:253], v[114:117]
	s_nop 3
	s_setprio 0
	s_setprio 1
	v_mfma_f32_16x16x128_f8f6f4 v[110:113], v[18:25], v[222:229], v[110:113]
	v_mfma_f32_16x16x128_f8f6f4 v[106:109], v[26:33], v[222:229], v[106:109]
	v_mfma_f32_16x16x128_f8f6f4 v[102:105], v[18:25], v[230:237], v[102:105]
	v_mfma_f32_16x16x128_f8f6f4 v[98:101], v[26:33], v[230:237], v[98:101]
	v_mfma_f32_16x16x128_f8f6f4 v[94:97], v[18:25], v[238:245], v[94:97]
	v_mfma_f32_16x16x128_f8f6f4 v[90:93], v[26:33], v[238:245], v[90:93]
	v_mfma_f32_16x16x128_f8f6f4 v[86:89], v[18:25], v[246:253], v[86:89]
	v_mfma_f32_16x16x128_f8f6f4 v[82:85], v[26:33], v[246:253], v[82:85]
	s_setprio 0
	s_barrier
	s_add_u32 s30, s40, 0x8000
	s_addc_u32 s31, s41, 0
	s_add_i32 s40, s70, s48
	v_lshl_add_u64 v[198:199], s[30:31], 0, v[162:163]
	s_mov_b32 m0, s40
	ds_read_b128 v[222:225], v213 offset:49152
	ds_read_b128 v[226:229], v213 offset:50176
	ds_read_b128 v[230:233], v213 offset:51200
	ds_read_b128 v[234:237], v213 offset:52224
	ds_read_b128 v[238:241], v213 offset:53248
	ds_read_b128 v[242:245], v213 offset:54272
	ds_read_b128 v[246:249], v213 offset:55296
	ds_read_b128 v[250:253], v213 offset:56320
	global_load_lds_dwordx4 v[198:199], off
	v_lshl_add_u64 v[198:199], s[30:31], 0, v[164:165]
	s_add_i32 m0, s40, 0x2000
	s_add_i32 s40, s71, s48
	global_load_lds_dwordx4 v[198:199], off
	v_lshl_add_u64 v[198:199], s[30:31], 0, v[166:167]
	s_mov_b32 m0, s40
	s_nop 0
	global_load_lds_dwordx4 v[198:199], off
	v_lshl_add_u64 v[198:199], s[30:31], 0, v[168:169]
	s_add_i32 m0, s40, 0x2000
	s_nop 0
	global_load_lds_dwordx4 v[198:199], off
	v_lshl_add_u64 v[198:199], v[204:205], 0, s[18:19]
	s_mov_b32 m0, s60
	s_nop 0
	global_load_lds_dwordx4 v[198:199], off
	v_lshl_add_u64 v[198:199], v[202:203], 0, s[18:19]
	s_mov_b32 m0, s61
	s_nop 0
	global_load_lds_dwordx4 v[198:199], off
	s_waitcnt vmcnt(8)
	s_waitcnt lgkmcnt(0)
	s_setprio 1
	v_mfma_f32_16x16x128_f8f6f4 v[78:81], v[2:9], v[222:229], v[78:81]
	v_mfma_f32_16x16x128_f8f6f4 v[74:77], v[10:17], v[222:229], v[74:77]
	v_mfma_f32_16x16x128_f8f6f4 v[70:73], v[2:9], v[230:237], v[70:73]
	v_mfma_f32_16x16x128_f8f6f4 v[66:69], v[10:17], v[230:237], v[66:69]
	v_mfma_f32_16x16x128_f8f6f4 v[62:65], v[2:9], v[238:245], v[62:65]
	v_mfma_f32_16x16x128_f8f6f4 v[58:61], v[10:17], v[238:245], v[58:61]
	v_mfma_f32_16x16x128_f8f6f4 v[54:57], v[2:9], v[246:253], v[54:57]
	v_mfma_f32_16x16x128_f8f6f4 v[50:53], v[10:17], v[246:253], v[50:53]
	s_nop 3
	s_setprio 0
	s_setprio 1
	v_mfma_f32_16x16x128_f8f6f4 v[46:49], v[18:25], v[222:229], v[46:49]
	v_mfma_f32_16x16x128_f8f6f4 v[42:45], v[26:33], v[222:229], v[42:45]
	v_mfma_f32_16x16x128_f8f6f4 v[38:41], v[18:25], v[230:237], v[38:41]
	v_mfma_f32_16x16x128_f8f6f4 v[34:37], v[26:33], v[230:237], v[34:37]
	v_mfma_f32_16x16x128_f8f6f4 v[146:149], v[18:25], v[238:245], v[146:149]
	v_mfma_f32_16x16x128_f8f6f4 v[150:153], v[26:33], v[238:245], v[150:153]
	v_mfma_f32_16x16x128_f8f6f4 v[154:157], v[18:25], v[246:253], v[154:157]
	v_mfma_f32_16x16x128_f8f6f4 v[158:161], v[26:33], v[246:253], v[158:161]
	s_setprio 0
	s_barrier
	s_add_i32 s69, s69, 2
	s_add_u32 s21, s21, 0x10000
	s_addc_u32 s68, s68, 0
	s_cmp_gt_u32 s69, 13
	s_cbranch_scc1 .LBB0_1062
	s_mov_b64 s[30:31], s[28:29]
	s_branch .LBB0_1058

; #define PG8_STAGE(bufoff, gbase, voff) do { _Pragma("unroll") for (int _i = 0; _i < 2; ++_i) \
;         __builtin_amdgcn_global_load_lds((const unsigned*)((const char*)(gbase) + (voff)[_i]), (PG8_LAS unsigned*)(lds + (bufoff) + ldsw + _i * 8192), 16, 0, 0); } while (0)
; #define PG8_WAIT_V(n) asm volatile("s_waitcnt vmcnt(" #n ")" ::: "memory")
; #define PG8_WAIT_L(n) asm volatile("s_waitcnt lgkmcnt(" #n ")" ::: "memory")
; #define PG8_BAR __builtin_amdgcn_s_barrier()
; #define PG8_SCHED __builtin_amdgcn_sched_barrier(0)
; template <class Epi, class Sched, bool ALIGN_EPI = true, bool F8 = false>
; __device__ __forceinline__ void gemm_phase(PG8_LAS unsigned char* lds, const Sched& S, const Epi& E) {
;     ...
;             if constexpr (Sched::GATHER) { if (last && has_next) S.a_off(nxt, Rs, Cs, voffAn); }
;             const char* a1 = cA + (size_t)(t + 1) * kstep;
;             const char* a2 = last ? nA : cA + (size_t)(t + 2) * kstep; const char* b2 = last ? nB : cB + (size_t)(t + 2) * kstepB;
;             const char* a3 = a2 + kstep; const char* b3 = b2 + kstepB;
;             unsigned vA2[2][2];
; #pragma unroll
;             for (int h = 0; h < 2; ++h)
; #pragma unroll
;                 for (int i = 0; i < 2; ++i) { if constexpr (Sched::GATHER) vA2[h][i] = (last && has_next) ? voffAn[h][i] : voffA[h][i]; else vA2[h][i] = voffA[h][i]; }
;             PG8_LDB(B0, 0, 0); PG8_LDB(B1, 0, 1); PG8_SCHED; PG8_LDA(At, 0, 0); PG8_STAGE(PG8_SA(1, 1), a1, voffA[1]);
;             PG8_WAIT_V(8); PG8_WAIT_L(0); PG8_BAR; PG8_MMA(0, 0, At, B0); PG8_MMA(0, 1, At, B1); PG8_BAR; PG8_SCHED;
;             PG8_LDA(At, 0, 1); PG8_STAGE(PG8_SB(0, 0), b2, voffB[0]); PG8_STAGE(PG8_SB(0, 1), b2, voffB[1]); PG8_STAGE(PG8_SA(0, 0), a2, vA2[0]);
;             PG8_WAIT_V(8); PG8_WAIT_L(0); PG8_BAR; PG8_MMA(1, 0, At, B0); PG8_MMA(1, 1, At, B1); PG8_BAR; PG8_SCHED;
;             PG8_LDB(B0, 1, 0); PG8_LDB(B1, 1, 1); PG8_SCHED; PG8_LDA(At, 1, 0); PG8_STAGE(PG8_SA(0, 1), a2, vA2[1]);
;             PG8_WAIT_V(8); PG8_WAIT_L(0); PG8_BAR; PG8_MMA(0, 0, At, B0); PG8_MMA(0, 1, At, B1); PG8_BAR; PG8_SCHED;
.Lh1_1060:
	v_add_u32_e32 v2, s12, v210
	v_add_u32_e32 v14, s62, v210
	s_add_u32 s28, s30, 0x100
	ds_read_b128 v[18:21], v2
	ds_read_b128 v[22:25], v2 offset:1024
	ds_read_b128 v[26:29], v2 offset:2048
	ds_read_b128 v[30:33], v2 offset:3072
	ds_read_b128 v[2:5], v14
	ds_read_b128 v[6:9], v14 offset:1024
	ds_read_b128 v[10:13], v14 offset:2048
	ds_read_b128 v[14:17], v14 offset:3072
	s_addc_u32 s29, s31, 0
	s_and_b64 s[42:43], s[40:41], exec
	s_cselect_b32 s42, 0, s28
	s_cselect_b32 s43, 0, s29
	s_add_u32 s42, s6, s42
	s_addc_u32 s43, s7, s43
	s_and_b64 s[40:41], s[40:41], exec
	s_cselect_b32 s41, s25, s68
	s_cselect_b32 s40, s24, s21
	v_lshl_add_u64 v[204:205], v[196:197], 0, s[30:31]
	s_add_i32 m0, s52, 0xc000
	ds_read_b128 v[222:225], v213
	ds_read_b128 v[226:229], v213 offset:1024
	ds_read_b128 v[230:233], v213 offset:2048
	ds_read_b128 v[234:237], v213 offset:3072
	ds_read_b128 v[238:241], v213 offset:4096
	ds_read_b128 v[242:245], v213 offset:5120
	ds_read_b128 v[246:249], v213 offset:6144
	ds_read_b128 v[250:253], v213 offset:7168
	global_load_lds_dwordx4 v[204:205], off
	v_lshl_add_u64 v[204:205], v[194:195], 0, s[30:31]
	s_add_i32 m0, s52, 0xe000
	s_nop 0
	global_load_lds_dwordx4 v[204:205], off
	s_waitcnt vmcnt(8)
	s_waitcnt lgkmcnt(0)
	s_barrier
	s_setprio 2
	v_mfma_f32_16x16x128_f8f6f4 v[142:145], v[18:25], v[222:229], v[142:145]
	v_mfma_f32_16x16x128_f8f6f4 v[138:141], v[26:33], v[222:229], v[138:141]
	v_mfma_f32_16x16x128_f8f6f4 v[134:137], v[18:25], v[230:237], v[134:137]
	v_mfma_f32_16x16x128_f8f6f4 v[130:133], v[26:33], v[230:237], v[130:133]
	v_mfma_f32_16x16x128_f8f6f4 v[126:129], v[18:25], v[238:245], v[126:129]
	v_mfma_f32_16x16x128_f8f6f4 v[122:125], v[26:33], v[238:245], v[122:125]
	v_mfma_f32_16x16x128_f8f6f4 v[118:121], v[18:25], v[246:253], v[118:121]
	v_mfma_f32_16x16x128_f8f6f4 v[114:117], v[26:33], v[246:253], v[114:117]
	s_nop 3
	s_setprio 0
	s_setprio 2
	v_mfma_f32_16x16x128_f8f6f4 v[110:113], v[2:9], v[222:229], v[110:113]
	v_mfma_f32_16x16x128_f8f6f4 v[106:109], v[10:17], v[222:229], v[106:109]
	v_mfma_f32_16x16x128_f8f6f4 v[102:105], v[2:9], v[230:237], v[102:105]
	v_mfma_f32_16x16x128_f8f6f4 v[98:101], v[10:17], v[230:237], v[98:101]
	v_mfma_f32_16x16x128_f8f6f4 v[94:97], v[2:9], v[238:245], v[94:97]
	v_mfma_f32_16x16x128_f8f6f4 v[90:93], v[10:17], v[238:245], v[90:93]
	v_mfma_f32_16x16x128_f8f6f4 v[86:89], v[2:9], v[246:253], v[86:89]
	v_mfma_f32_16x16x128_f8f6f4 v[82:85], v[10:17], v[246:253], v[82:85]
	s_setprio 0
	s_add_i32 s30, s12, s48
	v_lshl_add_u64 v[204:205], s[40:41], 0, v[162:163]
	s_mov_b32 m0, s30
	ds_read_b128 v[222:225], v213 offset:16384
	ds_read_b128 v[226:229], v213 offset:17408
	ds_read_b128 v[230:233], v213 offset:18432
	ds_read_b128 v[234:237], v213 offset:19456
	ds_read_b128 v[238:241], v213 offset:20480
	ds_read_b128 v[242:245], v213 offset:21504
	ds_read_b128 v[246:249], v213 offset:22528
	ds_read_b128 v[250:253], v213 offset:23552
	global_load_lds_dwordx4 v[204:205], off
	v_lshl_add_u64 v[204:205], s[40:41], 0, v[164:165]
	s_add_i32 m0, s30, 0x2000
	s_add_i32 s30, s62, s48
	global_load_lds_dwordx4 v[204:205], off
	v_lshl_add_u64 v[204:205], s[40:41], 0, v[166:167]
	s_mov_b32 m0, s30
	v_mov_b32_e32 v203, v171
	global_load_lds_dwordx4 v[204:205], off
	v_lshl_add_u64 v[204:205], s[40:41], 0, v[168:169]
	s_add_i32 m0, s30, 0x2000
	s_nop 0
	global_load_lds_dwordx4 v[204:205], off
	s_mov_b32 m0, s52
	v_lshl_add_u64 v[204:205], s[42:43], 0, v[170:171]
	global_load_lds_dwordx4 v170, s[42:43]
	s_mov_b32 m0, s53
	s_nop 0
	global_load_lds_dwordx4 v202, s[42:43]
	s_waitcnt vmcnt(8)
	s_waitcnt lgkmcnt(0)
	v_lshl_add_u64 v[202:203], s[42:43], 0, v[202:203]
	s_barrier
	s_setprio 2
	v_mfma_f32_16x16x128_f8f6f4 v[78:81], v[18:25], v[222:229], v[78:81]
	v_mfma_f32_16x16x128_f8f6f4 v[74:77], v[26:33], v[222:229], v[74:77]
	v_mfma_f32_16x16x128_f8f6f4 v[70:73], v[18:25], v[230:237], v[70:73]
	v_mfma_f32_16x16x128_f8f6f4 v[66:69], v[26:33], v[230:237], v[66:69]
	v_mfma_f32_16x16x128_f8f6f4 v[62:65], v[18:25], v[238:245], v[62:65]
	v_mfma_f32_16x16x128_f8f6f4 v[58:61], v[26:33], v[238:245], v[58:61]
	v_mfma_f32_16x16x128_f8f6f4 v[54:57], v[18:25], v[246:253], v[54:57]
	v_mfma_f32_16x16x128_f8f6f4 v[50:53], v[26:33], v[246:253], v[50:53]
	s_nop 3
	s_setprio 0
	s_setprio 2
	v_mfma_f32_16x16x128_f8f6f4 v[46:49], v[2:9], v[222:229], v[46:49]
	v_mfma_f32_16x16x128_f8f6f4 v[42:45], v[10:17], v[222:229], v[42:45]
	v_mfma_f32_16x16x128_f8f6f4 v[38:41], v[2:9], v[230:237], v[38:41]
	v_mfma_f32_16x16x128_f8f6f4 v[34:37], v[10:17], v[230:237], v[34:37]
	v_mfma_f32_16x16x128_f8f6f4 v[146:149], v[2:9], v[238:245], v[146:149]
	v_mfma_f32_16x16x128_f8f6f4 v[150:153], v[10:17], v[238:245], v[150:153]
	v_mfma_f32_16x16x128_f8f6f4 v[154:157], v[2:9], v[246:253], v[154:157]
	v_mfma_f32_16x16x128_f8f6f4 v[158:161], v[10:17], v[246:253], v[158:161]
	s_setprio 0
	s_add_i32 s70, 0, 0x18000
	s_add_i32 s71, 0, 0x1c000
	v_add_u32_e32 v14, s70, v210
	v_add_u32_e32 v30, s71, v210
	ds_read_b128 v[2:5], v14
	ds_read_b128 v[6:9], v14 offset:1024
	ds_read_b128 v[10:13], v14 offset:2048
	ds_read_b128 v[14:17], v14 offset:3072
	ds_read_b128 v[18:21], v30
	ds_read_b128 v[22:25], v30 offset:1024
	ds_read_b128 v[26:29], v30 offset:2048
	ds_read_b128 v[30:33], v30 offset:3072
	s_mov_b32 m0, s58
	v_lshl_add_u64 v[200:201], s[42:43], 0, v[200:201]
	ds_read_b128 v[222:225], v213 offset:32768
	ds_read_b128 v[226:229], v213 offset:33792
	ds_read_b128 v[230:233], v213 offset:34816
	ds_read_b128 v[234:237], v213 offset:35840
	ds_read_b128 v[238:241], v213 offset:36864
	ds_read_b128 v[242:245], v213 offset:37888
	ds_read_b128 v[246:249], v213 offset:38912
	ds_read_b128 v[250:253], v213 offset:39936
	global_load_lds_dwordx4 v[200:201], off
	v_lshl_add_u64 v[198:199], s[42:43], 0, v[198:199]
	s_mov_b32 m0, s59
	s_nop 0
	global_load_lds_dwordx4 v[198:199], off
	s_waitcnt vmcnt(8)
	s_waitcnt lgkmcnt(0)
	s_barrier
; #define PG8_STAGE(bufoff, gbase, voff) do { _Pragma("unroll") for (int _i = 0; _i < 2; ++_i) \
;         __builtin_amdgcn_global_load_lds((const unsigned*)((const char*)(gbase) + (voff)[_i]), (PG8_LAS unsigned*)(lds + (bufoff) + ldsw + _i * 8192), 16, 0, 0); } while (0)
; #define PG8_WAIT_V(n) asm volatile("s_waitcnt vmcnt(" #n ")" ::: "memory")
; #define PG8_WAIT_L(n) asm volatile("s_waitcnt lgkmcnt(" #n ")" ::: "memory")
; #define PG8_BAR __builtin_amdgcn_s_barrier()
; #define PG8_SCHED __builtin_amdgcn_sched_barrier(0)
; template <class Epi, class Sched, bool ALIGN_EPI = true, bool F8 = false>
; __device__ __forceinline__ void gemm_phase(PG8_LAS unsigned char* lds, const Sched& S, const Epi& E) {
;     ...
;             PG8_WAIT_V(8); PG8_WAIT_L(0); PG8_BAR; PG8_MMA(0, 0, At, B0); PG8_MMA(0, 1, At, B1); PG8_BAR; PG8_SCHED;
;             PG8_LDA(At, 1, 1); PG8_STAGE(PG8_SB(1, 0), b3, voffB[0]); PG8_STAGE(PG8_SB(1, 1), b3, voffB[1]); PG8_STAGE(PG8_SA(1, 0), a3, vA2[0]);
;             PG8_WAIT_V(8); PG8_WAIT_L(0); PG8_BAR; PG8_MMA(1, 0, At, B0); PG8_MMA(1, 1, At, B1); PG8_BAR; PG8_SCHED;
	s_setprio 2
	v_mfma_f32_16x16x128_f8f6f4 v[142:145], v[2:9], v[222:229], v[142:145]
	v_mfma_f32_16x16x128_f8f6f4 v[138:141], v[10:17], v[222:229], v[138:141]
	v_mfma_f32_16x16x128_f8f6f4 v[134:137], v[2:9], v[230:237], v[134:137]
	v_mfma_f32_16x16x128_f8f6f4 v[130:133], v[10:17], v[230:237], v[130:133]
	v_mfma_f32_16x16x128_f8f6f4 v[126:129], v[2:9], v[238:245], v[126:129]
	v_mfma_f32_16x16x128_f8f6f4 v[122:125], v[10:17], v[238:245], v[122:125]
	v_mfma_f32_16x16x128_f8f6f4 v[118:121], v[2:9], v[246:253], v[118:121]
	v_mfma_f32_16x16x128_f8f6f4 v[114:117], v[10:17], v[246:253], v[114:117]
	s_nop 3
	s_setprio 0
	s_setprio 2
	v_mfma_f32_16x16x128_f8f6f4 v[110:113], v[18:25], v[222:229], v[110:113]
	v_mfma_f32_16x16x128_f8f6f4 v[106:109], v[26:33], v[222:229], v[106:109]
	v_mfma_f32_16x16x128_f8f6f4 v[102:105], v[18:25], v[230:237], v[102:105]
	v_mfma_f32_16x16x128_f8f6f4 v[98:101], v[26:33], v[230:237], v[98:101]
	v_mfma_f32_16x16x128_f8f6f4 v[94:97], v[18:25], v[238:245], v[94:97]
	v_mfma_f32_16x16x128_f8f6f4 v[90:93], v[26:33], v[238:245], v[90:93]
	v_mfma_f32_16x16x128_f8f6f4 v[86:89], v[18:25], v[246:253], v[86:89]
	v_mfma_f32_16x16x128_f8f6f4 v[82:85], v[26:33], v[246:253], v[82:85]
	s_setprio 0
	s_add_u32 s30, s40, 0x8000
	s_addc_u32 s31, s41, 0
	s_add_i32 s40, s70, s48
	v_lshl_add_u64 v[198:199], s[30:31], 0, v[162:163]
	s_mov_b32 m0, s40
	ds_read_b128 v[222:225], v213 offset:49152
	ds_read_b128 v[226:229], v213 offset:50176
	ds_read_b128 v[230:233], v213 offset:51200
	ds_read_b128 v[234:237], v213 offset:52224
	ds_read_b128 v[238:241], v213 offset:53248
	ds_read_b128 v[242:245], v213 offset:54272
	ds_read_b128 v[246:249], v213 offset:55296
	ds_read_b128 v[250:253], v213 offset:56320
	global_load_lds_dwordx4 v[198:199], off
	v_lshl_add_u64 v[198:199], s[30:31], 0, v[164:165]
	s_add_i32 m0, s40, 0x2000
	s_add_i32 s40, s71, s48
	global_load_lds_dwordx4 v[198:199], off
	v_lshl_add_u64 v[198:199], s[30:31], 0, v[166:167]
	s_mov_b32 m0, s40
	s_nop 0
	global_load_lds_dwordx4 v[198:199], off
	v_lshl_add_u64 v[198:199], s[30:31], 0, v[168:169]
	s_add_i32 m0, s40, 0x2000
	s_nop 0
	global_load_lds_dwordx4 v[198:199], off
	v_lshl_add_u64 v[198:199], v[204:205], 0, s[18:19]
	s_mov_b32 m0, s60
	s_nop 0
	global_load_lds_dwordx4 v[198:199], off
	v_lshl_add_u64 v[198:199], v[202:203], 0, s[18:19]
	s_mov_b32 m0, s61
	s_nop 0
	global_load_lds_dwordx4 v[198:199], off
	s_waitcnt vmcnt(8)
	s_waitcnt lgkmcnt(0)
	s_barrier
	s_setprio 2
	v_mfma_f32_16x16x128_f8f6f4 v[78:81], v[2:9], v[222:229], v[78:81]
	v_mfma_f32_16x16x128_f8f6f4 v[74:77], v[10:17], v[222:229], v[74:77]
	v_mfma_f32_16x16x128_f8f6f4 v[70:73], v[2:9], v[230:237], v[70:73]
	v_mfma_f32_16x16x128_f8f6f4 v[66:69], v[10:17], v[230:237], v[66:69]
	v_mfma_f32_16x16x128_f8f6f4 v[62:65], v[2:9], v[238:245], v[62:65]
	v_mfma_f32_16x16x128_f8f6f4 v[58:61], v[10:17], v[238:245], v[58:61]
	v_mfma_f32_16x16x128_f8f6f4 v[54:57], v[2:9], v[246:253], v[54:57]
	v_mfma_f32_16x16x128_f8f6f4 v[50:53], v[10:17], v[246:253], v[50:53]
	s_nop 3
	s_setprio 0
	s_setprio 2
	v_mfma_f32_16x16x128_f8f6f4 v[46:49], v[18:25], v[222:229], v[46:49]
	v_mfma_f32_16x16x128_f8f6f4 v[42:45], v[26:33], v[222:229], v[42:45]
	v_mfma_f32_16x16x128_f8f6f4 v[38:41], v[18:25], v[230:237], v[38:41]
	v_mfma_f32_16x16x128_f8f6f4 v[34:37], v[26:33], v[230:237], v[34:37]
	v_mfma_f32_16x16x128_f8f6f4 v[146:149], v[18:25], v[238:245], v[146:149]
	v_mfma_f32_16x16x128_f8f6f4 v[150:153], v[26:33], v[238:245], v[150:153]
	v_mfma_f32_16x16x128_f8f6f4 v[154:157], v[18:25], v[246:253], v[154:157]
	v_mfma_f32_16x16x128_f8f6f4 v[158:161], v[26:33], v[246:253], v[158:161]
	s_setprio 0
	s_add_i32 s69, s69, 2
	s_add_u32 s21, s21, 0x10000
	s_addc_u32 s68, s68, 0
	s_cmp_gt_u32 s69, 13
	s_cbranch_scc1 .LBB0_1062
	s_mov_b64 s[30:31], s[28:29]
	s_branch .Lh1_1058

; #define PG8_STAGE(bufoff, gbase, voff) do { _Pragma("unroll") for (int _i = 0; _i < 2; ++_i) \
;         __builtin_amdgcn_global_load_lds((const unsigned*)((const char*)(gbase) + (voff)[_i]), (PG8_LAS unsigned*)(lds + (bufoff) + ldsw + _i * 8192), 16, 0, 0); } while (0)
; #define PG8_WAIT_V(n) asm volatile("s_waitcnt vmcnt(" #n ")" ::: "memory")
; #define PG8_WAIT_L(n) asm volatile("s_waitcnt lgkmcnt(" #n ")" ::: "memory")
; #define PG8_BAR __builtin_amdgcn_s_barrier()
; #define PG8_SCHED __builtin_amdgcn_sched_barrier(0)
; template <class Epi, class Sched, bool ALIGN_EPI = true, bool F8 = false>
; __device__ __forceinline__ void gemm_phase(PG8_LAS unsigned char* lds, const Sched& S, const Epi& E) {
;     ...
;             PG8_LDB(B0, 0, 0); PG8_LDB(B1, 0, 1); PG8_SCHED; PG8_LDA(At, 0, 0); PG8_STAGE(PG8_SA(1, 1), a1, voffA[1]);
;             PG8_WAIT_V(8); PG8_WAIT_L(0); PG8_BAR; PG8_MMA(0, 0, At, B0); PG8_MMA(0, 1, At, B1); PG8_BAR; PG8_SCHED;
;             PG8_LDA(At, 0, 1); PG8_STAGE(PG8_SB(0, 0), b2, voffB[0]); PG8_STAGE(PG8_SB(0, 1), b2, voffB[1]); PG8_STAGE(PG8_SA(0, 0), a2, vA2[0]);
;             PG8_WAIT_V(8); PG8_WAIT_L(0); PG8_BAR; PG8_MMA(1, 0, At, B0); PG8_MMA(1, 1, At, B1); PG8_BAR; PG8_SCHED;
.LBB0_1138:
	ds_read_b128 v[18:21], v189
	ds_read_b128 v[22:25], v189 offset:1024
	ds_read_b128 v[26:29], v189 offset:2048
	ds_read_b128 v[30:33], v189 offset:3072
	ds_read_b128 v[2:5], v190
	ds_read_b128 v[6:9], v190 offset:1024
	ds_read_b128 v[10:13], v190 offset:2048
	ds_read_b128 v[14:17], v190 offset:3072
	s_add_u32 s26, s24, 0x8000
	s_addc_u32 s27, s25, 0
	s_cmp_eq_u32 s68, 4
	s_cselect_b32 s30, s16, s26
	s_cselect_b32 s31, s17, s27
	s_cselect_b32 s28, s18, s23
	s_cselect_b32 s29, s19, s67
	s_add_u32 s26, s30, 0x8000
	s_addc_u32 s27, s31, 0
	v_lshl_add_u64 v[226:227], s[24:25], 0, v[184:185]
	s_add_i32 m0, s44, 0xc000
	ds_read_b128 v[194:197], v191
	ds_read_b128 v[198:201], v191 offset:1024
	ds_read_b128 v[202:205], v191 offset:2048
	ds_read_b128 v[206:209], v191 offset:3072
	ds_read_b128 v[210:213], v191 offset:4096
	ds_read_b128 v[214:217], v191 offset:5120
	ds_read_b128 v[218:221], v191 offset:6144
	ds_read_b128 v[222:225], v191 offset:7168
	global_load_lds_dwordx4 v[226:227], off
	v_lshl_add_u64 v[226:227], s[24:25], 0, v[182:183]
	s_add_i32 m0, s44, 0xe000
	s_nop 0
	global_load_lds_dwordx4 v[226:227], off
	s_waitcnt vmcnt(8)
	s_waitcnt lgkmcnt(0)
	s_setprio 1
	v_mfma_f32_16x16x128_f8f6f4 v[158:161], v[18:25], v[194:201], v[158:161]
	v_mfma_f32_16x16x128_f8f6f4 v[154:157], v[26:33], v[194:201], v[154:157]
	v_mfma_f32_16x16x128_f8f6f4 v[142:145], v[18:25], v[202:209], v[142:145]
	v_mfma_f32_16x16x128_f8f6f4 v[138:141], v[26:33], v[202:209], v[138:141]
	v_mfma_f32_16x16x128_f8f6f4 v[126:129], v[18:25], v[210:217], v[126:129]
	v_mfma_f32_16x16x128_f8f6f4 v[122:125], v[26:33], v[210:217], v[122:125]
	v_mfma_f32_16x16x128_f8f6f4 v[110:113], v[18:25], v[218:225], v[110:113]
	v_mfma_f32_16x16x128_f8f6f4 v[106:109], v[26:33], v[218:225], v[106:109]
	s_nop 3
	s_setprio 0
	s_setprio 1
	v_mfma_f32_16x16x128_f8f6f4 v[150:153], v[2:9], v[194:201], v[150:153]
	v_mfma_f32_16x16x128_f8f6f4 v[146:149], v[10:17], v[194:201], v[146:149]
	v_mfma_f32_16x16x128_f8f6f4 v[134:137], v[2:9], v[202:209], v[134:137]
	v_mfma_f32_16x16x128_f8f6f4 v[130:133], v[10:17], v[202:209], v[130:133]
	v_mfma_f32_16x16x128_f8f6f4 v[118:121], v[2:9], v[210:217], v[118:121]
	v_mfma_f32_16x16x128_f8f6f4 v[114:117], v[10:17], v[210:217], v[114:117]
	v_mfma_f32_16x16x128_f8f6f4 v[102:105], v[2:9], v[218:225], v[102:105]
	v_mfma_f32_16x16x128_f8f6f4 v[98:101], v[10:17], v[218:225], v[98:101]
	s_setprio 0
	s_barrier
	s_add_i32 s69, s53, s43
	v_lshl_add_u64 v[226:227], s[28:29], 0, v[164:165]
	s_mov_b32 m0, s69
	ds_read_b128 v[194:197], v191 offset:16384
	ds_read_b128 v[198:201], v191 offset:17408
	ds_read_b128 v[202:205], v191 offset:18432
	ds_read_b128 v[206:209], v191 offset:19456
	ds_read_b128 v[210:213], v191 offset:20480
	ds_read_b128 v[214:217], v191 offset:21504
	ds_read_b128 v[218:221], v191 offset:22528
	ds_read_b128 v[222:225], v191 offset:23552
	global_load_lds_dwordx4 v[226:227], off
	v_lshl_add_u64 v[228:229], s[28:29], 0, v[166:167]
	s_add_i32 m0, s69, 0x2000
	s_add_i32 s69, s58, s43
	global_load_lds_dwordx4 v[228:229], off
	v_lshl_add_u64 v[226:227], v[226:227], 0, s[4:5]
	s_mov_b32 m0, s69
	s_nop 0
	global_load_lds_dwordx4 v[226:227], off
	v_lshl_add_u64 v[226:227], v[228:229], 0, s[4:5]
	s_add_i32 m0, s69, 0x2000
	s_nop 0
	global_load_lds_dwordx4 v[226:227], off
	v_lshl_add_u64 v[226:227], s[30:31], 0, v[168:169]
	s_mov_b32 m0, s44
	s_nop 0
	global_load_lds_dwordx4 v[226:227], off
	v_lshl_add_u64 v[226:227], s[30:31], 0, v[170:171]
	s_mov_b32 m0, s45
	s_nop 0
	global_load_lds_dwordx4 v[226:227], off
	s_waitcnt vmcnt(8)
	s_waitcnt lgkmcnt(0)
	s_setprio 1
	v_mfma_f32_16x16x128_f8f6f4 v[94:97], v[18:25], v[194:201], v[94:97]
	v_mfma_f32_16x16x128_f8f6f4 v[90:93], v[26:33], v[194:201], v[90:93]
	v_mfma_f32_16x16x128_f8f6f4 v[78:81], v[18:25], v[202:209], v[78:81]
	v_mfma_f32_16x16x128_f8f6f4 v[74:77], v[26:33], v[202:209], v[74:77]
	v_mfma_f32_16x16x128_f8f6f4 v[62:65], v[18:25], v[210:217], v[62:65]
	v_mfma_f32_16x16x128_f8f6f4 v[58:61], v[26:33], v[210:217], v[58:61]
	v_mfma_f32_16x16x128_f8f6f4 v[46:49], v[18:25], v[218:225], v[46:49]
	v_mfma_f32_16x16x128_f8f6f4 v[42:45], v[26:33], v[218:225], v[42:45]
	s_nop 3
	s_setprio 0
	s_setprio 1
	v_mfma_f32_16x16x128_f8f6f4 v[86:89], v[2:9], v[194:201], v[86:89]
	v_mfma_f32_16x16x128_f8f6f4 v[82:85], v[10:17], v[194:201], v[82:85]
	v_mfma_f32_16x16x128_f8f6f4 v[70:73], v[2:9], v[202:209], v[70:73]
	v_mfma_f32_16x16x128_f8f6f4 v[66:69], v[10:17], v[202:209], v[66:69]
	v_mfma_f32_16x16x128_f8f6f4 v[54:57], v[2:9], v[210:217], v[54:57]
	v_mfma_f32_16x16x128_f8f6f4 v[50:53], v[10:17], v[210:217], v[50:53]
	v_mfma_f32_16x16x128_f8f6f4 v[38:41], v[2:9], v[218:225], v[38:41]
	v_mfma_f32_16x16x128_f8f6f4 v[34:37], v[10:17], v[218:225], v[34:37]
	s_setprio 0
	s_barrier
; #define PG8_STAGE(bufoff, gbase, voff) do { _Pragma("unroll") for (int _i = 0; _i < 2; ++_i) \
;         __builtin_amdgcn_global_load_lds((const unsigned*)((const char*)(gbase) + (voff)[_i]), (PG8_LAS unsigned*)(lds + (bufoff) + ldsw + _i * 8192), 16, 0, 0); } while (0)
; #define PG8_WAIT_V(n) asm volatile("s_waitcnt vmcnt(" #n ")" ::: "memory")
; #define PG8_WAIT_L(n) asm volatile("s_waitcnt lgkmcnt(" #n ")" ::: "memory")
; #define PG8_BAR __builtin_amdgcn_s_barrier()
; #define PG8_SCHED __builtin_amdgcn_sched_barrier(0)
; template <class Epi, class Sched, bool ALIGN_EPI = true, bool F8 = false>
; __device__ __forceinline__ void gemm_phase(PG8_LAS unsigned char* lds, const Sched& S, const Epi& E) {
;     ...
;             PG8_LDB(B0, 1, 0); PG8_LDB(B1, 1, 1); PG8_SCHED; PG8_LDA(At, 1, 0); PG8_STAGE(PG8_SA(0, 1), a2, vA2[1]);
;             PG8_WAIT_V(8); PG8_WAIT_L(0); PG8_BAR; PG8_MMA(0, 0, At, B0); PG8_MMA(0, 1, At, B1); PG8_BAR; PG8_SCHED;
;             PG8_LDA(At, 1, 1); PG8_STAGE(PG8_SB(1, 0), b3, voffB[0]); PG8_STAGE(PG8_SB(1, 1), b3, voffB[1]); PG8_STAGE(PG8_SA(1, 0), a3, vA2[0]);
;             PG8_WAIT_V(8); PG8_WAIT_L(0); PG8_BAR; PG8_MMA(1, 0, At, B0); PG8_MMA(1, 1, At, B1); PG8_BAR; PG8_SCHED;
	s_add_i32 s69, 0, 0x18000
	s_add_i32 s70, 0, 0x1c000
	v_add_u32_e32 v14, s69, v187
	v_add_u32_e32 v30, s70, v187
	ds_read_b128 v[2:5], v14
	ds_read_b128 v[6:9], v14 offset:1024
	ds_read_b128 v[10:13], v14 offset:2048
	ds_read_b128 v[14:17], v14 offset:3072
	ds_read_b128 v[18:21], v30
	ds_read_b128 v[22:25], v30 offset:1024
	ds_read_b128 v[26:29], v30 offset:2048
	ds_read_b128 v[30:33], v30 offset:3072
	s_mov_b32 m0, s46
	v_lshl_add_u64 v[226:227], s[30:31], 0, v[172:173]
	ds_read_b128 v[194:197], v191 offset:32768
	ds_read_b128 v[198:201], v191 offset:33792
	ds_read_b128 v[202:205], v191 offset:34816
	ds_read_b128 v[206:209], v191 offset:35840
	ds_read_b128 v[210:213], v191 offset:36864
	ds_read_b128 v[214:217], v191 offset:37888
	ds_read_b128 v[218:221], v191 offset:38912
	ds_read_b128 v[222:225], v191 offset:39936
	global_load_lds_dwordx4 v[226:227], off
	v_lshl_add_u64 v[226:227], s[30:31], 0, v[174:175]
	s_mov_b32 m0, s47
	s_nop 0
	global_load_lds_dwordx4 v[226:227], off
	s_waitcnt vmcnt(8)
	s_waitcnt lgkmcnt(0)
	s_setprio 1
	v_mfma_f32_16x16x128_f8f6f4 v[158:161], v[2:9], v[194:201], v[158:161]
	v_mfma_f32_16x16x128_f8f6f4 v[154:157], v[10:17], v[194:201], v[154:157]
	v_mfma_f32_16x16x128_f8f6f4 v[142:145], v[2:9], v[202:209], v[142:145]
	v_mfma_f32_16x16x128_f8f6f4 v[138:141], v[10:17], v[202:209], v[138:141]
	v_mfma_f32_16x16x128_f8f6f4 v[126:129], v[2:9], v[210:217], v[126:129]
	v_mfma_f32_16x16x128_f8f6f4 v[122:125], v[10:17], v[210:217], v[122:125]
	v_mfma_f32_16x16x128_f8f6f4 v[110:113], v[2:9], v[218:225], v[110:113]
	v_mfma_f32_16x16x128_f8f6f4 v[106:109], v[10:17], v[218:225], v[106:109]
	s_nop 3
	s_setprio 0
	s_setprio 1
	v_mfma_f32_16x16x128_f8f6f4 v[150:153], v[18:25], v[194:201], v[150:153]
	v_mfma_f32_16x16x128_f8f6f4 v[146:149], v[26:33], v[194:201], v[146:149]
	v_mfma_f32_16x16x128_f8f6f4 v[134:137], v[18:25], v[202:209], v[134:137]
	v_mfma_f32_16x16x128_f8f6f4 v[130:133], v[26:33], v[202:209], v[130:133]
	v_mfma_f32_16x16x128_f8f6f4 v[118:121], v[18:25], v[210:217], v[118:121]
	v_mfma_f32_16x16x128_f8f6f4 v[114:117], v[26:33], v[210:217], v[114:117]
	v_mfma_f32_16x16x128_f8f6f4 v[102:105], v[18:25], v[218:225], v[102:105]
	v_mfma_f32_16x16x128_f8f6f4 v[98:101], v[26:33], v[218:225], v[98:101]
	s_setprio 0
	s_barrier
	s_add_u32 s28, s28, 0x8000
	s_addc_u32 s29, s29, 0
	s_add_i32 s30, s69, s43
	v_lshl_add_u64 v[226:227], s[28:29], 0, v[164:165]
	s_mov_b32 m0, s30
	ds_read_b128 v[194:197], v191 offset:49152
	ds_read_b128 v[198:201], v191 offset:50176
	ds_read_b128 v[202:205], v191 offset:51200
	ds_read_b128 v[206:209], v191 offset:52224
	ds_read_b128 v[210:213], v191 offset:53248
	ds_read_b128 v[214:217], v191 offset:54272
	ds_read_b128 v[218:221], v191 offset:55296
	ds_read_b128 v[222:225], v191 offset:56320
	global_load_lds_dwordx4 v[226:227], off
	v_lshl_add_u64 v[226:227], s[28:29], 0, v[166:167]
	s_add_i32 m0, s30, 0x2000
	s_add_i32 s30, s70, s43
	global_load_lds_dwordx4 v[226:227], off
	v_lshl_add_u64 v[226:227], s[28:29], 0, v[178:179]
	s_mov_b32 m0, s30
	s_nop 0
	global_load_lds_dwordx4 v[226:227], off
	v_lshl_add_u64 v[226:227], s[28:29], 0, v[180:181]
	s_add_i32 m0, s30, 0x2000
	s_nop 0
	global_load_lds_dwordx4 v[226:227], off
	v_lshl_add_u64 v[226:227], s[26:27], 0, v[168:169]
	s_mov_b32 m0, s51
	s_nop 0
	global_load_lds_dwordx4 v[226:227], off
	v_lshl_add_u64 v[226:227], s[26:27], 0, v[170:171]
	s_mov_b32 m0, s52
	s_nop 0
	global_load_lds_dwordx4 v[226:227], off
	s_waitcnt vmcnt(8)
	s_waitcnt lgkmcnt(0)
	s_setprio 1
	v_mfma_f32_16x16x128_f8f6f4 v[94:97], v[2:9], v[194:201], v[94:97]
	v_mfma_f32_16x16x128_f8f6f4 v[90:93], v[10:17], v[194:201], v[90:93]
	v_mfma_f32_16x16x128_f8f6f4 v[78:81], v[2:9], v[202:209], v[78:81]
	v_mfma_f32_16x16x128_f8f6f4 v[74:77], v[10:17], v[202:209], v[74:77]
	v_mfma_f32_16x16x128_f8f6f4 v[62:65], v[2:9], v[210:217], v[62:65]
	v_mfma_f32_16x16x128_f8f6f4 v[58:61], v[10:17], v[210:217], v[58:61]
	v_mfma_f32_16x16x128_f8f6f4 v[46:49], v[2:9], v[218:225], v[46:49]
	v_mfma_f32_16x16x128_f8f6f4 v[42:45], v[10:17], v[218:225], v[42:45]
	s_nop 3
	s_setprio 0
	s_setprio 1
	v_mfma_f32_16x16x128_f8f6f4 v[86:89], v[18:25], v[194:201], v[86:89]
	v_mfma_f32_16x16x128_f8f6f4 v[82:85], v[26:33], v[194:201], v[82:85]
	v_mfma_f32_16x16x128_f8f6f4 v[70:73], v[18:25], v[202:209], v[70:73]
	v_mfma_f32_16x16x128_f8f6f4 v[66:69], v[26:33], v[202:209], v[66:69]
	v_mfma_f32_16x16x128_f8f6f4 v[54:57], v[18:25], v[210:217], v[54:57]
	v_mfma_f32_16x16x128_f8f6f4 v[50:53], v[26:33], v[210:217], v[50:53]
	v_mfma_f32_16x16x128_f8f6f4 v[38:41], v[18:25], v[218:225], v[38:41]
	v_mfma_f32_16x16x128_f8f6f4 v[34:37], v[26:33], v[218:225], v[34:37]
	s_setprio 0
	s_barrier
	s_add_i32 s68, s68, 2
	s_add_u32 s23, s23, 0x10000
	s_addc_u32 s67, s67, 0
	s_add_u32 s24, s24, 0x10000
	s_addc_u32 s25, s25, 0
	s_cmp_gt_u32 s68, 5
	s_cbranch_scc0 .LBB0_1138
	s_branch .Lfx_33571
; #define PG8_STAGE(bufoff, gbase, voff) do { _Pragma("unroll") for (int _i = 0; _i < 2; ++_i) \
;         __builtin_amdgcn_global_load_lds((const unsigned*)((const char*)(gbase) + (voff)[_i]), (PG8_LAS unsigned*)(lds + (bufoff) + ldsw + _i * 8192), 16, 0, 0); } while (0)
; #define PG8_WAIT_V(n) asm volatile("s_waitcnt vmcnt(" #n ")" ::: "memory")
; #define PG8_WAIT_L(n) asm volatile("s_waitcnt lgkmcnt(" #n ")" ::: "memory")
; #define PG8_BAR __builtin_amdgcn_s_barrier()
; #define PG8_SCHED __builtin_amdgcn_sched_barrier(0)
; template <class Epi, class Sched, bool ALIGN_EPI = true, bool F8 = false>
; __device__ __forceinline__ void gemm_phase(PG8_LAS unsigned char* lds, const Sched& S, const Epi& E) {
;     ...
;             PG8_LDB(B0, 0, 0); PG8_LDB(B1, 0, 1); PG8_SCHED; PG8_LDA(At, 0, 0); PG8_STAGE(PG8_SA(1, 1), a1, voffA[1]);
;             PG8_WAIT_V(8); PG8_WAIT_L(0); PG8_BAR; PG8_MMA(0, 0, At, B0); PG8_MMA(0, 1, At, B1); PG8_BAR; PG8_SCHED;
;             PG8_LDA(At, 0, 1); PG8_STAGE(PG8_SB(0, 0), b2, voffB[0]); PG8_STAGE(PG8_SB(0, 1), b2, voffB[1]); PG8_STAGE(PG8_SA(0, 0), a2, vA2[0]);
;             PG8_WAIT_V(8); PG8_WAIT_L(0); PG8_BAR; PG8_MMA(1, 0, At, B0); PG8_MMA(1, 1, At, B1); PG8_BAR; PG8_SCHED;
.Lh1e_33571:
.Lh1_1138:
	ds_read_b128 v[18:21], v189
	ds_read_b128 v[22:25], v189 offset:1024
	ds_read_b128 v[26:29], v189 offset:2048
	ds_read_b128 v[30:33], v189 offset:3072
	ds_read_b128 v[2:5], v190
	ds_read_b128 v[6:9], v190 offset:1024
	ds_read_b128 v[10:13], v190 offset:2048
	ds_read_b128 v[14:17], v190 offset:3072
	s_add_u32 s26, s24, 0x8000
	s_addc_u32 s27, s25, 0
	s_cmp_eq_u32 s68, 4
	s_cselect_b32 s30, s16, s26
	s_cselect_b32 s31, s17, s27
	s_cselect_b32 s28, s18, s23
	s_cselect_b32 s29, s19, s67
	s_add_u32 s26, s30, 0x8000
	s_addc_u32 s27, s31, 0
	v_lshl_add_u64 v[226:227], s[24:25], 0, v[184:185]
	s_add_i32 m0, s44, 0xc000
	ds_read_b128 v[194:197], v191
	ds_read_b128 v[198:201], v191 offset:1024
	ds_read_b128 v[202:205], v191 offset:2048
	ds_read_b128 v[206:209], v191 offset:3072
	ds_read_b128 v[210:213], v191 offset:4096
	ds_read_b128 v[214:217], v191 offset:5120
	ds_read_b128 v[218:221], v191 offset:6144
	ds_read_b128 v[222:225], v191 offset:7168
	global_load_lds_dwordx4 v[226:227], off
	v_lshl_add_u64 v[226:227], s[24:25], 0, v[182:183]
	s_add_i32 m0, s44, 0xe000
	s_nop 0
	global_load_lds_dwordx4 v[226:227], off
	s_waitcnt vmcnt(8)
	s_waitcnt lgkmcnt(0)
	s_barrier
	s_setprio 2
	v_mfma_f32_16x16x128_f8f6f4 v[158:161], v[18:25], v[194:201], v[158:161]
	v_mfma_f32_16x16x128_f8f6f4 v[154:157], v[26:33], v[194:201], v[154:157]
	v_mfma_f32_16x16x128_f8f6f4 v[142:145], v[18:25], v[202:209], v[142:145]
	v_mfma_f32_16x16x128_f8f6f4 v[138:141], v[26:33], v[202:209], v[138:141]
	v_mfma_f32_16x16x128_f8f6f4 v[126:129], v[18:25], v[210:217], v[126:129]
	v_mfma_f32_16x16x128_f8f6f4 v[122:125], v[26:33], v[210:217], v[122:125]
	v_mfma_f32_16x16x128_f8f6f4 v[110:113], v[18:25], v[218:225], v[110:113]
	v_mfma_f32_16x16x128_f8f6f4 v[106:109], v[26:33], v[218:225], v[106:109]
	s_nop 3
	s_setprio 0
	s_setprio 2
	v_mfma_f32_16x16x128_f8f6f4 v[150:153], v[2:9], v[194:201], v[150:153]
	v_mfma_f32_16x16x128_f8f6f4 v[146:149], v[10:17], v[194:201], v[146:149]
	v_mfma_f32_16x16x128_f8f6f4 v[134:137], v[2:9], v[202:209], v[134:137]
	v_mfma_f32_16x16x128_f8f6f4 v[130:133], v[10:17], v[202:209], v[130:133]
	v_mfma_f32_16x16x128_f8f6f4 v[118:121], v[2:9], v[210:217], v[118:121]
	v_mfma_f32_16x16x128_f8f6f4 v[114:117], v[10:17], v[210:217], v[114:117]
	v_mfma_f32_16x16x128_f8f6f4 v[102:105], v[2:9], v[218:225], v[102:105]
	v_mfma_f32_16x16x128_f8f6f4 v[98:101], v[10:17], v[218:225], v[98:101]
	s_setprio 0
	s_add_i32 s69, s53, s43
	v_lshl_add_u64 v[226:227], s[28:29], 0, v[164:165]
	s_mov_b32 m0, s69
	ds_read_b128 v[194:197], v191 offset:16384
	ds_read_b128 v[198:201], v191 offset:17408
	ds_read_b128 v[202:205], v191 offset:18432
	ds_read_b128 v[206:209], v191 offset:19456
	ds_read_b128 v[210:213], v191 offset:20480
	ds_read_b128 v[214:217], v191 offset:21504
	ds_read_b128 v[218:221], v191 offset:22528
	ds_read_b128 v[222:225], v191 offset:23552
	global_load_lds_dwordx4 v[226:227], off
	v_lshl_add_u64 v[228:229], s[28:29], 0, v[166:167]
	s_add_i32 m0, s69, 0x2000
	s_add_i32 s69, s58, s43
	global_load_lds_dwordx4 v[228:229], off
	v_lshl_add_u64 v[226:227], v[226:227], 0, s[4:5]
	s_mov_b32 m0, s69
	s_nop 0
	global_load_lds_dwordx4 v[226:227], off
	v_lshl_add_u64 v[226:227], v[228:229], 0, s[4:5]
	s_add_i32 m0, s69, 0x2000
	s_nop 0
	global_load_lds_dwordx4 v[226:227], off
	v_lshl_add_u64 v[226:227], s[30:31], 0, v[168:169]
	s_mov_b32 m0, s44
	s_nop 0
	global_load_lds_dwordx4 v[226:227], off
	v_lshl_add_u64 v[226:227], s[30:31], 0, v[170:171]
	s_mov_b32 m0, s45
	s_nop 0
	global_load_lds_dwordx4 v[226:227], off
	s_waitcnt vmcnt(8)
	s_waitcnt lgkmcnt(0)
	s_barrier
	s_setprio 2
	v_mfma_f32_16x16x128_f8f6f4 v[94:97], v[18:25], v[194:201], v[94:97]
	v_mfma_f32_16x16x128_f8f6f4 v[90:93], v[26:33], v[194:201], v[90:93]
	v_mfma_f32_16x16x128_f8f6f4 v[78:81], v[18:25], v[202:209], v[78:81]
	v_mfma_f32_16x16x128_f8f6f4 v[74:77], v[26:33], v[202:209], v[74:77]
	v_mfma_f32_16x16x128_f8f6f4 v[62:65], v[18:25], v[210:217], v[62:65]
	v_mfma_f32_16x16x128_f8f6f4 v[58:61], v[26:33], v[210:217], v[58:61]
	v_mfma_f32_16x16x128_f8f6f4 v[46:49], v[18:25], v[218:225], v[46:49]
	v_mfma_f32_16x16x128_f8f6f4 v[42:45], v[26:33], v[218:225], v[42:45]
	s_nop 3
	s_setprio 0
	s_setprio 2
	v_mfma_f32_16x16x128_f8f6f4 v[86:89], v[2:9], v[194:201], v[86:89]
	v_mfma_f32_16x16x128_f8f6f4 v[82:85], v[10:17], v[194:201], v[82:85]
	v_mfma_f32_16x16x128_f8f6f4 v[70:73], v[2:9], v[202:209], v[70:73]
	v_mfma_f32_16x16x128_f8f6f4 v[66:69], v[10:17], v[202:209], v[66:69]
	v_mfma_f32_16x16x128_f8f6f4 v[54:57], v[2:9], v[210:217], v[54:57]
	v_mfma_f32_16x16x128_f8f6f4 v[50:53], v[10:17], v[210:217], v[50:53]
	v_mfma_f32_16x16x128_f8f6f4 v[38:41], v[2:9], v[218:225], v[38:41]
	v_mfma_f32_16x16x128_f8f6f4 v[34:37], v[10:17], v[218:225], v[34:37]
	s_setprio 0
	s_add_i32 s69, 0, 0x18000
	s_add_i32 s70, 0, 0x1c000
	v_add_u32_e32 v14, s69, v187
	v_add_u32_e32 v30, s70, v187
	ds_read_b128 v[2:5], v14
	ds_read_b128 v[6:9], v14 offset:1024
	ds_read_b128 v[10:13], v14 offset:2048
	ds_read_b128 v[14:17], v14 offset:3072
	ds_read_b128 v[18:21], v30
	ds_read_b128 v[22:25], v30 offset:1024
	ds_read_b128 v[26:29], v30 offset:2048
	ds_read_b128 v[30:33], v30 offset:3072
	s_mov_b32 m0, s46
	v_lshl_add_u64 v[226:227], s[30:31], 0, v[172:173]
	ds_read_b128 v[194:197], v191 offset:32768
	ds_read_b128 v[198:201], v191 offset:33792
	ds_read_b128 v[202:205], v191 offset:34816
	ds_read_b128 v[206:209], v191 offset:35840
	ds_read_b128 v[210:213], v191 offset:36864
	ds_read_b128 v[214:217], v191 offset:37888
	ds_read_b128 v[218:221], v191 offset:38912
	ds_read_b128 v[222:225], v191 offset:39936
	global_load_lds_dwordx4 v[226:227], off
	v_lshl_add_u64 v[226:227], s[30:31], 0, v[174:175]
	s_mov_b32 m0, s47
	s_nop 0
	global_load_lds_dwordx4 v[226:227], off
	s_waitcnt vmcnt(8)
	s_waitcnt lgkmcnt(0)
	s_barrier
; #define PG8_STAGE(bufoff, gbase, voff) do { _Pragma("unroll") for (int _i = 0; _i < 2; ++_i) \
;         __builtin_amdgcn_global_load_lds((const unsigned*)((const char*)(gbase) + (voff)[_i]), (PG8_LAS unsigned*)(lds + (bufoff) + ldsw + _i * 8192), 16, 0, 0); } while (0)
; #define PG8_WAIT_V(n) asm volatile("s_waitcnt vmcnt(" #n ")" ::: "memory")
; #define PG8_WAIT_L(n) asm volatile("s_waitcnt lgkmcnt(" #n ")" ::: "memory")
; #define PG8_BAR __builtin_amdgcn_s_barrier()
; #define PG8_SCHED __builtin_amdgcn_sched_barrier(0)
; template <class Epi, class Sched, bool ALIGN_EPI = true, bool F8 = false>
; __device__ __forceinline__ void gemm_phase(PG8_LAS unsigned char* lds, const Sched& S, const Epi& E) {
;     ...
;         for (int t = 0; t < nt; t += 2) {
;     ...
;             PG8_LDB(B0, 1, 0); PG8_LDB(B1, 1, 1); PG8_SCHED; PG8_LDA(At, 1, 0); PG8_STAGE(PG8_SA(0, 1), a2, vA2[1]);
;             PG8_WAIT_V(8); PG8_WAIT_L(0); PG8_BAR; PG8_MMA(0, 0, At, B0); PG8_MMA(0, 1, At, B1); PG8_BAR; PG8_SCHED;
;             PG8_LDA(At, 1, 1); PG8_STAGE(PG8_SB(1, 0), b3, voffB[0]); PG8_STAGE(PG8_SB(1, 1), b3, voffB[1]); PG8_STAGE(PG8_SA(1, 0), a3, vA2[0]);
;             PG8_WAIT_V(8); PG8_WAIT_L(0); PG8_BAR; PG8_MMA(1, 0, At, B0); PG8_MMA(1, 1, At, B1); PG8_BAR; PG8_SCHED;
	s_setprio 2
	v_mfma_f32_16x16x128_f8f6f4 v[158:161], v[2:9], v[194:201], v[158:161]
	v_mfma_f32_16x16x128_f8f6f4 v[154:157], v[10:17], v[194:201], v[154:157]
	v_mfma_f32_16x16x128_f8f6f4 v[142:145], v[2:9], v[202:209], v[142:145]
	v_mfma_f32_16x16x128_f8f6f4 v[138:141], v[10:17], v[202:209], v[138:141]
	v_mfma_f32_16x16x128_f8f6f4 v[126:129], v[2:9], v[210:217], v[126:129]
	v_mfma_f32_16x16x128_f8f6f4 v[122:125], v[10:17], v[210:217], v[122:125]
	v_mfma_f32_16x16x128_f8f6f4 v[110:113], v[2:9], v[218:225], v[110:113]
	v_mfma_f32_16x16x128_f8f6f4 v[106:109], v[10:17], v[218:225], v[106:109]
	s_nop 3
	s_setprio 0
	s_setprio 2
	v_mfma_f32_16x16x128_f8f6f4 v[150:153], v[18:25], v[194:201], v[150:153]
	v_mfma_f32_16x16x128_f8f6f4 v[146:149], v[26:33], v[194:201], v[146:149]
	v_mfma_f32_16x16x128_f8f6f4 v[134:137], v[18:25], v[202:209], v[134:137]
	v_mfma_f32_16x16x128_f8f6f4 v[130:133], v[26:33], v[202:209], v[130:133]
	v_mfma_f32_16x16x128_f8f6f4 v[118:121], v[18:25], v[210:217], v[118:121]
	v_mfma_f32_16x16x128_f8f6f4 v[114:117], v[26:33], v[210:217], v[114:117]
	v_mfma_f32_16x16x128_f8f6f4 v[102:105], v[18:25], v[218:225], v[102:105]
	v_mfma_f32_16x16x128_f8f6f4 v[98:101], v[26:33], v[218:225], v[98:101]
	s_setprio 0
	s_add_u32 s28, s28, 0x8000
	s_addc_u32 s29, s29, 0
	s_add_i32 s30, s69, s43
	v_lshl_add_u64 v[226:227], s[28:29], 0, v[164:165]
	s_mov_b32 m0, s30
	ds_read_b128 v[194:197], v191 offset:49152
	ds_read_b128 v[198:201], v191 offset:50176
	ds_read_b128 v[202:205], v191 offset:51200
	ds_read_b128 v[206:209], v191 offset:52224
	ds_read_b128 v[210:213], v191 offset:53248
	ds_read_b128 v[214:217], v191 offset:54272
	ds_read_b128 v[218:221], v191 offset:55296
	ds_read_b128 v[222:225], v191 offset:56320
	global_load_lds_dwordx4 v[226:227], off
	v_lshl_add_u64 v[226:227], s[28:29], 0, v[166:167]
	s_add_i32 m0, s30, 0x2000
	s_add_i32 s30, s70, s43
	global_load_lds_dwordx4 v[226:227], off
	v_lshl_add_u64 v[226:227], s[28:29], 0, v[178:179]
	s_mov_b32 m0, s30
	s_nop 0
	global_load_lds_dwordx4 v[226:227], off
	v_lshl_add_u64 v[226:227], s[28:29], 0, v[180:181]
	s_add_i32 m0, s30, 0x2000
	s_nop 0
	global_load_lds_dwordx4 v[226:227], off
	v_lshl_add_u64 v[226:227], s[26:27], 0, v[168:169]
	s_mov_b32 m0, s51
	s_nop 0
	global_load_lds_dwordx4 v[226:227], off
	v_lshl_add_u64 v[226:227], s[26:27], 0, v[170:171]
	s_mov_b32 m0, s52
	s_nop 0
	global_load_lds_dwordx4 v[226:227], off
	s_waitcnt vmcnt(8)
	s_waitcnt lgkmcnt(0)
	s_barrier
	s_setprio 2
	v_mfma_f32_16x16x128_f8f6f4 v[94:97], v[2:9], v[194:201], v[94:97]
	v_mfma_f32_16x16x128_f8f6f4 v[90:93], v[10:17], v[194:201], v[90:93]
	v_mfma_f32_16x16x128_f8f6f4 v[78:81], v[2:9], v[202:209], v[78:81]
	v_mfma_f32_16x16x128_f8f6f4 v[74:77], v[10:17], v[202:209], v[74:77]
	v_mfma_f32_16x16x128_f8f6f4 v[62:65], v[2:9], v[210:217], v[62:65]
	v_mfma_f32_16x16x128_f8f6f4 v[58:61], v[10:17], v[210:217], v[58:61]
	v_mfma_f32_16x16x128_f8f6f4 v[46:49], v[2:9], v[218:225], v[46:49]
	v_mfma_f32_16x16x128_f8f6f4 v[42:45], v[10:17], v[218:225], v[42:45]
	s_nop 3
	s_setprio 0
	s_setprio 2
	v_mfma_f32_16x16x128_f8f6f4 v[86:89], v[18:25], v[194:201], v[86:89]
	v_mfma_f32_16x16x128_f8f6f4 v[82:85], v[26:33], v[194:201], v[82:85]
	v_mfma_f32_16x16x128_f8f6f4 v[70:73], v[18:25], v[202:209], v[70:73]
	v_mfma_f32_16x16x128_f8f6f4 v[66:69], v[26:33], v[202:209], v[66:69]
	v_mfma_f32_16x16x128_f8f6f4 v[54:57], v[18:25], v[210:217], v[54:57]
	v_mfma_f32_16x16x128_f8f6f4 v[50:53], v[26:33], v[210:217], v[50:53]
	v_mfma_f32_16x16x128_f8f6f4 v[38:41], v[18:25], v[218:225], v[38:41]
	v_mfma_f32_16x16x128_f8f6f4 v[34:37], v[26:33], v[218:225], v[34:37]
	s_setprio 0
	s_add_i32 s68, s68, 2
	s_add_u32 s23, s23, 0x10000
	s_addc_u32 s67, s67, 0
	s_add_u32 s24, s24, 0x10000
	s_addc_u32 s25, s25, 0
	s_cmp_gt_u32 s68, 5
	s_cbranch_scc0 .Lh1_1138
